# speedup vs baseline: 1.0268x; 1.0268x over previous
.LBB3_24:
	s_or_b64 exec, exec, s[2:3]
	v_lshrrev_b32_e32 v82, 3, v0
	v_lshlrev_b32_e32 v78, 3, v0
	s_movk_i32 s2, 0x70
	v_and_b32_e32 v83, 56, v78
	v_not_b32_e32 v78, v82
	v_bitop3_b32 v85, v191, s2, v0 bitop3:0x48
	s_mov_b64 s[2:3], 0x400000
	v_lshlrev_b32_e32 v78, 2, v78
	v_lshl_add_u64 v[182:183], v[74:75], 0, s[2:3]
	v_lshlrev_b32_e32 v74, 2, v83
	v_add3_u32 v74, s30, v78, v74
	v_sub_co_u32_e32 v78, vcc, v82, v83
	v_lshlrev_b32_e32 v122, 14, v239
	v_mov_b32_e32 v123, 0
	v_add_u32_e32 v75, 0x100, v74
	v_lshl_add_u32 v78, v78, 2, s30
	v_or_b32_e32 v86, 1, v83
	s_waitcnt lgkmcnt(0)
	v_lshl_add_u64 v[76:77], s[18:19], 0, v[122:123]
	v_mov_b32_e32 v179, v123
	v_cndmask_b32_e32 v227, v78, v75, vcc
	v_sub_u32_e32 v78, v82, v86
	v_lshl_add_u32 v78, v78, 2, s30
	v_add_u32_e32 v79, 0x104, v74
	v_cmp_lt_u32_e32 vcc, v83, v82
	v_lshl_add_u64 v[180:181], v[76:77], 0, v[178:179]
	v_or_b32_e32 v77, 2, v83
	v_cndmask_b32_e32 v228, v79, v78, vcc
	v_sub_co_u32_e32 v79, vcc, v82, v77
	s_add_i32 s18, 0, 0x10000
	v_add_u32_e32 v78, 0x108, v74
	v_lshl_add_u32 v79, v79, 2, s30
	v_or_b32_e32 v90, 3, v83
	s_add_u32 s2, s20, s50
	v_cndmask_b32_e32 v229, v79, v78, vcc
	v_sub_co_u32_e32 v78, vcc, v82, v90
	s_barrier
	s_addc_u32 s3, s21, s51
	v_lshl_add_u32 v91, v78, 2, s30
	global_load_dwordx4 v[78:81], v[180:181], off
	s_load_dword s34, s[2:3], 0x0
	ds_read_b32 v75, v227
	ds_read_b32 v87, v228
	ds_read_b32 v88, v229
	v_lshlrev_b32_e32 v138, 7, v188
	v_lshl_add_u32 v84, v82, 7, s18
	v_add_u32_e32 v130, s18, v138
	s_waitcnt lgkmcnt(0)
	v_add_f32_e32 v76, s34, v75
	v_cmp_eq_u32_e64 s[18:19], v83, v82
	v_add_u32_e32 v89, 0x10c, v74
	v_cmp_eq_u32_e64 s[20:21], v82, v86
	v_cndmask_b32_e64 v75, v75, v76, s[18:19]
	v_add_f32_e32 v76, s34, v87
	v_or_b32_e32 v93, 4, v83
	v_cndmask_b32_e32 v230, v91, v89, vcc
	v_cndmask_b32_e64 v76, v87, v76, s[20:21]
	v_add_f32_e32 v86, s34, v88
	v_cmp_eq_u32_e64 s[22:23], v77, v82
	v_sub_co_u32_e32 v87, vcc, v82, v93
	s_nop 0
	v_cndmask_b32_e64 v77, v88, v86, s[22:23]
	v_add_u32_e32 v86, 0x110, v74
	v_lshl_add_u32 v87, v87, 2, s30
	v_cndmask_b32_e32 v231, v87, v86, vcc
	global_load_dwordx4 v[86:89], v[180:181], off offset:16
	global_load_dwordx4 v[126:129], v[180:181], off offset:128
	global_load_dwordx4 v[132:135], v[180:181], off offset:144
	ds_read_b32 v91, v230
	ds_read_b32 v94, v231
	v_or_b32_e32 v95, 5, v83
	v_sub_co_u32_e32 v97, vcc, v82, v95
	s_waitcnt lgkmcnt(1)
	v_add_f32_e32 v92, s34, v91
	v_add_u32_e32 v96, 0x114, v74
	v_lshl_add_u32 v97, v97, 2, s30
	v_cmp_eq_u32_e64 s[24:25], v90, v82
	v_cmp_eq_u32_e64 s[26:27], v93, v82
	v_or_b32_e32 v93, 6, v83
	v_cndmask_b32_e32 v233, v97, v96, vcc
	v_cndmask_b32_e64 v90, v91, v92, s[24:25]
	s_waitcnt lgkmcnt(0)
	v_add_f32_e32 v91, s34, v94
	v_cmp_eq_u32_e64 s[28:29], v95, v82
	v_sub_co_u32_e32 v95, vcc, v82, v93
	v_cndmask_b32_e64 v91, v94, v91, s[26:27]
	v_add_u32_e32 v94, 0x118, v74
	v_lshl_add_u32 v95, v95, 2, s30
	v_or_b32_e32 v83, 7, v83
	v_cndmask_b32_e32 v234, v95, v94, vcc
	v_sub_co_u32_e32 v95, vcc, v82, v83
	v_add_u32_e32 v74, 0x11c, v74
	v_lshl_add_u32 v95, v95, 2, s30
	ds_read_b32 v94, v234
	v_cndmask_b32_e32 v235, v95, v74, vcc
	ds_read_b32 v96, v233
	ds_read_b32 v74, v235
	v_cmp_eq_u32_e64 s[30:31], v93, v82
	s_waitcnt lgkmcnt(2)
	v_add_f32_e32 v95, s34, v94
	v_cvt_pk_f16_f32 v141, v77, v90
	s_waitcnt lgkmcnt(1)
	v_add_f32_e32 v92, s34, v96
	v_cndmask_b32_e64 v93, v94, v95, s[30:31]
	s_waitcnt lgkmcnt(0)
	v_add_f32_e32 v94, s34, v74
	v_cmp_eq_u32_e64 s[34:35], v83, v82
	v_cndmask_b32_e64 v92, v96, v92, s[28:29]
	v_cvt_pk_f16_f32 v142, v91, v92
	v_cndmask_b32_e64 v74, v74, v94, s[34:35]
	v_cvt_pk_f16_f32 v143, v93, v74
	v_cvt_pk_f16_f32 v140, v75, v76
	v_add_u32_e32 v232, v84, v85
	global_load_dwordx4 v[144:147], v[180:181], off offset:256
	global_load_dwordx4 v[148:151], v[180:181], off offset:272
	global_load_dwordx4 v[94:97], v[180:181], off offset:384
	global_load_dwordx4 v[118:121], v[180:181], off offset:400
	global_load_dwordx4 v[102:105], v[180:181], off offset:512
	global_load_dwordx4 v[114:117], v[180:181], off offset:528
	global_load_dwordx4 v[110:113], v[180:181], off offset:640
	global_load_dwordx4 v[106:109], v[180:181], off offset:656
	global_load_dwordx4 v[98:101], v[180:181], off offset:768
	global_load_dwordx4 v[90:93], v[180:181], off offset:784
	global_load_dwordx4 v[82:85], v[180:181], off offset:896
	global_load_dwordx4 v[74:77], v[180:181], off offset:912
	s_add_u32 s40, s40, s50
	s_addc_u32 s41, s41, s51
	s_add_u32 s42, s42, s50
	s_addc_u32 s43, s43, s51
	ds_write_b128 v232, v[140:143]
	s_waitcnt lgkmcnt(0)
	s_barrier
	s_waitcnt vmcnt(15)
	v_cvt_f32_f16_e32 v125, v79
	v_cvt_f32_f16_e32 v124, v78
	v_cvt_f32_f16_sdwa v79, v79 dst_sel:DWORD dst_unused:UNUSED_PAD src0_sel:WORD_1
	v_cvt_f32_f16_sdwa v78, v78 dst_sel:DWORD dst_unused:UNUSED_PAD src0_sel:WORD_1
	s_load_dword s52, s[42:43], 0x0
	v_pk_add_f32 v[124:125], v[124:125], 1.0 op_sel_hi:[1,0]
	s_load_dword s50, s[40:41], 0x0
	v_pk_fma_f32 v[70:71], v[70:71], v[124:125], v[78:79]
	v_cvt_f32_f16_e32 v79, v81
	v_cvt_f32_f16_e32 v78, v80
	v_cvt_f32_f16_sdwa v81, v81 dst_sel:DWORD dst_unused:UNUSED_PAD src0_sel:WORD_1
	v_cvt_f32_f16_sdwa v80, v80 dst_sel:DWORD dst_unused:UNUSED_PAD src0_sel:WORD_1
	s_waitcnt lgkmcnt(0)
	v_mov_b64_e32 v[124:125], s[52:53]
	v_pk_add_f32 v[78:79], v[78:79], 1.0 op_sel_hi:[1,0]
	v_pk_fma_f32 v[70:71], v[70:71], s[50:51], v[124:125] op_sel_hi:[1,0,0]
	v_pk_fma_f32 v[72:73], v[72:73], v[78:79], v[80:81]
	v_cvt_pk_f16_f32 v70, v70, v71
	v_pk_fma_f32 v[72:73], v[72:73], s[50:51], v[124:125] op_sel_hi:[1,0,0]
	v_or_b32_e32 v122, 0x80, v178
	v_cvt_pk_f16_f32 v71, v72, v73
	v_lshlrev_b32_e32 v240, 2, v189
	v_lshrrev_b32_e32 v131, 1, v188
	v_add_u32_e32 v190, 0, v238
	s_waitcnt vmcnt(14)
	v_cvt_f32_f16_e32 v79, v87
	v_cvt_f32_f16_e32 v78, v86
	v_cvt_f32_f16_sdwa v81, v87 dst_sel:DWORD dst_unused:UNUSED_PAD src0_sel:WORD_1
	v_cvt_f32_f16_sdwa v80, v86 dst_sel:DWORD dst_unused:UNUSED_PAD src0_sel:WORD_1
	v_pk_add_f32 v[72:73], v[78:79], 1.0 op_sel_hi:[1,0]
	v_cvt_f32_f16_e32 v79, v89
	v_cvt_f32_f16_e32 v78, v88
	v_pk_fma_f32 v[66:67], v[66:67], v[72:73], v[80:81]
	v_cvt_f32_f16_sdwa v81, v89 dst_sel:DWORD dst_unused:UNUSED_PAD src0_sel:WORD_1
	v_cvt_f32_f16_sdwa v80, v88 dst_sel:DWORD dst_unused:UNUSED_PAD src0_sel:WORD_1
	v_pk_fma_f32 v[66:67], v[66:67], s[50:51], v[124:125] op_sel_hi:[1,0,0]
	s_nop 0
	v_cvt_pk_f16_f32 v72, v66, v67
	v_pk_add_f32 v[66:67], v[78:79], 1.0 op_sel_hi:[1,0]
	s_waitcnt vmcnt(13)
	v_cvt_f32_f16_sdwa v79, v127 dst_sel:DWORD dst_unused:UNUSED_PAD src0_sel:WORD_1
	v_pk_fma_f32 v[66:67], v[68:69], v[66:67], v[80:81]
	v_cvt_f32_f16_e32 v69, v127
	v_cvt_f32_f16_e32 v68, v126
	v_cvt_f32_f16_sdwa v78, v126 dst_sel:DWORD dst_unused:UNUSED_PAD src0_sel:WORD_1
	v_pk_fma_f32 v[66:67], v[66:67], s[50:51], v[124:125] op_sel_hi:[1,0,0]
	s_nop 0
	v_cvt_pk_f16_f32 v73, v66, v67
	v_pk_add_f32 v[66:67], v[68:69], 1.0 op_sel_hi:[1,0]
	v_cvt_f32_f16_sdwa v69, v129 dst_sel:DWORD dst_unused:UNUSED_PAD src0_sel:WORD_1
	v_pk_fma_f32 v[62:63], v[62:63], v[66:67], v[78:79]
	v_cvt_f32_f16_e32 v67, v129
	v_cvt_f32_f16_e32 v66, v128
	v_cvt_f32_f16_sdwa v68, v128 dst_sel:DWORD dst_unused:UNUSED_PAD src0_sel:WORD_1
	v_pk_fma_f32 v[62:63], v[62:63], s[50:51], v[124:125] op_sel_hi:[1,0,0]
	s_nop 0
	v_cvt_pk_f16_f32 v78, v62, v63
	v_pk_add_f32 v[62:63], v[66:67], 1.0 op_sel_hi:[1,0]
	s_waitcnt vmcnt(12)
	v_cvt_f32_f16_sdwa v67, v133 dst_sel:DWORD dst_unused:UNUSED_PAD src0_sel:WORD_1
	v_pk_fma_f32 v[62:63], v[64:65], v[62:63], v[68:69]
	v_cvt_f32_f16_e32 v65, v133
	v_cvt_f32_f16_e32 v64, v132
	v_cvt_f32_f16_sdwa v66, v132 dst_sel:DWORD dst_unused:UNUSED_PAD src0_sel:WORD_1
	v_pk_fma_f32 v[62:63], v[62:63], s[50:51], v[124:125] op_sel_hi:[1,0,0]
	s_nop 0
	v_cvt_pk_f16_f32 v79, v62, v63
	v_pk_add_f32 v[62:63], v[64:65], 1.0 op_sel_hi:[1,0]
	v_cvt_f32_f16_sdwa v65, v135 dst_sel:DWORD dst_unused:UNUSED_PAD src0_sel:WORD_1
	v_pk_fma_f32 v[38:39], v[38:39], v[62:63], v[66:67]
	v_cvt_f32_f16_e32 v63, v135
	v_cvt_f32_f16_e32 v62, v134
	v_cvt_f32_f16_sdwa v64, v134 dst_sel:DWORD dst_unused:UNUSED_PAD src0_sel:WORD_1
	v_pk_fma_f32 v[38:39], v[38:39], s[50:51], v[124:125] op_sel_hi:[1,0,0]
	s_waitcnt vmcnt(4)
	v_cvt_f32_f16_sdwa v67, v107 dst_sel:DWORD dst_unused:UNUSED_PAD src0_sel:WORD_1
	v_cvt_pk_f16_f32 v80, v38, v39
	v_pk_add_f32 v[38:39], v[62:63], 1.0 op_sel_hi:[1,0]
	v_cvt_f32_f16_sdwa v63, v145 dst_sel:DWORD dst_unused:UNUSED_PAD src0_sel:WORD_1
	v_pk_fma_f32 v[38:39], v[40:41], v[38:39], v[64:65]
	v_cvt_f32_f16_e32 v41, v145
	v_cvt_f32_f16_e32 v40, v144
	v_cvt_f32_f16_sdwa v62, v144 dst_sel:DWORD dst_unused:UNUSED_PAD src0_sel:WORD_1
	v_pk_fma_f32 v[38:39], v[38:39], s[50:51], v[124:125] op_sel_hi:[1,0,0]
	v_cvt_f32_f16_e32 v65, v107
	v_cvt_pk_f16_f32 v81, v38, v39
	v_pk_add_f32 v[38:39], v[40:41], 1.0 op_sel_hi:[1,0]
	v_cvt_f32_f16_sdwa v41, v147 dst_sel:DWORD dst_unused:UNUSED_PAD src0_sel:WORD_1
	v_pk_fma_f32 v[34:35], v[34:35], v[38:39], v[62:63]
	v_cvt_f32_f16_e32 v39, v147
	v_cvt_f32_f16_e32 v38, v146
	v_cvt_f32_f16_sdwa v40, v146 dst_sel:DWORD dst_unused:UNUSED_PAD src0_sel:WORD_1
	v_pk_fma_f32 v[34:35], v[34:35], s[50:51], v[124:125] op_sel_hi:[1,0,0]
	v_cvt_f32_f16_e32 v64, v106
	v_cvt_pk_f16_f32 v86, v34, v35
	v_pk_add_f32 v[34:35], v[38:39], 1.0 op_sel_hi:[1,0]
	v_cvt_f32_f16_sdwa v39, v149 dst_sel:DWORD dst_unused:UNUSED_PAD src0_sel:WORD_1
	v_pk_fma_f32 v[34:35], v[36:37], v[34:35], v[40:41]
	v_cvt_f32_f16_e32 v37, v149
	v_cvt_f32_f16_e32 v36, v148
	v_cvt_f32_f16_sdwa v38, v148 dst_sel:DWORD dst_unused:UNUSED_PAD src0_sel:WORD_1
	v_pk_fma_f32 v[34:35], v[34:35], s[50:51], v[124:125] op_sel_hi:[1,0,0]
	v_cvt_f32_f16_sdwa v66, v106 dst_sel:DWORD dst_unused:UNUSED_PAD src0_sel:WORD_1
	v_cvt_pk_f16_f32 v87, v34, v35
	v_pk_add_f32 v[34:35], v[36:37], 1.0 op_sel_hi:[1,0]
	v_cvt_f32_f16_sdwa v37, v151 dst_sel:DWORD dst_unused:UNUSED_PAD src0_sel:WORD_1
	v_pk_fma_f32 v[30:31], v[30:31], v[34:35], v[38:39]
	v_cvt_f32_f16_e32 v35, v151
	v_cvt_f32_f16_e32 v34, v150
	v_cvt_f32_f16_sdwa v36, v150 dst_sel:DWORD dst_unused:UNUSED_PAD src0_sel:WORD_1
	v_pk_fma_f32 v[30:31], v[30:31], s[50:51], v[124:125] op_sel_hi:[1,0,0]
	s_nop 0
	v_cvt_pk_f16_f32 v88, v30, v31
	v_pk_add_f32 v[30:31], v[34:35], 1.0 op_sel_hi:[1,0]
	v_cvt_f32_f16_sdwa v35, v95 dst_sel:DWORD dst_unused:UNUSED_PAD src0_sel:WORD_1
	v_pk_fma_f32 v[30:31], v[32:33], v[30:31], v[36:37]
	v_cvt_f32_f16_e32 v33, v95
	v_cvt_f32_f16_e32 v32, v94
	v_cvt_f32_f16_sdwa v34, v94 dst_sel:DWORD dst_unused:UNUSED_PAD src0_sel:WORD_1
	v_pk_fma_f32 v[30:31], v[30:31], s[50:51], v[124:125] op_sel_hi:[1,0,0]
	s_nop 0
	v_cvt_pk_f16_f32 v89, v30, v31
	v_pk_add_f32 v[30:31], v[32:33], 1.0 op_sel_hi:[1,0]
	v_cvt_f32_f16_sdwa v33, v97 dst_sel:DWORD dst_unused:UNUSED_PAD src0_sel:WORD_1
	v_pk_fma_f32 v[26:27], v[26:27], v[30:31], v[34:35]
	v_cvt_f32_f16_e32 v31, v97
	v_cvt_f32_f16_e32 v30, v96
	v_cvt_f32_f16_sdwa v32, v96 dst_sel:DWORD dst_unused:UNUSED_PAD src0_sel:WORD_1
	v_pk_fma_f32 v[26:27], v[26:27], s[50:51], v[124:125] op_sel_hi:[1,0,0]
	s_nop 0
	v_cvt_pk_f16_f32 v94, v26, v27
	v_pk_add_f32 v[26:27], v[30:31], 1.0 op_sel_hi:[1,0]
	v_cvt_f32_f16_sdwa v31, v119 dst_sel:DWORD dst_unused:UNUSED_PAD src0_sel:WORD_1
	v_pk_fma_f32 v[26:27], v[28:29], v[26:27], v[32:33]
	v_cvt_f32_f16_e32 v29, v119
	v_cvt_f32_f16_e32 v28, v118
	v_cvt_f32_f16_sdwa v30, v118 dst_sel:DWORD dst_unused:UNUSED_PAD src0_sel:WORD_1
	v_pk_fma_f32 v[26:27], v[26:27], s[50:51], v[124:125] op_sel_hi:[1,0,0]
	s_nop 0
	v_cvt_pk_f16_f32 v95, v26, v27
	v_pk_add_f32 v[26:27], v[28:29], 1.0 op_sel_hi:[1,0]
	v_cvt_f32_f16_sdwa v29, v121 dst_sel:DWORD dst_unused:UNUSED_PAD src0_sel:WORD_1
	v_pk_fma_f32 v[22:23], v[22:23], v[26:27], v[30:31]
	v_cvt_f32_f16_e32 v27, v121
	v_cvt_f32_f16_e32 v26, v120
	v_cvt_f32_f16_sdwa v28, v120 dst_sel:DWORD dst_unused:UNUSED_PAD src0_sel:WORD_1
	v_pk_fma_f32 v[22:23], v[22:23], s[50:51], v[124:125] op_sel_hi:[1,0,0]
	s_nop 0
	v_cvt_pk_f16_f32 v96, v22, v23
	v_pk_add_f32 v[22:23], v[26:27], 1.0 op_sel_hi:[1,0]
	v_cvt_f32_f16_sdwa v27, v103 dst_sel:DWORD dst_unused:UNUSED_PAD src0_sel:WORD_1
	v_pk_fma_f32 v[22:23], v[24:25], v[22:23], v[28:29]
	v_cvt_f32_f16_e32 v25, v103
	v_cvt_f32_f16_e32 v24, v102
	v_cvt_f32_f16_sdwa v26, v102 dst_sel:DWORD dst_unused:UNUSED_PAD src0_sel:WORD_1
	v_pk_fma_f32 v[22:23], v[22:23], s[50:51], v[124:125] op_sel_hi:[1,0,0]
	s_nop 0
	v_cvt_pk_f16_f32 v97, v22, v23
	v_pk_add_f32 v[22:23], v[24:25], 1.0 op_sel_hi:[1,0]
	v_cvt_f32_f16_sdwa v25, v105 dst_sel:DWORD dst_unused:UNUSED_PAD src0_sel:WORD_1
	v_pk_fma_f32 v[18:19], v[18:19], v[22:23], v[26:27]
	v_cvt_f32_f16_e32 v23, v105
	v_cvt_f32_f16_e32 v22, v104
	v_cvt_f32_f16_sdwa v24, v104 dst_sel:DWORD dst_unused:UNUSED_PAD src0_sel:WORD_1
	v_pk_fma_f32 v[18:19], v[18:19], s[50:51], v[124:125] op_sel_hi:[1,0,0]
	s_nop 0
	v_cvt_pk_f16_f32 v102, v18, v19
	v_pk_add_f32 v[18:19], v[22:23], 1.0 op_sel_hi:[1,0]
	v_cvt_f32_f16_sdwa v23, v115 dst_sel:DWORD dst_unused:UNUSED_PAD src0_sel:WORD_1
	v_pk_fma_f32 v[18:19], v[20:21], v[18:19], v[24:25]
	v_cvt_f32_f16_e32 v21, v115
	v_cvt_f32_f16_e32 v20, v114
	v_cvt_f32_f16_sdwa v22, v114 dst_sel:DWORD dst_unused:UNUSED_PAD src0_sel:WORD_1
	v_pk_fma_f32 v[18:19], v[18:19], s[50:51], v[124:125] op_sel_hi:[1,0,0]
	s_nop 0
	v_cvt_pk_f16_f32 v103, v18, v19
	v_pk_add_f32 v[18:19], v[20:21], 1.0 op_sel_hi:[1,0]
	v_cvt_f32_f16_sdwa v21, v117 dst_sel:DWORD dst_unused:UNUSED_PAD src0_sel:WORD_1
	v_pk_fma_f32 v[14:15], v[14:15], v[18:19], v[22:23]
	v_cvt_f32_f16_e32 v19, v117
	v_cvt_f32_f16_e32 v18, v116
	v_cvt_f32_f16_sdwa v20, v116 dst_sel:DWORD dst_unused:UNUSED_PAD src0_sel:WORD_1
	v_pk_fma_f32 v[14:15], v[14:15], s[50:51], v[124:125] op_sel_hi:[1,0,0]
	s_nop 0
	v_cvt_pk_f16_f32 v104, v14, v15
	v_pk_add_f32 v[14:15], v[18:19], 1.0 op_sel_hi:[1,0]
	v_cvt_f32_f16_sdwa v19, v111 dst_sel:DWORD dst_unused:UNUSED_PAD src0_sel:WORD_1
	v_pk_fma_f32 v[14:15], v[16:17], v[14:15], v[20:21]
	v_cvt_f32_f16_e32 v17, v111
	v_cvt_f32_f16_e32 v16, v110
	v_cvt_f32_f16_sdwa v18, v110 dst_sel:DWORD dst_unused:UNUSED_PAD src0_sel:WORD_1
	v_pk_fma_f32 v[14:15], v[14:15], s[50:51], v[124:125] op_sel_hi:[1,0,0]
	s_nop 0
	v_cvt_pk_f16_f32 v105, v14, v15
	v_pk_add_f32 v[14:15], v[16:17], 1.0 op_sel_hi:[1,0]
	v_cvt_f32_f16_sdwa v17, v113 dst_sel:DWORD dst_unused:UNUSED_PAD src0_sel:WORD_1
	v_pk_fma_f32 v[10:11], v[10:11], v[14:15], v[18:19]
	v_cvt_f32_f16_e32 v15, v113
	v_cvt_f32_f16_e32 v14, v112
	v_cvt_f32_f16_sdwa v16, v112 dst_sel:DWORD dst_unused:UNUSED_PAD src0_sel:WORD_1
	v_pk_fma_f32 v[10:11], v[10:11], s[50:51], v[124:125] op_sel_hi:[1,0,0]
	s_nop 0
	v_cvt_pk_f16_f32 v110, v10, v11
	v_pk_add_f32 v[10:11], v[14:15], 1.0 op_sel_hi:[1,0]
	s_nop 0
	v_pk_fma_f32 v[62:63], v[12:13], v[10:11], v[16:17]
	v_lshl_add_u64 v[10:11], v[182:183], 0, v[178:179]
	global_load_dwordx4 v[34:37], v[10:11], off offset:16
	global_load_dwordx4 v[38:41], v[10:11], off
	v_lshl_add_u64 v[10:11], v[182:183], 0, v[122:123]
	v_or_b32_e32 v122, 0x100, v178
	global_load_dwordx4 v[26:29], v[10:11], off offset:16
	global_load_dwordx4 v[30:33], v[10:11], off
	v_lshl_add_u64 v[10:11], v[182:183], 0, v[122:123]
	v_or_b32_e32 v122, 0x180, v178
	v_lshl_add_u64 v[14:15], v[182:183], 0, v[122:123]
	global_load_dwordx4 v[18:21], v[10:11], off offset:16
	global_load_dwordx4 v[22:25], v[10:11], off
	s_nop 0
	global_load_dwordx4 v[10:13], v[14:15], off offset:16
	s_nop 0
	global_load_dwordx4 v[14:17], v[14:15], off
	v_pk_fma_f32 v[62:63], v[62:63], s[50:51], v[124:125] op_sel_hi:[1,0,0]
	s_nop 0
	v_cvt_pk_f16_f32 v111, v62, v63
	v_pk_add_f32 v[62:63], v[64:65], 1.0 op_sel_hi:[1,0]
	v_cvt_f32_f16_sdwa v65, v109 dst_sel:DWORD dst_unused:UNUSED_PAD src0_sel:WORD_1
	v_pk_fma_f32 v[58:59], v[58:59], v[62:63], v[66:67]
	v_cvt_f32_f16_e32 v63, v109
	v_cvt_f32_f16_e32 v62, v108
	v_cvt_f32_f16_sdwa v64, v108 dst_sel:DWORD dst_unused:UNUSED_PAD src0_sel:WORD_1
	v_pk_fma_f32 v[58:59], v[58:59], s[50:51], v[124:125] op_sel_hi:[1,0,0]
	s_nop 0
	v_cvt_pk_f16_f32 v112, v58, v59
	v_pk_add_f32 v[58:59], v[62:63], 1.0 op_sel_hi:[1,0]
	s_waitcnt vmcnt(11)
	v_cvt_f32_f16_sdwa v63, v99 dst_sel:DWORD dst_unused:UNUSED_PAD src0_sel:WORD_1
	v_pk_fma_f32 v[58:59], v[60:61], v[58:59], v[64:65]
	v_cvt_f32_f16_e32 v61, v99
	v_cvt_f32_f16_e32 v60, v98
	v_cvt_f32_f16_sdwa v62, v98 dst_sel:DWORD dst_unused:UNUSED_PAD src0_sel:WORD_1
	v_pk_fma_f32 v[58:59], v[58:59], s[50:51], v[124:125] op_sel_hi:[1,0,0]
	s_nop 0
	v_cvt_pk_f16_f32 v113, v58, v59
	v_pk_add_f32 v[58:59], v[60:61], 1.0 op_sel_hi:[1,0]
	v_cvt_f32_f16_sdwa v61, v101 dst_sel:DWORD dst_unused:UNUSED_PAD src0_sel:WORD_1
	v_pk_fma_f32 v[54:55], v[54:55], v[58:59], v[62:63]
	v_cvt_f32_f16_e32 v59, v101
	v_cvt_f32_f16_e32 v58, v100
	v_cvt_f32_f16_sdwa v60, v100 dst_sel:DWORD dst_unused:UNUSED_PAD src0_sel:WORD_1
	v_pk_fma_f32 v[54:55], v[54:55], s[50:51], v[124:125] op_sel_hi:[1,0,0]
	s_nop 0
	v_cvt_pk_f16_f32 v126, v54, v55
	v_pk_add_f32 v[54:55], v[58:59], 1.0 op_sel_hi:[1,0]
	s_waitcnt vmcnt(10)
	v_cvt_f32_f16_sdwa v59, v91 dst_sel:DWORD dst_unused:UNUSED_PAD src0_sel:WORD_1
	v_pk_fma_f32 v[54:55], v[56:57], v[54:55], v[60:61]
	v_cvt_f32_f16_e32 v57, v91
	v_cvt_f32_f16_e32 v56, v90
	v_cvt_f32_f16_sdwa v58, v90 dst_sel:DWORD dst_unused:UNUSED_PAD src0_sel:WORD_1
	v_pk_fma_f32 v[54:55], v[54:55], s[50:51], v[124:125] op_sel_hi:[1,0,0]
	s_nop 0
	v_cvt_pk_f16_f32 v127, v54, v55
	v_pk_add_f32 v[54:55], v[56:57], 1.0 op_sel_hi:[1,0]
	v_cvt_f32_f16_sdwa v57, v93 dst_sel:DWORD dst_unused:UNUSED_PAD src0_sel:WORD_1
	v_pk_fma_f32 v[50:51], v[50:51], v[54:55], v[58:59]
	v_cvt_f32_f16_e32 v55, v93
	v_cvt_f32_f16_e32 v54, v92
	v_cvt_f32_f16_sdwa v56, v92 dst_sel:DWORD dst_unused:UNUSED_PAD src0_sel:WORD_1
	v_pk_fma_f32 v[50:51], v[50:51], s[50:51], v[124:125] op_sel_hi:[1,0,0]
	s_nop 0
	v_cvt_pk_f16_f32 v128, v50, v51
	v_pk_add_f32 v[50:51], v[54:55], 1.0 op_sel_hi:[1,0]
	s_waitcnt vmcnt(9)
	v_cvt_f32_f16_sdwa v55, v83 dst_sel:DWORD dst_unused:UNUSED_PAD src0_sel:WORD_1
	v_pk_fma_f32 v[50:51], v[52:53], v[50:51], v[56:57]
	v_cvt_f32_f16_e32 v53, v83
	v_cvt_f32_f16_e32 v52, v82
	v_cvt_f32_f16_sdwa v54, v82 dst_sel:DWORD dst_unused:UNUSED_PAD src0_sel:WORD_1
	v_pk_fma_f32 v[50:51], v[50:51], s[50:51], v[124:125] op_sel_hi:[1,0,0]
	s_nop 0
	v_cvt_pk_f16_f32 v129, v50, v51
	v_pk_add_f32 v[50:51], v[52:53], 1.0 op_sel_hi:[1,0]
	v_cvt_f32_f16_sdwa v53, v85 dst_sel:DWORD dst_unused:UNUSED_PAD src0_sel:WORD_1
	v_pk_fma_f32 v[46:47], v[46:47], v[50:51], v[54:55]
	v_cvt_f32_f16_e32 v51, v85
	v_cvt_f32_f16_e32 v50, v84
	v_cvt_f32_f16_sdwa v52, v84 dst_sel:DWORD dst_unused:UNUSED_PAD src0_sel:WORD_1
	v_pk_fma_f32 v[46:47], v[46:47], s[50:51], v[124:125] op_sel_hi:[1,0,0]
	s_nop 0
	v_cvt_pk_f16_f32 v134, v46, v47
	v_pk_add_f32 v[46:47], v[50:51], 1.0 op_sel_hi:[1,0]
	s_waitcnt vmcnt(8)
	v_cvt_f32_f16_sdwa v51, v75 dst_sel:DWORD dst_unused:UNUSED_PAD src0_sel:WORD_1
	v_pk_fma_f32 v[46:47], v[48:49], v[46:47], v[52:53]
	v_cvt_f32_f16_e32 v49, v75
	v_cvt_f32_f16_e32 v48, v74
	v_cvt_f32_f16_sdwa v50, v74 dst_sel:DWORD dst_unused:UNUSED_PAD src0_sel:WORD_1
	v_pk_fma_f32 v[46:47], v[46:47], s[50:51], v[124:125] op_sel_hi:[1,0,0]
	s_nop 0
	v_cvt_pk_f16_f32 v135, v46, v47
	v_pk_add_f32 v[46:47], v[48:49], 1.0 op_sel_hi:[1,0]
	v_cvt_f32_f16_sdwa v49, v77 dst_sel:DWORD dst_unused:UNUSED_PAD src0_sel:WORD_1
	v_pk_fma_f32 v[42:43], v[42:43], v[46:47], v[50:51]
	v_cvt_f32_f16_e32 v47, v77
	v_cvt_f32_f16_e32 v46, v76
	v_cvt_f32_f16_sdwa v48, v76 dst_sel:DWORD dst_unused:UNUSED_PAD src0_sel:WORD_1
	v_pk_fma_f32 v[42:43], v[42:43], s[50:51], v[124:125] op_sel_hi:[1,0,0]
	s_nop 0
	v_cvt_pk_f16_f32 v136, v42, v43
	v_pk_add_f32 v[42:43], v[46:47], 1.0 op_sel_hi:[1,0]
	s_nop 0
	v_pk_fma_f32 v[42:43], v[44:45], v[42:43], v[48:49]
	s_nop 0
	v_pk_fma_f32 v[42:43], v[42:43], s[50:51], v[124:125] op_sel_hi:[1,0,0]
	s_nop 0
	v_cvt_pk_f16_f32 v137, v42, v43
	v_xor_b32_e32 v42, v189, v131
	v_lshlrev_b32_e32 v139, 4, v42
	v_add_u32_e32 v236, v130, v139
	ds_read_b128 v[42:45], v236
	ds_read_b128 v[46:49], v236 offset:2048
	v_bitop3_b32 v62, v189, v131, 4 bitop3:0x36
	v_lshlrev_b32_e32 v152, 4, v62
	v_add_u32_e32 v237, v130, v152
	s_waitcnt lgkmcnt(1)
	v_mfma_f32_16x16x32_f16 v[50:53], v[42:45], v[70:73], 0
	ds_read_b128 v[62:65], v237
	ds_read_b128 v[66:69], v237 offset:2048
	v_or_b32_e32 v194, v138, v139
	v_or_b32_e32 v195, v138, v152
	v_mfma_f32_16x16x32_f16 v[54:57], v[42:45], v[86:89], 0
	v_lshlrev_b32_e32 v179, 7, v189
	v_mov_b32_e32 v241, v179
	v_mov_b32_e32 v242, v195
	v_mfma_f32_16x16x32_f16 v[58:61], v[42:45], v[102:105], 0
	v_mov_b32_e32 v243, v194
	v_mfma_f32_16x16x32_f16 v[42:45], v[42:45], v[126:129], 0
	s_waitcnt lgkmcnt(1)
	v_mfma_f32_16x16x32_f16 v[130:133], v[62:65], v[78:81], v[50:53]
	v_mfma_f32_16x16x32_f16 v[122:125], v[62:65], v[94:97], v[54:57]
	v_mfma_f32_16x16x32_f16 v[114:117], v[62:65], v[134:137], v[42:45]
	v_mfma_f32_16x16x32_f16 v[42:45], v[46:49], v[70:73], 0
	v_mfma_f32_16x16x32_f16 v[50:53], v[46:49], v[86:89], 0
	v_mfma_f32_16x16x32_f16 v[54:57], v[46:49], v[102:105], 0
	v_mfma_f32_16x16x32_f16 v[46:49], v[46:49], v[126:129], 0
	s_waitcnt lgkmcnt(0)
	v_mfma_f32_16x16x32_f16 v[106:109], v[66:69], v[78:81], v[42:45]
	v_mfma_f32_16x16x32_f16 v[82:85], v[66:69], v[134:137], v[46:49]
	s_nop 1
	ds_read_b128 v[42:45], v236 offset:4096
	s_nop 1
	ds_read_b128 v[46:49], v236 offset:6144
	ds_read_b128 v[140:143], v237 offset:4096
	ds_read_b128 v[144:147], v237 offset:6144
	v_mfma_f32_16x16x32_f16 v[118:121], v[62:65], v[110:113], v[58:61]
	v_mfma_f32_16x16x32_f16 v[98:101], v[66:69], v[94:97], v[50:53]
	v_mfma_f32_16x16x32_f16 v[90:93], v[66:69], v[110:113], v[54:57]
	s_waitcnt lgkmcnt(3)
	v_mfma_f32_16x16x32_f16 v[50:53], v[42:45], v[70:73], 0
	v_mfma_f32_16x16x32_f16 v[54:57], v[42:45], v[86:89], 0
	v_mfma_f32_16x16x32_f16 v[58:61], v[42:45], v[102:105], 0
	v_mfma_f32_16x16x32_f16 v[42:45], v[42:45], v[126:129], 0
	s_waitcnt lgkmcnt(1)
	v_mfma_f32_16x16x32_f16 v[74:77], v[140:143], v[78:81], v[50:53]
	v_mfma_f32_16x16x32_f16 v[66:69], v[140:143], v[94:97], v[54:57]
	v_mfma_f32_16x16x32_f16 v[62:65], v[140:143], v[110:113], v[58:61]
	v_mfma_f32_16x16x32_f16 v[58:61], v[140:143], v[134:137], v[42:45]
	v_mfma_f32_16x16x32_f16 v[42:45], v[46:49], v[70:73], 0
	v_mfma_f32_16x16x32_f16 v[50:53], v[46:49], v[86:89], 0
	v_mfma_f32_16x16x32_f16 v[140:143], v[46:49], v[102:105], 0
	v_mfma_f32_16x16x32_f16 v[148:151], v[46:49], v[126:129], 0
	s_waitcnt lgkmcnt(0)
	v_mfma_f32_16x16x32_f16 v[54:57], v[144:147], v[78:81], v[42:45]
	v_mfma_f32_16x16x32_f16 v[50:53], v[144:147], v[94:97], v[50:53]
	v_mfma_f32_16x16x32_f16 v[46:49], v[144:147], v[110:113], v[140:143]
	v_mfma_f32_16x16x32_f16 v[42:45], v[144:147], v[134:137], v[148:151]
.LBB3_25:
	s_nop 1
	v_add_u32_e32 v142, 0, v243
	ds_read_b128 v[138:141], v142
	ds_read_b128 v[142:145], v142 offset:2048
	s_waitcnt lgkmcnt(1)
	v_mfma_f32_16x16x32_f16 v[146:149], v[138:141], v[70:73], 0
	v_mfma_f32_16x16x32_f16 v[150:153], v[138:141], v[86:89], 0
	v_mfma_f32_16x16x32_f16 v[154:157], v[138:141], v[102:105], 0
	v_mfma_f32_16x16x32_f16 v[158:161], v[138:141], v[126:129], 0
	v_add_u32_e32 v138, 0, v242
	ds_read_b128 v[166:169], v138
	ds_read_b128 v[170:173], v138 offset:2048
	s_waitcnt lgkmcnt(1)
	v_mfma_f32_16x16x32_f16 v[162:165], v[166:169], v[78:81], v[146:149]
	v_mfma_f32_16x16x32_f16 v[150:153], v[166:169], v[94:97], v[150:153]
	v_mfma_f32_16x16x32_f16 v[138:141], v[166:169], v[110:113], v[154:157]
	v_mfma_f32_16x16x32_f16 v[244:247], v[166:169], v[134:137], v[158:161]
	v_mfma_f32_16x16x32_f16 v[146:149], v[142:145], v[70:73], 0
	v_mfma_f32_16x16x32_f16 v[154:157], v[142:145], v[86:89], 0
	v_mfma_f32_16x16x32_f16 v[166:169], v[142:145], v[102:105], 0
	v_mfma_f32_16x16x32_f16 v[174:177], v[142:145], v[126:129], 0
	s_waitcnt lgkmcnt(0)
	v_mfma_f32_16x16x32_f16 v[158:161], v[170:173], v[78:81], v[146:149]
	v_mfma_f32_16x16x32_f16 v[154:157], v[170:173], v[94:97], v[154:157]
	v_mfma_f32_16x16x32_f16 v[142:145], v[170:173], v[110:113], v[166:169]
	v_mfma_f32_16x16x32_f16 v[170:173], v[170:173], v[134:137], v[174:177]
	v_add_u32_e32 v184, 0, v241
	v_add_u32_e32 v146, 0x12600, v184
	ds_read_b128 v[146:149], v146
	v_add_u32_e32 v166, 0x12620, v184
	ds_read_b64 v[186:187], v166
	v_add_u32_e32 v166, 0x12610, v184
	ds_read_b128 v[166:169], v166
	s_waitcnt lgkmcnt(2)
	v_fma_f32 v174, v146, v162, v150
	v_fma_f32 v174, -v147, v163, v174
	v_fma_f32 v175, v146, v163, v151
	v_fmac_f32_e32 v175, v147, v162
	v_fma_f32 v176, v146, v174, v138
	v_fma_f32 v176, -v147, v175, v176
	v_fma_f32 v175, v146, v175, v139
	v_fmac_f32_e32 v175, v147, v174
	v_fma_f32 v174, v146, v176, v244
	v_fma_f32 v174, -v147, v175, v174
	v_fma_f32 v248, v146, v175, v245
	v_fmac_f32_e32 v248, v147, v176
	v_mov_b32_dpp v175, v174 row_shr:1 row_mask:0xf bank_mask:0xf bound_ctrl:1
	v_fmac_f32_e32 v174, v148, v175
	v_mov_b32_dpp v176, v248 row_shr:1 row_mask:0xf bank_mask:0xf bound_ctrl:1
	v_fma_f32 v174, -v149, v176, v174
	v_fmac_f32_e32 v248, v148, v176
	v_fmac_f32_e32 v248, v149, v175
	v_mov_b32_dpp v148, v174 row_shr:2 row_mask:0xf bank_mask:0xf bound_ctrl:1
	v_add_u32_e32 v175, 0x12660, v184
	v_mov_b32_dpp v149, v248 row_shr:2 row_mask:0xf bank_mask:0xf bound_ctrl:1
	ds_read_b64 v[244:245], v175
	s_waitcnt lgkmcnt(1)
	v_fmac_f32_e32 v174, v166, v148
	v_fma_f32 v174, -v167, v149, v174
	v_fmac_f32_e32 v248, v166, v149
	v_fmac_f32_e32 v248, v167, v148
	v_mov_b32_dpp v148, v174 row_shr:4 row_mask:0xf bank_mask:0xf bound_ctrl:1
	v_fmac_f32_e32 v174, v168, v148
	v_mov_b32_dpp v149, v248 row_shr:4 row_mask:0xf bank_mask:0xf bound_ctrl:1
	v_fma_f32 v166, -v169, v149, v174
	v_fmac_f32_e32 v248, v168, v149
	v_fmac_f32_e32 v248, v169, v148
	v_mov_b32_dpp v148, v166 row_shr:8 row_mask:0xf bank_mask:0xf bound_ctrl:1
	v_fmac_f32_e32 v166, v186, v148
	v_mov_b32_dpp v149, v248 row_shr:8 row_mask:0xf bank_mask:0xf bound_ctrl:1
	v_fma_f32 v249, -v187, v149, v166
	v_add_u32_e32 v166, 0x12640, v184
	v_add_u32_e32 v167, 0x12650, v184
	ds_read_b128 v[174:177], v167
	ds_read_b128 v[166:169], v166
	v_fmac_f32_e32 v248, v186, v149
	v_fmac_f32_e32 v248, v187, v148
	v_mov_b32_dpp v186, v249 row_shr:1 row_mask:0xf bank_mask:0xf bound_ctrl:1
	v_xor_b32_e32 v185, 0x80000000, v147
	s_waitcnt lgkmcnt(0)
	v_fma_f32 v148, v166, v164, v152
	v_mov_b32_dpp v187, v248 row_shr:1 row_mask:0xf bank_mask:0xf bound_ctrl:1
	v_fma_f32 v148, -v167, v165, v148
	v_fma_f32 v248, v166, v165, v153
	v_fmac_f32_e32 v248, v167, v164
	v_fma_f32 v249, v166, v148, v140
	v_fma_f32 v249, -v167, v248, v249
	v_fma_f32 v248, v166, v248, v141
	v_fmac_f32_e32 v248, v167, v148
	v_fma_f32 v148, v166, v249, v246
	v_fma_f32 v148, -v167, v248, v148
	v_fmac_f32_e32 v247, v166, v248
	v_fmac_f32_e32 v247, v167, v249
	v_mov_b32_dpp v246, v148 row_shr:1 row_mask:0xf bank_mask:0xf bound_ctrl:1
	v_fmac_f32_e32 v148, v168, v246
	v_mov_b32_dpp v248, v247 row_shr:1 row_mask:0xf bank_mask:0xf bound_ctrl:1
	v_fma_f32 v148, -v169, v248, v148
	v_fmac_f32_e32 v247, v168, v248
	v_fmac_f32_e32 v247, v169, v246
	v_mov_b32_dpp v168, v148 row_shr:2 row_mask:0xf bank_mask:0xf bound_ctrl:1
	v_fmac_f32_e32 v148, v174, v168
	v_mov_b32_dpp v169, v247 row_shr:2 row_mask:0xf bank_mask:0xf bound_ctrl:1
	v_fma_f32 v148, -v175, v169, v148
	v_fmac_f32_e32 v247, v174, v169
	v_fmac_f32_e32 v247, v175, v168
	v_mov_b32_dpp v168, v148 row_shr:4 row_mask:0xf bank_mask:0xf bound_ctrl:1
	v_fmac_f32_e32 v148, v176, v168
	v_mov_b32_dpp v169, v247 row_shr:4 row_mask:0xf bank_mask:0xf bound_ctrl:1
	v_fma_f32 v148, -v177, v169, v148
	v_fmac_f32_e32 v247, v176, v169
	v_fmac_f32_e32 v247, v177, v168
	v_mov_b32_dpp v168, v148 row_shr:8 row_mask:0xf bank_mask:0xf bound_ctrl:1
	v_fmac_f32_e32 v148, v244, v168
	v_mov_b32_dpp v169, v247 row_shr:8 row_mask:0xf bank_mask:0xf bound_ctrl:1
	v_fma_f32 v148, -v245, v169, v148
	v_fmac_f32_e32 v247, v244, v169
	v_add_u32_e32 v169, 0x12820, v184
	v_fmac_f32_e32 v247, v245, v168
	v_add_u32_e32 v168, 0x12800, v184
	ds_read_b64 v[248:249], v169
	ds_read_b128 v[174:177], v168
	v_mov_b32_dpp v250, v148 row_shr:1 row_mask:0xf bank_mask:0xf bound_ctrl:1
	v_add_u32_e32 v148, 0x12810, v184
	v_mov_b32_dpp v251, v247 row_shr:1 row_mask:0xf bank_mask:0xf bound_ctrl:1
	ds_read_b128 v[244:247], v148
	s_waitcnt lgkmcnt(1)
	v_fma_f32 v148, v174, v158, v154
	v_fma_f32 v148, -v175, v159, v148
	v_fma_f32 v168, v174, v159, v155
	v_fmac_f32_e32 v168, v175, v158
	v_fma_f32 v169, v174, v148, v142
	v_fma_f32 v169, -v175, v168, v169
	v_fma_f32 v168, v174, v168, v143
	v_fmac_f32_e32 v168, v175, v148
	v_fma_f32 v252, v174, v168, v171
	v_fma_f32 v148, v174, v169, v170
	v_fmac_f32_e32 v252, v175, v169
	v_fma_f32 v148, -v175, v168, v148
	v_add_u32_e32 v170, 0x12860, v184
	v_mov_b32_dpp v169, v252 row_shr:1 row_mask:0xf bank_mask:0xf bound_ctrl:1
	v_mov_b32_dpp v168, v148 row_shr:1 row_mask:0xf bank_mask:0xf bound_ctrl:1
	v_fmac_f32_e32 v252, v176, v169
	v_fmac_f32_e32 v148, v176, v168
	v_fmac_f32_e32 v252, v177, v168
	v_fma_f32 v148, -v177, v169, v148
	ds_read_b64 v[176:177], v170
	v_mov_b32_dpp v169, v252 row_shr:2 row_mask:0xf bank_mask:0xf bound_ctrl:1
	v_mov_b32_dpp v168, v148 row_shr:2 row_mask:0xf bank_mask:0xf bound_ctrl:1
	s_waitcnt lgkmcnt(1)
	v_fmac_f32_e32 v252, v244, v169
	v_fmac_f32_e32 v148, v244, v168
	v_fmac_f32_e32 v252, v245, v168
	v_fma_f32 v148, -v245, v169, v148
	v_add_u32_e32 v244, 0x12840, v184
	v_mov_b32_dpp v169, v252 row_shr:4 row_mask:0xf bank_mask:0xf bound_ctrl:1
	v_mov_b32_dpp v168, v148 row_shr:4 row_mask:0xf bank_mask:0xf bound_ctrl:1
	v_fmac_f32_e32 v252, v246, v169
	v_fmac_f32_e32 v148, v246, v168
	v_fmac_f32_e32 v252, v247, v168
	v_add_u32_e32 v168, 0x12850, v184
	v_fma_f32 v148, -v247, v169, v148
	ds_read_b128 v[168:171], v168
	ds_read_b128 v[244:247], v244
	v_mov_b32_dpp v254, v148 row_shr:8 row_mask:0xf bank_mask:0xf bound_ctrl:1
	v_mov_b32_dpp v255, v252 row_shr:8 row_mask:0xf bank_mask:0xf bound_ctrl:1
	v_fmac_f32_e32 v148, v248, v254
	v_fma_f32 v148, -v249, v255, v148
	v_fmac_f32_e32 v252, v248, v255
	v_fmac_f32_e32 v252, v249, v254
	v_mov_b32_dpp v248, v148 row_shr:1 row_mask:0xf bank_mask:0xf bound_ctrl:1
	s_waitcnt lgkmcnt(0)
	v_fma_f32 v148, v244, v160, v156
	v_fma_f32 v148, -v245, v161, v148
	v_fma_f32 v184, v244, v161, v157
	v_mov_b32_dpp v249, v252 row_shr:1 row_mask:0xf bank_mask:0xf bound_ctrl:1
	v_fmac_f32_e32 v184, v245, v160
	v_fma_f32 v252, v244, v148, v144
	v_fma_f32 v252, -v245, v184, v252
	v_fma_f32 v184, v244, v184, v145
	v_fmac_f32_e32 v184, v245, v148
	v_fma_f32 v148, v244, v252, v172
	v_fmac_f32_e32 v173, v244, v184
	v_fma_f32 v148, -v245, v184, v148
	v_fmac_f32_e32 v173, v245, v252
	v_xor_b32_e32 v149, 0x80000000, v167
	v_mov_b32_dpp v172, v148 row_shr:1 row_mask:0xf bank_mask:0xf bound_ctrl:1
	v_mov_b32_dpp v184, v173 row_shr:1 row_mask:0xf bank_mask:0xf bound_ctrl:1
	v_fmac_f32_e32 v148, v246, v172
	v_fmac_f32_e32 v173, v246, v184
	v_fma_f32 v148, -v247, v184, v148
	v_fmac_f32_e32 v173, v247, v172
	v_xor_b32_e32 v253, 0x80000000, v175
	v_mov_b32_dpp v172, v148 row_shr:2 row_mask:0xf bank_mask:0xf bound_ctrl:1
	v_mov_b32_dpp v184, v173 row_shr:2 row_mask:0xf bank_mask:0xf bound_ctrl:1
	v_fmac_f32_e32 v148, v168, v172
	v_fmac_f32_e32 v173, v168, v184
	v_fma_f32 v148, -v169, v184, v148
	v_fmac_f32_e32 v173, v169, v172
	v_xor_b32_e32 v255, 0x80000000, v245
	v_mov_b32_dpp v168, v148 row_shr:4 row_mask:0xf bank_mask:0xf bound_ctrl:1
	v_mov_b32_dpp v169, v173 row_shr:4 row_mask:0xf bank_mask:0xf bound_ctrl:1
	v_fmac_f32_e32 v148, v170, v168
	v_fmac_f32_e32 v173, v170, v169
	v_fma_f32 v148, -v171, v169, v148
	v_fmac_f32_e32 v173, v171, v168
	s_nop 0
	v_mov_b32_dpp v168, v148 row_shr:8 row_mask:0xf bank_mask:0xf bound_ctrl:1
	v_mov_b32_dpp v169, v173 row_shr:8 row_mask:0xf bank_mask:0xf bound_ctrl:1
	v_fmac_f32_e32 v148, v176, v168
	v_fmac_f32_e32 v173, v176, v169
	v_fma_f32 v148, -v177, v169, v148
	v_fmac_f32_e32 v173, v177, v168
	s_nop 0
	v_mov_b32_dpp v168, v148 row_shr:1 row_mask:0xf bank_mask:0xf bound_ctrl:1
	v_mov_b32_dpp v169, v173 row_shr:1 row_mask:0xf bank_mask:0xf bound_ctrl:1
	v_pk_fma_f32 v[162:163], v[146:147], v[186:187], v[162:163] op_sel_hi:[0,1,1]
	v_pk_fma_f32 v[170:171], v[174:175], v[248:249], v[158:159] op_sel_hi:[0,1,1]
	v_pk_fma_f32 v[164:165], v[166:167], v[250:251], v[164:165] op_sel_hi:[0,1,1]
	v_pk_fma_f32 v[172:173], v[244:245], v[168:169], v[160:161] op_sel_hi:[0,1,1]
	v_cvt_pk_f16_f32 v161, v168, v169
	v_add_u32_e32 v176, s33, v189
	v_pk_fma_f32 v[162:163], v[146:147], v[186:187], v[162:163] op_sel:[1,0,1] op_sel_hi:[1,1,0] neg_hi:[1,0,0]
	v_pk_fma_f32 v[170:171], v[174:175], v[248:249], v[170:171] op_sel:[1,0,1] op_sel_hi:[1,1,0] neg_hi:[1,0,0]
	v_pk_fma_f32 v[164:165], v[166:167], v[250:251], v[164:165] op_sel:[1,0,1] op_sel_hi:[1,1,0] neg_hi:[1,0,0]
	v_pk_fma_f32 v[168:169], v[244:245], v[168:169], v[172:173] op_sel:[1,0,1] op_sel_hi:[1,1,0] neg_hi:[1,0,0]
	v_mov_b32_e32 v184, v147
	v_mov_b32_e32 v252, v175
	v_mov_b32_e32 v148, v167
	v_mov_b32_e32 v254, v245
	v_cvt_pk_f16_f32 v158, v186, v187
	v_xor_b32_e32 v186, v176, v188
	v_pk_fma_f32 v[172:173], v[146:147], v[162:163], v[150:151] op_sel:[0,1,0] op_sel_hi:[0,0,1]
	v_pk_fma_f32 v[154:155], v[174:175], v[170:171], v[154:155] op_sel:[0,1,0] op_sel_hi:[0,0,1]
	v_pk_fma_f32 v[176:177], v[166:167], v[164:165], v[152:153] op_sel:[0,1,0] op_sel_hi:[0,0,1]
	v_pk_fma_f32 v[156:157], v[244:245], v[168:169], v[156:157] op_sel:[0,1,0] op_sel_hi:[0,0,1]
	v_cvt_pk_f16_f32 v153, v169, v168
	v_cvt_pk_f16_f32 v152, v171, v170
	v_lshl_add_u32 v186, v186, 4, v190
	v_pk_fma_f32 v[172:173], v[184:185], v[162:163], v[172:173] op_sel:[1,0,0] op_sel_hi:[0,1,1]
	v_pk_fma_f32 v[170:171], v[252:253], v[170:171], v[154:155] op_sel:[1,0,0] op_sel_hi:[0,1,1]
	v_pk_fma_f32 v[148:149], v[148:149], v[164:165], v[176:177] op_sel:[1,0,0] op_sel_hi:[0,1,1]
	v_pk_fma_f32 v[168:169], v[254:255], v[168:169], v[156:157] op_sel:[1,0,0] op_sel_hi:[0,1,1]
	v_cvt_pk_f16_f32 v151, v165, v164
	v_cvt_pk_f16_f32 v150, v163, v162
	ds_read_b128 v[154:157], v186 offset:32768
	ds_read_b128 v[162:165], v186 offset:36864
	v_pk_fma_f32 v[176:177], v[146:147], v[172:173], v[138:139] op_sel_hi:[0,1,1]
	v_pk_fma_f32 v[142:143], v[174:175], v[170:171], v[142:143] op_sel_hi:[0,1,1]
	v_pk_fma_f32 v[184:185], v[166:167], v[148:149], v[140:141] op_sel_hi:[0,1,1]
	v_pk_fma_f32 v[144:145], v[244:245], v[168:169], v[144:145] op_sel_hi:[0,1,1]
	v_cvt_pk_f16_f32 v139, v148, v149
	v_pk_fma_f32 v[146:147], v[146:147], v[172:173], v[176:177] op_sel:[1,0,1] op_sel_hi:[1,1,0] neg_hi:[1,0,0]
	v_pk_fma_f32 v[142:143], v[174:175], v[170:171], v[142:143] op_sel:[1,0,1] op_sel_hi:[1,1,0] neg_hi:[1,0,0]
	v_pk_fma_f32 v[148:149], v[166:167], v[148:149], v[184:185] op_sel:[1,0,1] op_sel_hi:[1,1,0] neg_hi:[1,0,0]
	v_pk_fma_f32 v[144:145], v[244:245], v[168:169], v[144:145] op_sel:[1,0,1] op_sel_hi:[1,1,0] neg_hi:[1,0,0]
	v_cvt_pk_f16_f32 v146, v146, v147
	v_cvt_pk_f16_f32 v147, v142, v143
	v_cvt_pk_f16_f32 v142, v148, v149
	v_cvt_pk_f16_f32 v145, v144, v145
	v_cvt_pk_f16_f32 v160, v248, v249
	v_cvt_pk_f16_f32 v159, v250, v251
	v_cvt_pk_f16_f32 v141, v168, v169
	v_cvt_pk_f16_f32 v140, v170, v171
	v_cvt_pk_f16_f32 v138, v172, v173
	v_alignbit_b32 v143, v142, v142, 16
	v_alignbit_b32 v142, v146, v146, 16
	v_alignbit_b32 v144, v147, v147, 16
	v_alignbit_b32 v145, v145, v145, 16
	s_waitcnt lgkmcnt(1)
	v_mfma_f32_16x16x32_f16 v[130:133], v[154:157], v[158:161], v[130:133]
	s_add_i32 s33, s33, 4
	v_add_u32_e32 v243, 0x1000, v243
	v_add_u32_e32 v242, 0x1000, v242
	v_mfma_f32_16x16x32_f16 v[122:125], v[154:157], v[150:153], v[122:125]
	s_cmp_eq_u32 s33, 16
	v_add_u32_e32 v241, 0x400, v241
	v_mfma_f32_16x16x32_f16 v[118:121], v[154:157], v[138:141], v[118:121]
	v_mfma_f32_16x16x32_f16 v[114:117], v[154:157], v[142:145], v[114:117]
	ds_read_b128 v[146:149], v186 offset:40960
	ds_read_b128 v[154:157], v186 offset:45056
	s_waitcnt lgkmcnt(2)
	v_mfma_f32_16x16x32_f16 v[106:109], v[162:165], v[158:161], v[106:109]
	v_mfma_f32_16x16x32_f16 v[98:101], v[162:165], v[150:153], v[98:101]
	v_mfma_f32_16x16x32_f16 v[90:93], v[162:165], v[138:141], v[90:93]
	v_mfma_f32_16x16x32_f16 v[82:85], v[162:165], v[142:145], v[82:85]
	s_waitcnt lgkmcnt(1)
	v_mfma_f32_16x16x32_f16 v[74:77], v[146:149], v[158:161], v[74:77]
	v_mfma_f32_16x16x32_f16 v[66:69], v[146:149], v[150:153], v[66:69]
	v_mfma_f32_16x16x32_f16 v[62:65], v[146:149], v[138:141], v[62:65]
	v_mfma_f32_16x16x32_f16 v[58:61], v[146:149], v[142:145], v[58:61]
	s_waitcnt lgkmcnt(0)
	v_mfma_f32_16x16x32_f16 v[54:57], v[154:157], v[158:161], v[54:57]
	v_mfma_f32_16x16x32_f16 v[50:53], v[154:157], v[150:153], v[50:53]
	v_mfma_f32_16x16x32_f16 v[46:49], v[154:157], v[138:141], v[46:49]
	v_mfma_f32_16x16x32_f16 v[42:45], v[154:157], v[142:145], v[42:45]
	s_cbranch_scc0 .LBB3_25
	v_or_b32_e32 v174, 0x4000, v195
	v_or_b32_e32 v175, 0x4000, v194
	s_mov_b32 s33, 0
	v_mov_b32_e32 v176, v175
	v_mov_b32_e32 v177, v174
	v_mov_b32_e32 v184, v179
.LBB3_27:
	v_add_u32_e32 v142, 0, v176
	ds_read_b128 v[138:141], v142
	ds_read_b128 v[142:145], v142 offset:2048
	s_waitcnt lgkmcnt(1)
	v_mfma_f32_16x16x32_f16 v[146:149], v[138:141], v[70:73], 0
	v_mfma_f32_16x16x32_f16 v[150:153], v[138:141], v[86:89], 0
	v_mfma_f32_16x16x32_f16 v[154:157], v[138:141], v[102:105], 0
	v_mfma_f32_16x16x32_f16 v[158:161], v[138:141], v[126:129], 0
	v_add_u32_e32 v138, 0, v177
	ds_read_b128 v[162:165], v138
	ds_read_b128 v[166:169], v138 offset:2048
	s_waitcnt lgkmcnt(1)
	v_mfma_f32_16x16x32_f16 v[242:245], v[162:165], v[78:81], v[146:149]
	v_mfma_f32_16x16x32_f16 v[138:141], v[162:165], v[94:97], v[150:153]
	v_mfma_f32_16x16x32_f16 v[146:149], v[162:165], v[110:113], v[154:157]
	v_mfma_f32_16x16x32_f16 v[162:165], v[162:165], v[134:137], v[158:161]
	v_mfma_f32_16x16x32_f16 v[150:153], v[142:145], v[70:73], 0
	v_mfma_f32_16x16x32_f16 v[154:157], v[142:145], v[86:89], 0
	v_mfma_f32_16x16x32_f16 v[158:161], v[142:145], v[102:105], 0
	v_mfma_f32_16x16x32_f16 v[246:249], v[142:145], v[126:129], 0
	s_waitcnt lgkmcnt(0)
	v_mfma_f32_16x16x32_f16 v[170:173], v[166:169], v[78:81], v[150:153]
	v_mfma_f32_16x16x32_f16 v[142:145], v[166:169], v[94:97], v[154:157]
	v_mfma_f32_16x16x32_f16 v[154:157], v[166:169], v[110:113], v[158:161]
	v_mfma_f32_16x16x32_f16 v[158:161], v[166:169], v[134:137], v[246:249]
	v_add_u32_e32 v185, 0, v184
	v_add_u32_e32 v150, 0x12600, v185
	ds_read_b128 v[150:153], v150
	v_add_u32_e32 v166, 0x12620, v185
	ds_read_b64 v[186:187], v166
	v_add_u32_e32 v166, 0x12610, v185
	ds_read_b128 v[166:169], v166
	s_waitcnt lgkmcnt(2)
	v_fma_f32 v241, v150, v162, v146
	v_fma_f32 v241, -v151, v163, v241
	v_fma_f32 v246, v150, v163, v147
	v_fmac_f32_e32 v246, v151, v162
	v_fma_f32 v247, v150, v241, v138
	v_fma_f32 v247, -v151, v246, v247
	v_fma_f32 v246, v150, v246, v139
	v_fmac_f32_e32 v246, v151, v241
	v_fma_f32 v241, v150, v247, v242
	v_fma_f32 v241, -v151, v246, v241
	v_fma_f32 v250, v150, v246, v243
	v_fmac_f32_e32 v250, v151, v247
	v_mov_b32_dpp v242, v241 row_shl:1 row_mask:0xf bank_mask:0xf bound_ctrl:1
	v_fmac_f32_e32 v241, v152, v242
	v_mov_b32_dpp v243, v250 row_shl:1 row_mask:0xf bank_mask:0xf bound_ctrl:1
	v_fma_f32 v241, -v153, v243, v241
	v_fmac_f32_e32 v250, v152, v243
	v_fmac_f32_e32 v250, v153, v242
	v_mov_b32_dpp v152, v241 row_shl:2 row_mask:0xf bank_mask:0xf bound_ctrl:1
	v_add_u32_e32 v242, 0x12660, v185
	v_mov_b32_dpp v153, v250 row_shl:2 row_mask:0xf bank_mask:0xf bound_ctrl:1
	ds_read_b64 v[242:243], v242
	s_waitcnt lgkmcnt(1)
	v_fmac_f32_e32 v241, v166, v152
	v_fma_f32 v241, -v167, v153, v241
	v_fmac_f32_e32 v250, v166, v153
	v_fmac_f32_e32 v250, v167, v152
	v_mov_b32_dpp v152, v241 row_shl:4 row_mask:0xf bank_mask:0xf bound_ctrl:1
	v_fmac_f32_e32 v241, v168, v152
	v_mov_b32_dpp v153, v250 row_shl:4 row_mask:0xf bank_mask:0xf bound_ctrl:1
	v_fma_f32 v166, -v169, v153, v241
	v_fmac_f32_e32 v250, v168, v153
	v_fmac_f32_e32 v250, v169, v152
	v_mov_b32_dpp v152, v166 row_shl:8 row_mask:0xf bank_mask:0xf bound_ctrl:1
	v_fmac_f32_e32 v166, v186, v152
	v_mov_b32_dpp v153, v250 row_shl:8 row_mask:0xf bank_mask:0xf bound_ctrl:1
	v_fma_f32 v241, -v187, v153, v166
	v_add_u32_e32 v166, 0x12640, v185
	v_add_u32_e32 v167, 0x12650, v185
	ds_read_b128 v[246:249], v167
	ds_read_b128 v[166:169], v166
	v_fmac_f32_e32 v250, v186, v153
	v_fmac_f32_e32 v250, v187, v152
	v_mov_b32_dpp v152, v241 row_shl:1 row_mask:0xf bank_mask:0xf bound_ctrl:1
	s_waitcnt lgkmcnt(0)
	v_fma_f32 v186, v166, v164, v148
	v_fma_f32 v186, -v167, v165, v186
	v_fma_f32 v187, v166, v165, v149
	v_fmac_f32_e32 v187, v167, v164
	v_fma_f32 v241, v166, v186, v140
	v_fma_f32 v241, -v167, v187, v241
	v_fma_f32 v187, v166, v187, v141
	v_fmac_f32_e32 v187, v167, v186
	v_fma_f32 v186, v166, v241, v244
	v_fma_f32 v186, -v167, v187, v186
	v_fmac_f32_e32 v245, v166, v187
	v_fmac_f32_e32 v245, v167, v241
	v_mov_b32_dpp v187, v186 row_shl:1 row_mask:0xf bank_mask:0xf bound_ctrl:1
	v_fmac_f32_e32 v186, v168, v187
	v_mov_b32_dpp v241, v245 row_shl:1 row_mask:0xf bank_mask:0xf bound_ctrl:1
	v_fma_f32 v186, -v169, v241, v186
	v_fmac_f32_e32 v245, v168, v241
	v_fmac_f32_e32 v245, v169, v187
	v_mov_b32_dpp v168, v186 row_shl:2 row_mask:0xf bank_mask:0xf bound_ctrl:1
	v_fmac_f32_e32 v186, v246, v168
	v_mov_b32_dpp v169, v245 row_shl:2 row_mask:0xf bank_mask:0xf bound_ctrl:1
	v_fma_f32 v186, -v247, v169, v186
	v_fmac_f32_e32 v245, v246, v169
	v_fmac_f32_e32 v245, v247, v168
	v_mov_b32_dpp v168, v186 row_shl:4 row_mask:0xf bank_mask:0xf bound_ctrl:1
	v_fmac_f32_e32 v186, v248, v168
	v_mov_b32_dpp v169, v245 row_shl:4 row_mask:0xf bank_mask:0xf bound_ctrl:1
	v_fma_f32 v186, -v249, v169, v186
	v_fmac_f32_e32 v245, v248, v169
	v_fmac_f32_e32 v245, v249, v168
	v_mov_b32_dpp v168, v186 row_shl:8 row_mask:0xf bank_mask:0xf bound_ctrl:1
	v_fmac_f32_e32 v186, v242, v168
	v_mov_b32_dpp v169, v245 row_shl:8 row_mask:0xf bank_mask:0xf bound_ctrl:1
	v_fma_f32 v241, -v243, v169, v186
	v_fmac_f32_e32 v245, v242, v169
	v_add_u32_e32 v169, 0x12820, v185
	v_fmac_f32_e32 v245, v243, v168
	v_add_u32_e32 v168, 0x12800, v185
	ds_read_b64 v[186:187], v169
	ds_read_b128 v[246:249], v168
	v_mov_b32_dpp v168, v241 row_shl:1 row_mask:0xf bank_mask:0xf bound_ctrl:1
	v_add_u32_e32 v241, 0x12810, v185
	v_mov_b32_dpp v169, v245 row_shl:1 row_mask:0xf bank_mask:0xf bound_ctrl:1
	ds_read_b128 v[242:245], v241
	s_waitcnt lgkmcnt(1)
	v_fma_f32 v241, v246, v158, v154
	v_mov_b32_dpp v153, v250 row_shl:1 row_mask:0xf bank_mask:0xf bound_ctrl:1
	v_fma_f32 v241, -v247, v159, v241
	v_fma_f32 v250, v246, v159, v155
	v_fmac_f32_e32 v250, v247, v158
	v_fma_f32 v251, v246, v241, v142
	v_fma_f32 v251, -v247, v250, v251
	v_fma_f32 v250, v246, v250, v143
	v_fmac_f32_e32 v250, v247, v241
	v_fma_f32 v170, v246, v251, v170
	v_fma_f32 v170, -v247, v250, v170
	v_fma_f32 v241, v246, v250, v171
	v_fmac_f32_e32 v241, v247, v251
	v_mov_b32_dpp v171, v170 row_shl:1 row_mask:0xf bank_mask:0xf bound_ctrl:1
	v_fmac_f32_e32 v170, v248, v171
	v_mov_b32_dpp v250, v241 row_shl:1 row_mask:0xf bank_mask:0xf bound_ctrl:1
	v_fma_f32 v251, -v249, v250, v170
	v_fmac_f32_e32 v241, v248, v250
	v_fmac_f32_e32 v241, v249, v171
	v_mov_b32_dpp v248, v251 row_shl:2 row_mask:0xf bank_mask:0xf bound_ctrl:1
	s_waitcnt lgkmcnt(0)
	v_fmac_f32_e32 v251, v242, v248
	v_mov_b32_dpp v249, v241 row_shl:2 row_mask:0xf bank_mask:0xf bound_ctrl:1
	v_fma_f32 v250, -v243, v249, v251
	v_fmac_f32_e32 v241, v242, v249
	v_fmac_f32_e32 v241, v243, v248
	v_mov_b32_dpp v242, v250 row_shl:4 row_mask:0xf bank_mask:0xf bound_ctrl:1
	v_fmac_f32_e32 v250, v244, v242
	v_mov_b32_dpp v243, v241 row_shl:4 row_mask:0xf bank_mask:0xf bound_ctrl:1
	v_fma_f32 v248, -v245, v243, v250
	v_fmac_f32_e32 v241, v244, v243
	v_fmac_f32_e32 v241, v245, v242
	v_mov_b32_dpp v252, v248 row_shl:8 row_mask:0xf bank_mask:0xf bound_ctrl:1
	v_fmac_f32_e32 v248, v186, v252
	v_mov_b32_dpp v253, v241 row_shl:8 row_mask:0xf bank_mask:0xf bound_ctrl:1
	v_add_u32_e32 v170, 0x12860, v185
	v_fma_f32 v254, -v187, v253, v248
	v_add_u32_e32 v248, 0x12840, v185
	v_add_u32_e32 v185, 0x12850, v185
	ds_read_b64 v[170:171], v170
	ds_read_b128 v[242:245], v185
	ds_read_b128 v[248:251], v248
	v_fmac_f32_e32 v241, v186, v253
	v_fmac_f32_e32 v241, v187, v252
	v_mov_b32_dpp v186, v254 row_shl:1 row_mask:0xf bank_mask:0xf bound_ctrl:1
	s_waitcnt lgkmcnt(0)
	v_fma_f32 v185, v248, v160, v156
	v_mov_b32_dpp v187, v241 row_shl:1 row_mask:0xf bank_mask:0xf bound_ctrl:1
	v_fma_f32 v185, -v249, v161, v185
	v_fma_f32 v241, v248, v161, v157
	v_fmac_f32_e32 v241, v249, v160
	v_fma_f32 v252, v248, v185, v144
	v_fma_f32 v252, -v249, v241, v252
	v_fma_f32 v241, v248, v241, v145
	v_fmac_f32_e32 v241, v249, v185
	v_fma_f32 v172, v248, v252, v172
	v_fmac_f32_e32 v173, v248, v241
	v_fma_f32 v172, -v249, v241, v172
	v_fmac_f32_e32 v173, v249, v252
	s_nop 0
	v_mov_b32_dpp v185, v172 row_shl:1 row_mask:0xf bank_mask:0xf bound_ctrl:1
	v_mov_b32_dpp v241, v173 row_shl:1 row_mask:0xf bank_mask:0xf bound_ctrl:1
	v_fmac_f32_e32 v172, v250, v185
	v_fmac_f32_e32 v173, v250, v241
	v_fma_f32 v172, -v251, v241, v172
	v_fmac_f32_e32 v173, v251, v185
	s_nop 0
	v_mov_b32_dpp v185, v172 row_shl:2 row_mask:0xf bank_mask:0xf bound_ctrl:1
	v_mov_b32_dpp v241, v173 row_shl:2 row_mask:0xf bank_mask:0xf bound_ctrl:1
	v_fmac_f32_e32 v172, v242, v185
	v_fmac_f32_e32 v173, v242, v241
	v_fma_f32 v172, -v243, v241, v172
	v_fmac_f32_e32 v173, v243, v185
	s_nop 0
	v_mov_b32_dpp v185, v172 row_shl:4 row_mask:0xf bank_mask:0xf bound_ctrl:1
	v_mov_b32_dpp v241, v173 row_shl:4 row_mask:0xf bank_mask:0xf bound_ctrl:1
	v_fmac_f32_e32 v172, v244, v185
	v_fmac_f32_e32 v173, v244, v241
	v_fma_f32 v172, -v245, v241, v172
	v_fmac_f32_e32 v173, v245, v185
	s_nop 0
	v_mov_b32_dpp v185, v172 row_shl:8 row_mask:0xf bank_mask:0xf bound_ctrl:1
	v_mov_b32_dpp v241, v173 row_shl:8 row_mask:0xf bank_mask:0xf bound_ctrl:1
	v_fmac_f32_e32 v172, v170, v185
	v_fmac_f32_e32 v173, v170, v241
	v_fma_f32 v172, -v171, v241, v172
	v_fmac_f32_e32 v173, v171, v185
	s_nop 0
	v_mov_b32_dpp v170, v172 row_shl:1 row_mask:0xf bank_mask:0xf bound_ctrl:1
	v_mov_b32_dpp v171, v173 row_shl:1 row_mask:0xf bank_mask:0xf bound_ctrl:1
	v_pk_fma_f32 v[172:173], v[150:151], v[152:153], v[162:163] op_sel_hi:[0,1,1]
	v_pk_fma_f32 v[158:159], v[246:247], v[186:187], v[158:159] op_sel_hi:[0,1,1]
	v_pk_fma_f32 v[160:161], v[248:249], v[170:171], v[160:161] op_sel_hi:[0,1,1]
	v_add_u32_e32 v163, s33, v189
	v_cvt_pk_f16_f32 v162, v152, v153
	v_pk_fma_f32 v[164:165], v[166:167], v[168:169], v[164:165] op_sel_hi:[0,1,1]
	v_pk_fma_f32 v[152:153], v[150:151], v[152:153], v[172:173] op_sel:[1,1,0] op_sel_hi:[1,0,1] neg_lo:[1,0,0]
	v_pk_fma_f32 v[172:173], v[246:247], v[186:187], v[158:159] op_sel:[1,1,0] op_sel_hi:[1,0,1] neg_lo:[1,0,0]
	v_pk_fma_f32 v[160:161], v[248:249], v[170:171], v[160:161] op_sel:[1,1,0] op_sel_hi:[1,0,1] neg_lo:[1,0,0]
	v_xor_b32_e32 v163, v163, v188
	v_pk_fma_f32 v[164:165], v[166:167], v[168:169], v[164:165] op_sel:[1,1,0] op_sel_hi:[1,0,1] neg_lo:[1,0,0]
	v_pk_fma_f32 v[158:159], v[150:151], v[152:153], v[146:147] op_sel_hi:[0,1,1]
	v_pk_fma_f32 v[154:155], v[246:247], v[172:173], v[154:155] op_sel_hi:[0,1,1]
	v_pk_fma_f32 v[156:157], v[248:249], v[160:161], v[156:157] op_sel_hi:[0,1,1]
	v_lshl_add_u32 v185, v163, 4, v190
	v_cvt_pk_f16_f32 v146, v152, v153
	v_pk_fma_f32 v[148:149], v[166:167], v[164:165], v[148:149] op_sel_hi:[0,1,1]
	v_pk_fma_f32 v[242:243], v[150:151], v[152:153], v[158:159] op_sel:[1,1,0] op_sel_hi:[1,0,1] neg_lo:[1,0,0]
	v_pk_fma_f32 v[244:245], v[246:247], v[172:173], v[154:155] op_sel:[1,1,0] op_sel_hi:[1,0,1] neg_lo:[1,0,0]
	v_pk_fma_f32 v[250:251], v[248:249], v[160:161], v[156:157] op_sel:[1,1,0] op_sel_hi:[1,0,1] neg_lo:[1,0,0]
	ds_read_b128 v[152:155], v185 offset:49152
	ds_read_b128 v[156:159], v185 offset:53248
	v_pk_fma_f32 v[148:149], v[166:167], v[164:165], v[148:149] op_sel:[1,1,0] op_sel_hi:[1,0,1] neg_lo:[1,0,0]
	v_pk_fma_f32 v[252:253], v[150:151], v[242:243], v[138:139] op_sel_hi:[0,1,1]
	v_pk_fma_f32 v[142:143], v[246:247], v[244:245], v[142:143] op_sel_hi:[0,1,1]
	v_pk_fma_f32 v[140:141], v[166:167], v[148:149], v[140:141] op_sel_hi:[0,1,1]
	v_pk_fma_f32 v[144:145], v[248:249], v[250:251], v[144:145] op_sel_hi:[0,1,1]
	v_cvt_pk_f16_f32 v138, v242, v243
	v_pk_fma_f32 v[150:151], v[150:151], v[242:243], v[252:253] op_sel:[1,1,0] op_sel_hi:[1,0,1] neg_lo:[1,0,0]
	v_pk_fma_f32 v[242:243], v[246:247], v[244:245], v[142:143] op_sel:[1,1,0] op_sel_hi:[1,0,1] neg_lo:[1,0,0]
	v_pk_fma_f32 v[140:141], v[166:167], v[148:149], v[140:141] op_sel:[1,1,0] op_sel_hi:[1,0,1] neg_lo:[1,0,0]
	v_pk_fma_f32 v[166:167], v[248:249], v[250:251], v[144:145] op_sel:[1,1,0] op_sel_hi:[1,0,1] neg_lo:[1,0,0]
	v_cvt_pk_f16_f32 v142, v150, v151
	v_cvt_pk_f16_f32 v144, v242, v243
	v_cvt_pk_f16_f32 v143, v140, v141
	v_cvt_pk_f16_f32 v145, v166, v167
	v_cvt_pk_f16_f32 v140, v244, v245
	v_cvt_pk_f16_f32 v139, v148, v149
	v_cvt_pk_f16_f32 v141, v250, v251
	v_cvt_pk_f16_f32 v148, v172, v173
	v_cvt_pk_f16_f32 v147, v164, v165
	v_cvt_pk_f16_f32 v149, v160, v161
	v_cvt_pk_f16_f32 v164, v186, v187
	v_cvt_pk_f16_f32 v163, v168, v169
	v_cvt_pk_f16_f32 v165, v170, v171
	s_waitcnt lgkmcnt(1)
	v_mfma_f32_16x16x32_f16 v[130:133], v[152:155], v[142:145], v[130:133]
	s_add_i32 s33, s33, 4
	v_add_u32_e32 v184, 0x400, v184
	v_add_u32_e32 v177, 0x1000, v177
	v_mfma_f32_16x16x32_f16 v[122:125], v[152:155], v[138:141], v[122:125]
	s_cmp_lg_u32 s33, 16
	v_add_u32_e32 v176, 0x1000, v176
	v_mfma_f32_16x16x32_f16 v[118:121], v[152:155], v[146:149], v[118:121]
	v_mfma_f32_16x16x32_f16 v[114:117], v[152:155], v[162:165], v[114:117]
	s_waitcnt lgkmcnt(0)
	v_mfma_f32_16x16x32_f16 v[106:109], v[156:159], v[142:145], v[106:109]
	v_mfma_f32_16x16x32_f16 v[98:101], v[156:159], v[138:141], v[98:101]
	v_mfma_f32_16x16x32_f16 v[90:93], v[156:159], v[146:149], v[90:93]
	v_mfma_f32_16x16x32_f16 v[82:85], v[156:159], v[162:165], v[82:85]
	ds_read_b128 v[150:153], v185 offset:57344
	ds_read_b128 v[154:157], v185 offset:61440
	s_waitcnt lgkmcnt(1)
	v_mfma_f32_16x16x32_f16 v[74:77], v[150:153], v[142:145], v[74:77]
	v_mfma_f32_16x16x32_f16 v[66:69], v[150:153], v[138:141], v[66:69]
	v_mfma_f32_16x16x32_f16 v[62:65], v[150:153], v[146:149], v[62:65]
	v_mfma_f32_16x16x32_f16 v[58:61], v[150:153], v[162:165], v[58:61]
	s_waitcnt lgkmcnt(0)
	v_mfma_f32_16x16x32_f16 v[54:57], v[154:157], v[142:145], v[54:57]
	v_mfma_f32_16x16x32_f16 v[50:53], v[154:157], v[138:141], v[50:53]
	v_mfma_f32_16x16x32_f16 v[46:49], v[154:157], v[146:149], v[46:49]
	v_mfma_f32_16x16x32_f16 v[42:45], v[154:157], v[162:165], v[42:45]
	s_cbranch_scc1 .LBB3_27
	s_load_dwordx2 s[0:1], s[0:1], 0x38
	v_lshlrev_b32_e32 v136, 22, v239
	v_mov_b32_e32 v137, 0
	s_waitcnt lgkmcnt(0)
	v_lshl_add_u64 v[70:71], s[0:1], 0, v[136:137]
	v_lshlrev_b32_e32 v136, 1, v240
	v_lshl_add_u64 v[138:139], v[70:71], 0, v[136:137]
	s_lshl_b64 s[0:1], s[48:49], 13
	v_lshl_add_u64 v[72:73], v[138:139], 0, s[0:1]
	s_mov_b32 s1, 0x3f3504f3
	v_mul_f32_e64 v70, |v130|, s1
	s_mov_b32 s33, 0x3ea7ba05
	v_fma_f32 v71, v70, s33, 1.0
	v_rcp_f32_e32 v78, v71
	v_mul_f32_e32 v71, 0xbfb8aa3b, v70
	v_mul_f32_e32 v70, v70, v71
	v_exp_f32_e32 v80, v70
	v_mul_f32_e64 v70, |v131|, s1
	v_fma_f32 v71, v70, s33, 1.0
	v_rcp_f32_e32 v79, v71
	v_mul_f32_e32 v71, 0xbfb8aa3b, v70
	v_mul_f32_e32 v70, v70, v71
	s_mov_b32 s48, 0xbfba00e3
	v_exp_f32_e32 v81, v70
	s_mov_b32 s0, 0x3f87dc22
	v_mov_b64_e32 v[70:71], s[48:49]
	v_pk_fma_f32 v[86:87], v[78:79], s[0:1], v[70:71] op_sel_hi:[1,0,0]
	s_mov_b32 s48, 0x3fb5f0e3
	v_pk_fma_f32 v[86:87], v[78:79], v[86:87], s[48:49] op_sel_hi:[1,1,0]
	s_mov_b32 s50, 0xbe91a98e
	v_pk_fma_f32 v[86:87], v[78:79], v[86:87], s[50:51] op_sel_hi:[1,1,0]
	s_mov_b32 s52, 0x3e827906
	v_pk_fma_f32 v[86:87], v[78:79], v[86:87], s[52:53] op_sel_hi:[1,1,0]
	v_cmp_le_f32_e32 vcc, 0, v131
	v_pk_mul_f32 v[78:79], v[78:79], v[86:87]
	v_lshlrev_b32_e32 v136, 1, v238
	v_pk_mul_f32 v[78:79], v[78:79], 0.5 op_sel_hi:[1,0]
	v_lshl_add_u64 v[72:73], v[72:73], 0, v[136:137]
	v_pk_mul_f32 v[78:79], v[80:81], v[78:79]
	s_nop 0
	v_pk_mul_f32 v[80:81], v[130:131], v[78:79]
	v_pk_fma_f32 v[78:79], v[130:131], v[78:79], v[130:131] neg_lo:[1,0,0] neg_hi:[1,0,0]
	s_nop 0
	v_cndmask_b32_e32 v79, v81, v79, vcc
	v_cmp_le_f32_e32 vcc, 0, v130
	s_nop 1
	v_cndmask_b32_e32 v78, v80, v78, vcc
	v_cvt_pk_f16_f32 v78, v78, v79
	v_mul_f32_e64 v79, |v132|, s1
	v_mul_f32_e32 v81, 0xbfb8aa3b, v79
	v_fma_f32 v80, v79, s33, 1.0
	v_mul_f32_e32 v79, v79, v81
	v_exp_f32_e32 v86, v79
	v_mul_f32_e64 v79, |v133|, s1
	v_fma_f32 v81, v79, s33, 1.0
	v_rcp_f32_e32 v80, v80
	v_rcp_f32_e32 v81, v81
	v_mul_f32_e32 v87, 0xbfb8aa3b, v79
	v_mul_f32_e32 v79, v79, v87
	v_exp_f32_e32 v87, v79
	v_pk_fma_f32 v[88:89], v[80:81], s[0:1], v[70:71] op_sel_hi:[1,0,0]
	v_cmp_le_f32_e32 vcc, 0, v133
	v_pk_fma_f32 v[88:89], v[80:81], v[88:89], s[48:49] op_sel_hi:[1,1,0]
	s_nop 0
	v_pk_fma_f32 v[88:89], v[80:81], v[88:89], s[50:51] op_sel_hi:[1,1,0]
	s_nop 0
	v_pk_fma_f32 v[88:89], v[80:81], v[88:89], s[52:53] op_sel_hi:[1,1,0]
	s_nop 0
	v_pk_mul_f32 v[80:81], v[80:81], v[88:89]
	s_nop 0
	v_pk_mul_f32 v[80:81], v[80:81], 0.5 op_sel_hi:[1,0]
	s_nop 0
	v_pk_mul_f32 v[80:81], v[86:87], v[80:81]
	s_nop 0
	v_pk_mul_f32 v[86:87], v[132:133], v[80:81]
	v_pk_fma_f32 v[80:81], v[132:133], v[80:81], v[132:133] neg_lo:[1,0,0] neg_hi:[1,0,0]
	s_nop 0
	v_cndmask_b32_e32 v79, v87, v81, vcc
	v_cmp_le_f32_e32 vcc, 0, v132
	v_mul_f32_e64 v81, |v123|, s1
	s_nop 0
	v_cndmask_b32_e32 v80, v86, v80, vcc
	v_cvt_pk_f16_f32 v79, v80, v79
	global_store_dwordx2 v[72:73], v[78:79], off
	v_mul_f32_e64 v79, |v122|, s1
	v_mul_f32_e32 v80, 0xbfb8aa3b, v79
	v_fma_f32 v78, v79, s33, 1.0
	v_mul_f32_e32 v79, v79, v80
	v_exp_f32_e32 v80, v79
	v_fma_f32 v79, v81, s33, 1.0
	v_rcp_f32_e32 v78, v78
	v_rcp_f32_e32 v79, v79
	v_mul_f32_e32 v86, 0xbfb8aa3b, v81
	v_mul_f32_e32 v81, v81, v86
	v_exp_f32_e32 v81, v81
	v_pk_fma_f32 v[86:87], v[78:79], s[0:1], v[70:71] op_sel_hi:[1,0,0]
	v_cmp_le_f32_e32 vcc, 0, v123
	v_pk_fma_f32 v[86:87], v[78:79], v[86:87], s[48:49] op_sel_hi:[1,1,0]
	s_nop 0
	v_pk_fma_f32 v[86:87], v[78:79], v[86:87], s[50:51] op_sel_hi:[1,1,0]
	s_nop 0
	v_pk_fma_f32 v[86:87], v[78:79], v[86:87], s[52:53] op_sel_hi:[1,1,0]
	s_nop 0
	v_pk_mul_f32 v[78:79], v[78:79], v[86:87]
	s_nop 0
	v_pk_mul_f32 v[78:79], v[78:79], 0.5 op_sel_hi:[1,0]
	s_nop 0
	v_pk_mul_f32 v[78:79], v[80:81], v[78:79]
	s_nop 0
	v_pk_mul_f32 v[80:81], v[122:123], v[78:79]
	v_pk_fma_f32 v[78:79], v[122:123], v[78:79], v[122:123] neg_lo:[1,0,0] neg_hi:[1,0,0]
	s_nop 0
	v_cndmask_b32_e32 v79, v81, v79, vcc
	v_cmp_le_f32_e32 vcc, 0, v122
	s_nop 1
	v_cndmask_b32_e32 v78, v80, v78, vcc
	v_cvt_pk_f16_f32 v78, v78, v79
	v_mul_f32_e64 v79, |v124|, s1
	v_mul_f32_e32 v81, 0xbfb8aa3b, v79
	v_fma_f32 v80, v79, s33, 1.0
	v_mul_f32_e32 v79, v79, v81
	v_exp_f32_e32 v86, v79
	v_mul_f32_e64 v79, |v125|, s1
	v_fma_f32 v81, v79, s33, 1.0
	v_rcp_f32_e32 v80, v80
	v_rcp_f32_e32 v81, v81
	v_mul_f32_e32 v87, 0xbfb8aa3b, v79
	v_mul_f32_e32 v79, v79, v87
	v_exp_f32_e32 v87, v79
	v_pk_fma_f32 v[88:89], v[80:81], s[0:1], v[70:71] op_sel_hi:[1,0,0]
	v_cmp_le_f32_e32 vcc, 0, v125
	v_pk_fma_f32 v[88:89], v[80:81], v[88:89], s[48:49] op_sel_hi:[1,1,0]
	s_nop 0
	v_pk_fma_f32 v[88:89], v[80:81], v[88:89], s[50:51] op_sel_hi:[1,1,0]
	s_nop 0
	v_pk_fma_f32 v[88:89], v[80:81], v[88:89], s[52:53] op_sel_hi:[1,1,0]
	s_nop 0
	v_pk_mul_f32 v[80:81], v[80:81], v[88:89]
	s_nop 0
	v_pk_mul_f32 v[80:81], v[80:81], 0.5 op_sel_hi:[1,0]
	s_nop 0
	v_pk_mul_f32 v[80:81], v[86:87], v[80:81]
	s_nop 0
	v_pk_mul_f32 v[86:87], v[124:125], v[80:81]
	v_pk_fma_f32 v[80:81], v[124:125], v[80:81], v[124:125] neg_lo:[1,0,0] neg_hi:[1,0,0]
	s_nop 0
	v_cndmask_b32_e32 v79, v87, v81, vcc
	v_cmp_le_f32_e32 vcc, 0, v124
	v_mul_f32_e64 v81, |v119|, s1
	s_nop 0
	v_cndmask_b32_e32 v80, v86, v80, vcc
	v_cvt_pk_f16_f32 v79, v80, v79
	global_store_dwordx2 v[72:73], v[78:79], off offset:128
	v_mul_f32_e64 v79, |v118|, s1
	v_mul_f32_e32 v80, 0xbfb8aa3b, v79
	v_fma_f32 v78, v79, s33, 1.0
	v_mul_f32_e32 v79, v79, v80
	v_exp_f32_e32 v80, v79
	v_fma_f32 v79, v81, s33, 1.0
	v_rcp_f32_e32 v78, v78
	v_rcp_f32_e32 v79, v79
	v_mul_f32_e32 v86, 0xbfb8aa3b, v81
	v_mul_f32_e32 v81, v81, v86
	v_exp_f32_e32 v81, v81
	v_pk_fma_f32 v[86:87], v[78:79], s[0:1], v[70:71] op_sel_hi:[1,0,0]
	v_cmp_le_f32_e32 vcc, 0, v119
	v_pk_fma_f32 v[86:87], v[78:79], v[86:87], s[48:49] op_sel_hi:[1,1,0]
	s_nop 0
	v_pk_fma_f32 v[86:87], v[78:79], v[86:87], s[50:51] op_sel_hi:[1,1,0]
	s_nop 0
	v_pk_fma_f32 v[86:87], v[78:79], v[86:87], s[52:53] op_sel_hi:[1,1,0]
	s_nop 0
	v_pk_mul_f32 v[78:79], v[78:79], v[86:87]
	s_nop 0
	v_pk_mul_f32 v[78:79], v[78:79], 0.5 op_sel_hi:[1,0]
	s_nop 0
	v_pk_mul_f32 v[78:79], v[80:81], v[78:79]
	s_nop 0
	v_pk_mul_f32 v[80:81], v[118:119], v[78:79]
	v_pk_fma_f32 v[78:79], v[118:119], v[78:79], v[118:119] neg_lo:[1,0,0] neg_hi:[1,0,0]
	s_nop 0
	v_cndmask_b32_e32 v79, v81, v79, vcc
	v_cmp_le_f32_e32 vcc, 0, v118
	s_nop 1
	v_cndmask_b32_e32 v78, v80, v78, vcc
	v_cvt_pk_f16_f32 v78, v78, v79
	v_mul_f32_e64 v79, |v120|, s1
	v_mul_f32_e32 v81, 0xbfb8aa3b, v79
	v_fma_f32 v80, v79, s33, 1.0
	v_mul_f32_e32 v79, v79, v81
	v_exp_f32_e32 v86, v79
	v_mul_f32_e64 v79, |v121|, s1
	v_fma_f32 v81, v79, s33, 1.0
	v_rcp_f32_e32 v80, v80
	v_rcp_f32_e32 v81, v81
	v_mul_f32_e32 v87, 0xbfb8aa3b, v79
	v_mul_f32_e32 v79, v79, v87
	v_exp_f32_e32 v87, v79
	v_pk_fma_f32 v[88:89], v[80:81], s[0:1], v[70:71] op_sel_hi:[1,0,0]
	v_cmp_le_f32_e32 vcc, 0, v121
	v_pk_fma_f32 v[88:89], v[80:81], v[88:89], s[48:49] op_sel_hi:[1,1,0]
	s_nop 0
	v_pk_fma_f32 v[88:89], v[80:81], v[88:89], s[50:51] op_sel_hi:[1,1,0]
	s_nop 0
	v_pk_fma_f32 v[88:89], v[80:81], v[88:89], s[52:53] op_sel_hi:[1,1,0]
	s_nop 0
	v_pk_mul_f32 v[80:81], v[80:81], v[88:89]
	s_nop 0
	v_pk_mul_f32 v[80:81], v[80:81], 0.5 op_sel_hi:[1,0]
	s_nop 0
	v_pk_mul_f32 v[80:81], v[86:87], v[80:81]
	s_nop 0
	v_pk_mul_f32 v[86:87], v[120:121], v[80:81]
	v_pk_fma_f32 v[80:81], v[120:121], v[80:81], v[120:121] neg_lo:[1,0,0] neg_hi:[1,0,0]
	s_nop 0
	v_cndmask_b32_e32 v79, v87, v81, vcc
	v_cmp_le_f32_e32 vcc, 0, v120
	v_mul_f32_e64 v81, |v115|, s1
	s_nop 0
	v_cndmask_b32_e32 v80, v86, v80, vcc
	v_cvt_pk_f16_f32 v79, v80, v79
	global_store_dwordx2 v[72:73], v[78:79], off offset:256
	v_mul_f32_e64 v79, |v114|, s1
	v_mul_f32_e32 v80, 0xbfb8aa3b, v79
	v_fma_f32 v78, v79, s33, 1.0
	v_mul_f32_e32 v79, v79, v80
	v_exp_f32_e32 v80, v79
	v_fma_f32 v79, v81, s33, 1.0
	v_rcp_f32_e32 v78, v78
	v_rcp_f32_e32 v79, v79
	v_mul_f32_e32 v86, 0xbfb8aa3b, v81
	v_mul_f32_e32 v81, v81, v86
	v_exp_f32_e32 v81, v81
	v_pk_fma_f32 v[86:87], v[78:79], s[0:1], v[70:71] op_sel_hi:[1,0,0]
	v_cmp_le_f32_e32 vcc, 0, v115
	v_pk_fma_f32 v[86:87], v[78:79], v[86:87], s[48:49] op_sel_hi:[1,1,0]
	s_nop 0
	v_pk_fma_f32 v[86:87], v[78:79], v[86:87], s[50:51] op_sel_hi:[1,1,0]
	s_nop 0
	v_pk_fma_f32 v[86:87], v[78:79], v[86:87], s[52:53] op_sel_hi:[1,1,0]
	s_nop 0
	v_pk_mul_f32 v[78:79], v[78:79], v[86:87]
	s_nop 0
	v_pk_mul_f32 v[78:79], v[78:79], 0.5 op_sel_hi:[1,0]
	s_nop 0
	v_pk_mul_f32 v[78:79], v[80:81], v[78:79]
	s_nop 0
	v_pk_mul_f32 v[80:81], v[114:115], v[78:79]
	v_pk_fma_f32 v[78:79], v[114:115], v[78:79], v[114:115] neg_lo:[1,0,0] neg_hi:[1,0,0]
	s_nop 0
	v_cndmask_b32_e32 v79, v81, v79, vcc
	v_cmp_le_f32_e32 vcc, 0, v114
	s_nop 1
	v_cndmask_b32_e32 v78, v80, v78, vcc
	v_cvt_pk_f16_f32 v78, v78, v79
	v_mul_f32_e64 v79, |v116|, s1
	v_mul_f32_e32 v81, 0xbfb8aa3b, v79
	v_fma_f32 v80, v79, s33, 1.0
	v_mul_f32_e32 v79, v79, v81
	v_exp_f32_e32 v86, v79
	v_mul_f32_e64 v79, |v117|, s1
	v_fma_f32 v81, v79, s33, 1.0
	v_rcp_f32_e32 v80, v80
	v_rcp_f32_e32 v81, v81
	v_mul_f32_e32 v87, 0xbfb8aa3b, v79
	v_mul_f32_e32 v79, v79, v87
	v_exp_f32_e32 v87, v79
	v_pk_fma_f32 v[88:89], v[80:81], s[0:1], v[70:71] op_sel_hi:[1,0,0]
	v_cmp_le_f32_e32 vcc, 0, v117
	v_pk_fma_f32 v[88:89], v[80:81], v[88:89], s[48:49] op_sel_hi:[1,1,0]
	s_nop 0
	v_pk_fma_f32 v[88:89], v[80:81], v[88:89], s[50:51] op_sel_hi:[1,1,0]
	s_nop 0
	v_pk_fma_f32 v[88:89], v[80:81], v[88:89], s[52:53] op_sel_hi:[1,1,0]
	s_nop 0
	v_pk_mul_f32 v[80:81], v[80:81], v[88:89]
	s_nop 0
	v_pk_mul_f32 v[80:81], v[80:81], 0.5 op_sel_hi:[1,0]
	s_nop 0
	v_pk_mul_f32 v[80:81], v[86:87], v[80:81]
	s_nop 0
	v_pk_mul_f32 v[86:87], v[116:117], v[80:81]
	v_pk_fma_f32 v[80:81], v[116:117], v[80:81], v[116:117] neg_lo:[1,0,0] neg_hi:[1,0,0]
	s_nop 0
	v_cndmask_b32_e32 v79, v87, v81, vcc
	v_cmp_le_f32_e32 vcc, 0, v116
	v_mul_f32_e64 v81, |v107|, s1
	s_nop 0
	v_cndmask_b32_e32 v80, v86, v80, vcc
	v_cvt_pk_f16_f32 v79, v80, v79
	global_store_dwordx2 v[72:73], v[78:79], off offset:384
	v_mul_f32_e64 v79, |v106|, s1
	v_mul_f32_e32 v80, 0xbfb8aa3b, v79
	v_fma_f32 v78, v79, s33, 1.0
	v_mul_f32_e32 v79, v79, v80
	v_exp_f32_e32 v80, v79
	v_fma_f32 v79, v81, s33, 1.0
	v_rcp_f32_e32 v78, v78
	v_rcp_f32_e32 v79, v79
	v_mul_f32_e32 v86, 0xbfb8aa3b, v81
	v_mul_f32_e32 v81, v81, v86
	v_exp_f32_e32 v81, v81
	v_pk_fma_f32 v[86:87], v[78:79], s[0:1], v[70:71] op_sel_hi:[1,0,0]
	v_cmp_le_f32_e32 vcc, 0, v107
	v_pk_fma_f32 v[86:87], v[78:79], v[86:87], s[48:49] op_sel_hi:[1,1,0]
	s_nop 0
	v_pk_fma_f32 v[86:87], v[78:79], v[86:87], s[50:51] op_sel_hi:[1,1,0]
	s_nop 0
	v_pk_fma_f32 v[86:87], v[78:79], v[86:87], s[52:53] op_sel_hi:[1,1,0]
	s_nop 0
	v_pk_mul_f32 v[78:79], v[78:79], v[86:87]
	s_nop 0
	v_pk_mul_f32 v[78:79], v[78:79], 0.5 op_sel_hi:[1,0]
	s_nop 0
	v_pk_mul_f32 v[78:79], v[80:81], v[78:79]
	s_nop 0
	v_pk_mul_f32 v[80:81], v[106:107], v[78:79]
	v_pk_fma_f32 v[78:79], v[106:107], v[78:79], v[106:107] neg_lo:[1,0,0] neg_hi:[1,0,0]
	s_nop 0
	v_cndmask_b32_e32 v79, v81, v79, vcc
	v_cmp_le_f32_e32 vcc, 0, v106
	s_nop 1
	v_cndmask_b32_e32 v78, v80, v78, vcc
	v_cvt_pk_f16_f32 v78, v78, v79
	v_mul_f32_e64 v79, |v108|, s1
	v_mul_f32_e32 v81, 0xbfb8aa3b, v79
	v_fma_f32 v80, v79, s33, 1.0
	v_mul_f32_e32 v79, v79, v81
	v_exp_f32_e32 v86, v79
	v_mul_f32_e64 v79, |v109|, s1
	v_fma_f32 v81, v79, s33, 1.0
	v_rcp_f32_e32 v80, v80
	v_rcp_f32_e32 v81, v81
	v_mul_f32_e32 v87, 0xbfb8aa3b, v79
	v_mul_f32_e32 v79, v79, v87
	v_exp_f32_e32 v87, v79
	v_pk_fma_f32 v[88:89], v[80:81], s[0:1], v[70:71] op_sel_hi:[1,0,0]
	v_cmp_le_f32_e32 vcc, 0, v109
	v_pk_fma_f32 v[88:89], v[80:81], v[88:89], s[48:49] op_sel_hi:[1,1,0]
	s_nop 0
	v_pk_fma_f32 v[88:89], v[80:81], v[88:89], s[50:51] op_sel_hi:[1,1,0]
	s_nop 0
	v_pk_fma_f32 v[88:89], v[80:81], v[88:89], s[52:53] op_sel_hi:[1,1,0]
	s_nop 0
	v_pk_mul_f32 v[80:81], v[80:81], v[88:89]
	s_nop 0
	v_pk_mul_f32 v[80:81], v[80:81], 0.5 op_sel_hi:[1,0]
	s_nop 0
	v_pk_mul_f32 v[80:81], v[86:87], v[80:81]
	s_nop 0
	v_pk_mul_f32 v[86:87], v[108:109], v[80:81]
	v_pk_fma_f32 v[80:81], v[108:109], v[80:81], v[108:109] neg_lo:[1,0,0] neg_hi:[1,0,0]
	s_nop 0
	v_cndmask_b32_e32 v79, v87, v81, vcc
	v_cmp_le_f32_e32 vcc, 0, v108
	v_mul_f32_e64 v81, |v99|, s1
	s_nop 0
	v_cndmask_b32_e32 v80, v86, v80, vcc
	v_cvt_pk_f16_f32 v79, v80, v79
	global_store_dwordx2 v[72:73], v[78:79], off offset:32
	v_mul_f32_e64 v79, |v98|, s1
	v_mul_f32_e32 v80, 0xbfb8aa3b, v79
	v_fma_f32 v78, v79, s33, 1.0
	v_mul_f32_e32 v79, v79, v80
	v_exp_f32_e32 v80, v79
	v_fma_f32 v79, v81, s33, 1.0
	v_rcp_f32_e32 v78, v78
	v_rcp_f32_e32 v79, v79
	v_mul_f32_e32 v86, 0xbfb8aa3b, v81
	v_mul_f32_e32 v81, v81, v86
	v_exp_f32_e32 v81, v81
	v_pk_fma_f32 v[86:87], v[78:79], s[0:1], v[70:71] op_sel_hi:[1,0,0]
	v_cmp_le_f32_e32 vcc, 0, v99
	v_pk_fma_f32 v[86:87], v[78:79], v[86:87], s[48:49] op_sel_hi:[1,1,0]
	s_nop 0
	v_pk_fma_f32 v[86:87], v[78:79], v[86:87], s[50:51] op_sel_hi:[1,1,0]
	s_nop 0
	v_pk_fma_f32 v[86:87], v[78:79], v[86:87], s[52:53] op_sel_hi:[1,1,0]
	s_nop 0
	v_pk_mul_f32 v[78:79], v[78:79], v[86:87]
	s_nop 0
	v_pk_mul_f32 v[78:79], v[78:79], 0.5 op_sel_hi:[1,0]
	s_nop 0
	v_pk_mul_f32 v[78:79], v[80:81], v[78:79]
	s_nop 0
	v_pk_mul_f32 v[80:81], v[98:99], v[78:79]
	v_pk_fma_f32 v[78:79], v[98:99], v[78:79], v[98:99] neg_lo:[1,0,0] neg_hi:[1,0,0]
	s_nop 0
	v_cndmask_b32_e32 v79, v81, v79, vcc
	v_cmp_le_f32_e32 vcc, 0, v98
	s_nop 1
	v_cndmask_b32_e32 v78, v80, v78, vcc
	v_cvt_pk_f16_f32 v78, v78, v79
	v_mul_f32_e64 v79, |v100|, s1
	v_mul_f32_e32 v81, 0xbfb8aa3b, v79
	v_fma_f32 v80, v79, s33, 1.0
	v_mul_f32_e32 v79, v79, v81
	v_exp_f32_e32 v86, v79
	v_mul_f32_e64 v79, |v101|, s1
	v_fma_f32 v81, v79, s33, 1.0
	v_rcp_f32_e32 v80, v80
	v_rcp_f32_e32 v81, v81
	v_mul_f32_e32 v87, 0xbfb8aa3b, v79
	v_mul_f32_e32 v79, v79, v87
	v_exp_f32_e32 v87, v79
	v_pk_fma_f32 v[88:89], v[80:81], s[0:1], v[70:71] op_sel_hi:[1,0,0]
	v_cmp_le_f32_e32 vcc, 0, v101
	v_pk_fma_f32 v[88:89], v[80:81], v[88:89], s[48:49] op_sel_hi:[1,1,0]
	s_nop 0
	v_pk_fma_f32 v[88:89], v[80:81], v[88:89], s[50:51] op_sel_hi:[1,1,0]
	s_nop 0
	v_pk_fma_f32 v[88:89], v[80:81], v[88:89], s[52:53] op_sel_hi:[1,1,0]
	s_nop 0
	v_pk_mul_f32 v[80:81], v[80:81], v[88:89]
	s_nop 0
	v_pk_mul_f32 v[80:81], v[80:81], 0.5 op_sel_hi:[1,0]
	s_nop 0
	v_pk_mul_f32 v[80:81], v[86:87], v[80:81]
	s_nop 0
	v_pk_mul_f32 v[86:87], v[100:101], v[80:81]
	v_pk_fma_f32 v[80:81], v[100:101], v[80:81], v[100:101] neg_lo:[1,0,0] neg_hi:[1,0,0]
	s_nop 0
	v_cndmask_b32_e32 v79, v87, v81, vcc
	v_cmp_le_f32_e32 vcc, 0, v100
	v_mul_f32_e64 v81, |v91|, s1
	s_nop 0
	v_cndmask_b32_e32 v80, v86, v80, vcc
	v_cvt_pk_f16_f32 v79, v80, v79
	global_store_dwordx2 v[72:73], v[78:79], off offset:160
	v_mul_f32_e64 v79, |v90|, s1
	v_mul_f32_e32 v80, 0xbfb8aa3b, v79
	v_fma_f32 v78, v79, s33, 1.0
	v_mul_f32_e32 v79, v79, v80
	v_exp_f32_e32 v80, v79
	v_fma_f32 v79, v81, s33, 1.0
	v_rcp_f32_e32 v78, v78
	v_rcp_f32_e32 v79, v79
	v_mul_f32_e32 v86, 0xbfb8aa3b, v81
	v_mul_f32_e32 v81, v81, v86
	v_exp_f32_e32 v81, v81
	v_pk_fma_f32 v[86:87], v[78:79], s[0:1], v[70:71] op_sel_hi:[1,0,0]
	v_cmp_le_f32_e32 vcc, 0, v91
	v_pk_fma_f32 v[86:87], v[78:79], v[86:87], s[48:49] op_sel_hi:[1,1,0]
	s_nop 0
	v_pk_fma_f32 v[86:87], v[78:79], v[86:87], s[50:51] op_sel_hi:[1,1,0]
	s_nop 0
	v_pk_fma_f32 v[86:87], v[78:79], v[86:87], s[52:53] op_sel_hi:[1,1,0]
	s_nop 0
	v_pk_mul_f32 v[78:79], v[78:79], v[86:87]
	s_nop 0
	v_pk_mul_f32 v[78:79], v[78:79], 0.5 op_sel_hi:[1,0]
	s_nop 0
	v_pk_mul_f32 v[78:79], v[80:81], v[78:79]
	s_nop 0
	v_pk_mul_f32 v[80:81], v[90:91], v[78:79]
	v_pk_fma_f32 v[78:79], v[90:91], v[78:79], v[90:91] neg_lo:[1,0,0] neg_hi:[1,0,0]
	s_nop 0
	v_cndmask_b32_e32 v79, v81, v79, vcc
	v_cmp_le_f32_e32 vcc, 0, v90
	s_nop 1
	v_cndmask_b32_e32 v78, v80, v78, vcc
	v_cvt_pk_f16_f32 v78, v78, v79
	v_mul_f32_e64 v79, |v92|, s1
	v_mul_f32_e32 v81, 0xbfb8aa3b, v79
	v_fma_f32 v80, v79, s33, 1.0
	v_mul_f32_e32 v79, v79, v81
	v_exp_f32_e32 v86, v79
	v_mul_f32_e64 v79, |v93|, s1
	v_fma_f32 v81, v79, s33, 1.0
	v_rcp_f32_e32 v80, v80
	v_rcp_f32_e32 v81, v81
	v_mul_f32_e32 v87, 0xbfb8aa3b, v79
	v_mul_f32_e32 v79, v79, v87
	v_exp_f32_e32 v87, v79
	v_pk_fma_f32 v[88:89], v[80:81], s[0:1], v[70:71] op_sel_hi:[1,0,0]
	v_cmp_le_f32_e32 vcc, 0, v93
	v_pk_fma_f32 v[88:89], v[80:81], v[88:89], s[48:49] op_sel_hi:[1,1,0]
	s_nop 0
	v_pk_fma_f32 v[88:89], v[80:81], v[88:89], s[50:51] op_sel_hi:[1,1,0]
	s_nop 0
	v_pk_fma_f32 v[88:89], v[80:81], v[88:89], s[52:53] op_sel_hi:[1,1,0]
	s_nop 0
	v_pk_mul_f32 v[80:81], v[80:81], v[88:89]
	s_nop 0
	v_pk_mul_f32 v[80:81], v[80:81], 0.5 op_sel_hi:[1,0]
	s_nop 0
	v_pk_mul_f32 v[80:81], v[86:87], v[80:81]
	s_nop 0
	v_pk_mul_f32 v[86:87], v[92:93], v[80:81]
	v_pk_fma_f32 v[80:81], v[92:93], v[80:81], v[92:93] neg_lo:[1,0,0] neg_hi:[1,0,0]
	s_nop 0
	v_cndmask_b32_e32 v79, v87, v81, vcc
	v_cmp_le_f32_e32 vcc, 0, v92
	v_mul_f32_e64 v81, |v83|, s1
	s_nop 0
	v_cndmask_b32_e32 v80, v86, v80, vcc
	v_cvt_pk_f16_f32 v79, v80, v79
	global_store_dwordx2 v[72:73], v[78:79], off offset:288
	v_mul_f32_e64 v79, |v82|, s1
	v_mul_f32_e32 v80, 0xbfb8aa3b, v79
	v_fma_f32 v78, v79, s33, 1.0
	v_mul_f32_e32 v79, v79, v80
	v_exp_f32_e32 v80, v79
	v_fma_f32 v79, v81, s33, 1.0
	v_rcp_f32_e32 v78, v78
	v_rcp_f32_e32 v79, v79
	v_mul_f32_e32 v86, 0xbfb8aa3b, v81
	v_mul_f32_e32 v81, v81, v86
	v_exp_f32_e32 v81, v81
	v_pk_fma_f32 v[86:87], v[78:79], s[0:1], v[70:71] op_sel_hi:[1,0,0]
	v_cmp_le_f32_e32 vcc, 0, v83
	v_pk_fma_f32 v[86:87], v[78:79], v[86:87], s[48:49] op_sel_hi:[1,1,0]
	s_nop 0
	v_pk_fma_f32 v[86:87], v[78:79], v[86:87], s[50:51] op_sel_hi:[1,1,0]
	s_nop 0
	v_pk_fma_f32 v[86:87], v[78:79], v[86:87], s[52:53] op_sel_hi:[1,1,0]
	s_nop 0
	v_pk_mul_f32 v[78:79], v[78:79], v[86:87]
	s_nop 0
	v_pk_mul_f32 v[78:79], v[78:79], 0.5 op_sel_hi:[1,0]
	s_nop 0
	v_pk_mul_f32 v[78:79], v[80:81], v[78:79]
	s_nop 0
	v_pk_mul_f32 v[80:81], v[82:83], v[78:79]
	v_pk_fma_f32 v[78:79], v[82:83], v[78:79], v[82:83] neg_lo:[1,0,0] neg_hi:[1,0,0]
	s_nop 0
	v_cndmask_b32_e32 v79, v81, v79, vcc
	v_cmp_le_f32_e32 vcc, 0, v82
	s_nop 1
	v_cndmask_b32_e32 v78, v80, v78, vcc
	v_cvt_pk_f16_f32 v78, v78, v79
	v_mul_f32_e64 v79, |v84|, s1
	v_mul_f32_e32 v81, 0xbfb8aa3b, v79
	v_fma_f32 v80, v79, s33, 1.0
	v_mul_f32_e32 v79, v79, v81
	v_exp_f32_e32 v82, v79
	v_mul_f32_e64 v79, |v85|, s1
	v_fma_f32 v81, v79, s33, 1.0
	v_rcp_f32_e32 v80, v80
	v_rcp_f32_e32 v81, v81
	v_mul_f32_e32 v83, 0xbfb8aa3b, v79
	v_mul_f32_e32 v79, v79, v83
	v_exp_f32_e32 v83, v79
	v_pk_fma_f32 v[86:87], v[80:81], s[0:1], v[70:71] op_sel_hi:[1,0,0]
	v_cmp_le_f32_e32 vcc, 0, v85
	v_pk_fma_f32 v[86:87], v[80:81], v[86:87], s[48:49] op_sel_hi:[1,1,0]
	s_nop 0
	v_pk_fma_f32 v[86:87], v[80:81], v[86:87], s[50:51] op_sel_hi:[1,1,0]
	s_nop 0
	v_pk_fma_f32 v[86:87], v[80:81], v[86:87], s[52:53] op_sel_hi:[1,1,0]
	s_nop 0
	v_pk_mul_f32 v[80:81], v[80:81], v[86:87]
	s_nop 0
	v_pk_mul_f32 v[80:81], v[80:81], 0.5 op_sel_hi:[1,0]
	s_nop 0
	v_pk_mul_f32 v[80:81], v[82:83], v[80:81]
	s_nop 0
	v_pk_mul_f32 v[82:83], v[84:85], v[80:81]
	v_pk_fma_f32 v[80:81], v[84:85], v[80:81], v[84:85] neg_lo:[1,0,0] neg_hi:[1,0,0]
	s_nop 0
	v_cndmask_b32_e32 v79, v83, v81, vcc
	v_cmp_le_f32_e32 vcc, 0, v84
	v_mul_f32_e64 v81, |v75|, s1
	s_nop 0
	v_cndmask_b32_e32 v80, v82, v80, vcc
	v_cvt_pk_f16_f32 v79, v80, v79
	global_store_dwordx2 v[72:73], v[78:79], off offset:416
	v_mul_f32_e64 v79, |v74|, s1
	v_mul_f32_e32 v80, 0xbfb8aa3b, v79
	v_fma_f32 v78, v79, s33, 1.0
	v_mul_f32_e32 v79, v79, v80
	v_exp_f32_e32 v80, v79
	v_fma_f32 v79, v81, s33, 1.0
	v_rcp_f32_e32 v78, v78
	v_rcp_f32_e32 v79, v79
	v_mul_f32_e32 v82, 0xbfb8aa3b, v81
	v_mul_f32_e32 v81, v81, v82
	v_exp_f32_e32 v81, v81
	v_pk_fma_f32 v[82:83], v[78:79], s[0:1], v[70:71] op_sel_hi:[1,0,0]
	v_cmp_le_f32_e32 vcc, 0, v75
	v_pk_fma_f32 v[82:83], v[78:79], v[82:83], s[48:49] op_sel_hi:[1,1,0]
	s_nop 0
	v_pk_fma_f32 v[82:83], v[78:79], v[82:83], s[50:51] op_sel_hi:[1,1,0]
	s_nop 0
	v_pk_fma_f32 v[82:83], v[78:79], v[82:83], s[52:53] op_sel_hi:[1,1,0]
	s_nop 0
	v_pk_mul_f32 v[78:79], v[78:79], v[82:83]
	s_nop 0
	v_pk_mul_f32 v[78:79], v[78:79], 0.5 op_sel_hi:[1,0]
	s_nop 0
	v_pk_mul_f32 v[78:79], v[80:81], v[78:79]
	s_nop 0
	v_pk_mul_f32 v[80:81], v[74:75], v[78:79]
	v_pk_fma_f32 v[78:79], v[74:75], v[78:79], v[74:75] neg_lo:[1,0,0] neg_hi:[1,0,0]
	s_nop 0
	v_cndmask_b32_e32 v75, v81, v79, vcc
	v_cmp_le_f32_e32 vcc, 0, v74
	s_nop 1
	v_cndmask_b32_e32 v74, v80, v78, vcc
	v_cvt_pk_f16_f32 v74, v74, v75
	v_mul_f32_e64 v75, |v76|, s1
	v_mul_f32_e32 v79, 0xbfb8aa3b, v75
	v_fma_f32 v78, v75, s33, 1.0
	v_mul_f32_e32 v75, v75, v79
	v_exp_f32_e32 v80, v75
	v_mul_f32_e64 v75, |v77|, s1
	v_fma_f32 v79, v75, s33, 1.0
	v_rcp_f32_e32 v78, v78
	v_rcp_f32_e32 v79, v79
	v_mul_f32_e32 v81, 0xbfb8aa3b, v75
	v_mul_f32_e32 v75, v75, v81
	v_exp_f32_e32 v81, v75
	v_pk_fma_f32 v[82:83], v[78:79], s[0:1], v[70:71] op_sel_hi:[1,0,0]
	v_cmp_le_f32_e32 vcc, 0, v77
	v_pk_fma_f32 v[82:83], v[78:79], v[82:83], s[48:49] op_sel_hi:[1,1,0]
	s_nop 0
	v_pk_fma_f32 v[82:83], v[78:79], v[82:83], s[50:51] op_sel_hi:[1,1,0]
	s_nop 0
	v_pk_fma_f32 v[82:83], v[78:79], v[82:83], s[52:53] op_sel_hi:[1,1,0]
	s_nop 0
	v_pk_mul_f32 v[78:79], v[78:79], v[82:83]
	s_nop 0
	v_pk_mul_f32 v[78:79], v[78:79], 0.5 op_sel_hi:[1,0]
	s_nop 0
	v_pk_mul_f32 v[78:79], v[80:81], v[78:79]
	s_nop 0
	v_pk_mul_f32 v[80:81], v[76:77], v[78:79]
	v_pk_fma_f32 v[78:79], v[76:77], v[78:79], v[76:77] neg_lo:[1,0,0] neg_hi:[1,0,0]
	v_mul_f32_e64 v77, |v67|, s1
	v_cndmask_b32_e32 v75, v81, v79, vcc
	v_cmp_le_f32_e32 vcc, 0, v76
	s_nop 1
	v_cndmask_b32_e32 v76, v80, v78, vcc
	v_cvt_pk_f16_f32 v75, v76, v75
	global_store_dwordx2 v[72:73], v[74:75], off offset:64
	v_mul_f32_e64 v75, |v66|, s1
	v_mul_f32_e32 v76, 0xbfb8aa3b, v75
	v_fma_f32 v74, v75, s33, 1.0
	v_mul_f32_e32 v75, v75, v76
	v_exp_f32_e32 v76, v75
	v_fma_f32 v75, v77, s33, 1.0
	v_rcp_f32_e32 v74, v74
	v_rcp_f32_e32 v75, v75
	v_mul_f32_e32 v78, 0xbfb8aa3b, v77
	v_mul_f32_e32 v77, v77, v78
	v_exp_f32_e32 v77, v77
	v_pk_fma_f32 v[78:79], v[74:75], s[0:1], v[70:71] op_sel_hi:[1,0,0]
	v_cmp_le_f32_e32 vcc, 0, v67
	v_pk_fma_f32 v[78:79], v[74:75], v[78:79], s[48:49] op_sel_hi:[1,1,0]
	s_nop 0
	v_pk_fma_f32 v[78:79], v[74:75], v[78:79], s[50:51] op_sel_hi:[1,1,0]
	s_nop 0
	v_pk_fma_f32 v[78:79], v[74:75], v[78:79], s[52:53] op_sel_hi:[1,1,0]
	s_nop 0
	v_pk_mul_f32 v[74:75], v[74:75], v[78:79]
	s_nop 0
	v_pk_mul_f32 v[74:75], v[74:75], 0.5 op_sel_hi:[1,0]
	s_nop 0
	v_pk_mul_f32 v[74:75], v[76:77], v[74:75]
	s_nop 0
	v_pk_mul_f32 v[76:77], v[66:67], v[74:75]
	v_pk_fma_f32 v[74:75], v[66:67], v[74:75], v[66:67] neg_lo:[1,0,0] neg_hi:[1,0,0]
	s_nop 0
	v_cndmask_b32_e32 v67, v77, v75, vcc
	v_cmp_le_f32_e32 vcc, 0, v66
	s_nop 1
	v_cndmask_b32_e32 v66, v76, v74, vcc
	v_cvt_pk_f16_f32 v66, v66, v67
	v_mul_f32_e64 v67, |v68|, s1
	v_mul_f32_e32 v75, 0xbfb8aa3b, v67
	v_fma_f32 v74, v67, s33, 1.0
	v_mul_f32_e32 v67, v67, v75
	v_exp_f32_e32 v76, v67
	v_mul_f32_e64 v67, |v69|, s1
	v_fma_f32 v75, v67, s33, 1.0
	v_rcp_f32_e32 v74, v74
	v_rcp_f32_e32 v75, v75
	v_mul_f32_e32 v77, 0xbfb8aa3b, v67
	v_mul_f32_e32 v67, v67, v77
	v_exp_f32_e32 v77, v67
	v_pk_fma_f32 v[78:79], v[74:75], s[0:1], v[70:71] op_sel_hi:[1,0,0]
	v_cmp_le_f32_e32 vcc, 0, v69
	v_pk_fma_f32 v[78:79], v[74:75], v[78:79], s[48:49] op_sel_hi:[1,1,0]
	s_nop 0
	v_pk_fma_f32 v[78:79], v[74:75], v[78:79], s[50:51] op_sel_hi:[1,1,0]
	s_nop 0
	v_pk_fma_f32 v[78:79], v[74:75], v[78:79], s[52:53] op_sel_hi:[1,1,0]
	s_nop 0
	v_pk_mul_f32 v[74:75], v[74:75], v[78:79]
	s_nop 0
	v_pk_mul_f32 v[74:75], v[74:75], 0.5 op_sel_hi:[1,0]
	s_nop 0
	v_pk_mul_f32 v[74:75], v[76:77], v[74:75]
	s_nop 0
	v_pk_mul_f32 v[76:77], v[68:69], v[74:75]
	v_pk_fma_f32 v[74:75], v[68:69], v[74:75], v[68:69] neg_lo:[1,0,0] neg_hi:[1,0,0]
	v_mul_f32_e64 v69, |v63|, s1
	v_cndmask_b32_e32 v67, v77, v75, vcc
	v_cmp_le_f32_e32 vcc, 0, v68
	s_nop 1
	v_cndmask_b32_e32 v68, v76, v74, vcc
	v_cvt_pk_f16_f32 v67, v68, v67
	global_store_dwordx2 v[72:73], v[66:67], off offset:192
	v_mul_f32_e64 v67, |v62|, s1
	v_mul_f32_e32 v68, 0xbfb8aa3b, v67
	v_fma_f32 v66, v67, s33, 1.0
	v_mul_f32_e32 v67, v67, v68
	v_exp_f32_e32 v68, v67
	v_fma_f32 v67, v69, s33, 1.0
	v_rcp_f32_e32 v66, v66
	v_rcp_f32_e32 v67, v67
	v_mul_f32_e32 v74, 0xbfb8aa3b, v69
	v_mul_f32_e32 v69, v69, v74
	v_exp_f32_e32 v69, v69
	v_pk_fma_f32 v[74:75], v[66:67], s[0:1], v[70:71] op_sel_hi:[1,0,0]
	v_cmp_le_f32_e32 vcc, 0, v63
	v_pk_fma_f32 v[74:75], v[66:67], v[74:75], s[48:49] op_sel_hi:[1,1,0]
	s_nop 0
	v_pk_fma_f32 v[74:75], v[66:67], v[74:75], s[50:51] op_sel_hi:[1,1,0]
	s_nop 0
	v_pk_fma_f32 v[74:75], v[66:67], v[74:75], s[52:53] op_sel_hi:[1,1,0]
	s_nop 0
	v_pk_mul_f32 v[66:67], v[66:67], v[74:75]
	s_nop 0
	v_pk_mul_f32 v[66:67], v[66:67], 0.5 op_sel_hi:[1,0]
	s_nop 0
	v_pk_mul_f32 v[66:67], v[68:69], v[66:67]
	s_nop 0
	v_pk_mul_f32 v[68:69], v[62:63], v[66:67]
	v_pk_fma_f32 v[66:67], v[62:63], v[66:67], v[62:63] neg_lo:[1,0,0] neg_hi:[1,0,0]
	s_nop 0
	v_cndmask_b32_e32 v63, v69, v67, vcc
	v_cmp_le_f32_e32 vcc, 0, v62
	s_nop 1
	v_cndmask_b32_e32 v62, v68, v66, vcc
	v_cvt_pk_f16_f32 v62, v62, v63
	v_mul_f32_e64 v63, |v64|, s1
	v_mul_f32_e32 v67, 0xbfb8aa3b, v63
	v_fma_f32 v66, v63, s33, 1.0
	v_mul_f32_e32 v63, v63, v67
	v_exp_f32_e32 v68, v63
	v_mul_f32_e64 v63, |v65|, s1
	v_fma_f32 v67, v63, s33, 1.0
	v_rcp_f32_e32 v66, v66
	v_rcp_f32_e32 v67, v67
	v_mul_f32_e32 v69, 0xbfb8aa3b, v63
	v_mul_f32_e32 v63, v63, v69
	v_exp_f32_e32 v69, v63
	v_pk_fma_f32 v[74:75], v[66:67], s[0:1], v[70:71] op_sel_hi:[1,0,0]
	v_cmp_le_f32_e32 vcc, 0, v65
	v_pk_fma_f32 v[74:75], v[66:67], v[74:75], s[48:49] op_sel_hi:[1,1,0]
	s_nop 0
	v_pk_fma_f32 v[74:75], v[66:67], v[74:75], s[50:51] op_sel_hi:[1,1,0]
	s_nop 0
	v_pk_fma_f32 v[74:75], v[66:67], v[74:75], s[52:53] op_sel_hi:[1,1,0]
	s_nop 0
	v_pk_mul_f32 v[66:67], v[66:67], v[74:75]
	s_nop 0
	v_pk_mul_f32 v[66:67], v[66:67], 0.5 op_sel_hi:[1,0]
	s_nop 0
	v_pk_mul_f32 v[66:67], v[68:69], v[66:67]
	s_nop 0
	v_pk_mul_f32 v[68:69], v[64:65], v[66:67]
	v_pk_fma_f32 v[66:67], v[64:65], v[66:67], v[64:65] neg_lo:[1,0,0] neg_hi:[1,0,0]
	v_mul_f32_e64 v65, |v59|, s1
	v_cndmask_b32_e32 v63, v69, v67, vcc
	v_cmp_le_f32_e32 vcc, 0, v64
	s_nop 1
	v_cndmask_b32_e32 v64, v68, v66, vcc
	v_cvt_pk_f16_f32 v63, v64, v63
	global_store_dwordx2 v[72:73], v[62:63], off offset:320
	v_mul_f32_e64 v63, |v58|, s1
	v_mul_f32_e32 v64, 0xbfb8aa3b, v63
	v_fma_f32 v62, v63, s33, 1.0
	v_mul_f32_e32 v63, v63, v64
	v_exp_f32_e32 v64, v63
	v_fma_f32 v63, v65, s33, 1.0
	v_rcp_f32_e32 v62, v62
	v_rcp_f32_e32 v63, v63
	v_mul_f32_e32 v66, 0xbfb8aa3b, v65
	v_mul_f32_e32 v65, v65, v66
	v_exp_f32_e32 v65, v65
	v_pk_fma_f32 v[66:67], v[62:63], s[0:1], v[70:71] op_sel_hi:[1,0,0]
	v_cmp_le_f32_e32 vcc, 0, v59
	v_pk_fma_f32 v[66:67], v[62:63], v[66:67], s[48:49] op_sel_hi:[1,1,0]
	s_nop 0
	v_pk_fma_f32 v[66:67], v[62:63], v[66:67], s[50:51] op_sel_hi:[1,1,0]
	s_nop 0
	v_pk_fma_f32 v[66:67], v[62:63], v[66:67], s[52:53] op_sel_hi:[1,1,0]
	s_nop 0
	v_pk_mul_f32 v[62:63], v[62:63], v[66:67]
	s_nop 0
	v_pk_mul_f32 v[62:63], v[62:63], 0.5 op_sel_hi:[1,0]
	s_nop 0
	v_pk_mul_f32 v[62:63], v[64:65], v[62:63]
	s_nop 0
	v_pk_mul_f32 v[64:65], v[58:59], v[62:63]
	v_pk_fma_f32 v[62:63], v[58:59], v[62:63], v[58:59] neg_lo:[1,0,0] neg_hi:[1,0,0]
	s_nop 0
	v_cndmask_b32_e32 v59, v65, v63, vcc
	v_cmp_le_f32_e32 vcc, 0, v58
	s_nop 1
	v_cndmask_b32_e32 v58, v64, v62, vcc
	v_cvt_pk_f16_f32 v58, v58, v59
	v_mul_f32_e64 v59, |v60|, s1
	v_mul_f32_e32 v63, 0xbfb8aa3b, v59
	v_fma_f32 v62, v59, s33, 1.0
	v_mul_f32_e32 v59, v59, v63
	v_exp_f32_e32 v64, v59
	v_mul_f32_e64 v59, |v61|, s1
	v_fma_f32 v63, v59, s33, 1.0
	v_rcp_f32_e32 v62, v62
	v_rcp_f32_e32 v63, v63
	v_mul_f32_e32 v65, 0xbfb8aa3b, v59
	v_mul_f32_e32 v59, v59, v65
	v_exp_f32_e32 v65, v59
	v_pk_fma_f32 v[66:67], v[62:63], s[0:1], v[70:71] op_sel_hi:[1,0,0]
	v_cmp_le_f32_e32 vcc, 0, v61
	v_pk_fma_f32 v[66:67], v[62:63], v[66:67], s[48:49] op_sel_hi:[1,1,0]
	s_nop 0
	v_pk_fma_f32 v[66:67], v[62:63], v[66:67], s[50:51] op_sel_hi:[1,1,0]
	s_nop 0
	v_pk_fma_f32 v[66:67], v[62:63], v[66:67], s[52:53] op_sel_hi:[1,1,0]
	s_nop 0
	v_pk_mul_f32 v[62:63], v[62:63], v[66:67]
	s_nop 0
	v_pk_mul_f32 v[62:63], v[62:63], 0.5 op_sel_hi:[1,0]
	s_nop 0
	v_pk_mul_f32 v[62:63], v[64:65], v[62:63]
	s_nop 0
	v_pk_mul_f32 v[64:65], v[60:61], v[62:63]
	v_pk_fma_f32 v[62:63], v[60:61], v[62:63], v[60:61] neg_lo:[1,0,0] neg_hi:[1,0,0]
	v_mul_f32_e64 v61, |v55|, s1
	v_cndmask_b32_e32 v59, v65, v63, vcc
	v_cmp_le_f32_e32 vcc, 0, v60
	s_nop 1
	v_cndmask_b32_e32 v60, v64, v62, vcc
	v_cvt_pk_f16_f32 v59, v60, v59
	global_store_dwordx2 v[72:73], v[58:59], off offset:448
	v_mul_f32_e64 v59, |v54|, s1
	v_mul_f32_e32 v60, 0xbfb8aa3b, v59
	v_fma_f32 v58, v59, s33, 1.0
	v_mul_f32_e32 v59, v59, v60
	v_exp_f32_e32 v60, v59
	v_fma_f32 v59, v61, s33, 1.0
	v_rcp_f32_e32 v58, v58
	v_rcp_f32_e32 v59, v59
	v_mul_f32_e32 v62, 0xbfb8aa3b, v61
	v_mul_f32_e32 v61, v61, v62
	v_exp_f32_e32 v61, v61
	v_pk_fma_f32 v[62:63], v[58:59], s[0:1], v[70:71] op_sel_hi:[1,0,0]
	v_cmp_le_f32_e32 vcc, 0, v55
	v_pk_fma_f32 v[62:63], v[58:59], v[62:63], s[48:49] op_sel_hi:[1,1,0]
	s_nop 0
	v_pk_fma_f32 v[62:63], v[58:59], v[62:63], s[50:51] op_sel_hi:[1,1,0]
	s_nop 0
	v_pk_fma_f32 v[62:63], v[58:59], v[62:63], s[52:53] op_sel_hi:[1,1,0]
	s_nop 0
	v_pk_mul_f32 v[58:59], v[58:59], v[62:63]
	s_nop 0
	v_pk_mul_f32 v[58:59], v[58:59], 0.5 op_sel_hi:[1,0]
	s_nop 0
	v_pk_mul_f32 v[58:59], v[60:61], v[58:59]
	s_nop 0
	v_pk_mul_f32 v[60:61], v[54:55], v[58:59]
	v_pk_fma_f32 v[58:59], v[54:55], v[58:59], v[54:55] neg_lo:[1,0,0] neg_hi:[1,0,0]
	s_nop 0
	v_cndmask_b32_e32 v55, v61, v59, vcc
	v_cmp_le_f32_e32 vcc, 0, v54
	s_nop 1
	v_cndmask_b32_e32 v54, v60, v58, vcc
	v_cvt_pk_f16_f32 v54, v54, v55
	v_mul_f32_e64 v55, |v56|, s1
	v_mul_f32_e32 v59, 0xbfb8aa3b, v55
	v_fma_f32 v58, v55, s33, 1.0
	v_mul_f32_e32 v55, v55, v59
	v_exp_f32_e32 v60, v55
	v_mul_f32_e64 v55, |v57|, s1
	v_fma_f32 v59, v55, s33, 1.0
	v_rcp_f32_e32 v58, v58
	v_rcp_f32_e32 v59, v59
	v_mul_f32_e32 v61, 0xbfb8aa3b, v55
	v_mul_f32_e32 v55, v55, v61
	v_exp_f32_e32 v61, v55
	v_pk_fma_f32 v[62:63], v[58:59], s[0:1], v[70:71] op_sel_hi:[1,0,0]
	v_cmp_le_f32_e32 vcc, 0, v57
	v_pk_fma_f32 v[62:63], v[58:59], v[62:63], s[48:49] op_sel_hi:[1,1,0]
	s_nop 0
	v_pk_fma_f32 v[62:63], v[58:59], v[62:63], s[50:51] op_sel_hi:[1,1,0]
	s_nop 0
	v_pk_fma_f32 v[62:63], v[58:59], v[62:63], s[52:53] op_sel_hi:[1,1,0]
	s_nop 0
	v_pk_mul_f32 v[58:59], v[58:59], v[62:63]
	s_nop 0
	v_pk_mul_f32 v[58:59], v[58:59], 0.5 op_sel_hi:[1,0]
	s_nop 0
	v_pk_mul_f32 v[58:59], v[60:61], v[58:59]
	s_nop 0
	v_pk_mul_f32 v[60:61], v[56:57], v[58:59]
	v_pk_fma_f32 v[58:59], v[56:57], v[58:59], v[56:57] neg_lo:[1,0,0] neg_hi:[1,0,0]
	v_mul_f32_e64 v57, |v51|, s1
	v_cndmask_b32_e32 v55, v61, v59, vcc
	v_cmp_le_f32_e32 vcc, 0, v56
	s_nop 1
	v_cndmask_b32_e32 v56, v60, v58, vcc
	v_cvt_pk_f16_f32 v55, v56, v55
	global_store_dwordx2 v[72:73], v[54:55], off offset:96
	v_mul_f32_e64 v55, |v50|, s1
	v_mul_f32_e32 v56, 0xbfb8aa3b, v55
	v_fma_f32 v54, v55, s33, 1.0
	v_mul_f32_e32 v55, v55, v56
	v_exp_f32_e32 v56, v55
	v_fma_f32 v55, v57, s33, 1.0
	v_rcp_f32_e32 v54, v54
	v_rcp_f32_e32 v55, v55
	v_mul_f32_e32 v58, 0xbfb8aa3b, v57
	v_mul_f32_e32 v57, v57, v58
	v_exp_f32_e32 v57, v57
	v_pk_fma_f32 v[58:59], v[54:55], s[0:1], v[70:71] op_sel_hi:[1,0,0]
	v_cmp_le_f32_e32 vcc, 0, v51
	v_pk_fma_f32 v[58:59], v[54:55], v[58:59], s[48:49] op_sel_hi:[1,1,0]
	s_nop 0
	v_pk_fma_f32 v[58:59], v[54:55], v[58:59], s[50:51] op_sel_hi:[1,1,0]
	s_nop 0
	v_pk_fma_f32 v[58:59], v[54:55], v[58:59], s[52:53] op_sel_hi:[1,1,0]
	s_nop 0
	v_pk_mul_f32 v[54:55], v[54:55], v[58:59]
	s_nop 0
	v_pk_mul_f32 v[54:55], v[54:55], 0.5 op_sel_hi:[1,0]
	s_nop 0
	v_pk_mul_f32 v[54:55], v[56:57], v[54:55]
	s_nop 0
	v_pk_mul_f32 v[56:57], v[50:51], v[54:55]
	v_pk_fma_f32 v[54:55], v[50:51], v[54:55], v[50:51] neg_lo:[1,0,0] neg_hi:[1,0,0]
	s_nop 0
	v_cndmask_b32_e32 v51, v57, v55, vcc
	v_cmp_le_f32_e32 vcc, 0, v50
	s_nop 1
	v_cndmask_b32_e32 v50, v56, v54, vcc
	v_cvt_pk_f16_f32 v50, v50, v51
	v_mul_f32_e64 v51, |v52|, s1
	v_mul_f32_e32 v55, 0xbfb8aa3b, v51
	v_fma_f32 v54, v51, s33, 1.0
	v_mul_f32_e32 v51, v51, v55
	v_exp_f32_e32 v56, v51
	v_mul_f32_e64 v51, |v53|, s1
	v_fma_f32 v55, v51, s33, 1.0
	v_rcp_f32_e32 v54, v54
	v_rcp_f32_e32 v55, v55
	v_mul_f32_e32 v57, 0xbfb8aa3b, v51
	v_mul_f32_e32 v51, v51, v57
	v_exp_f32_e32 v57, v51
	v_pk_fma_f32 v[58:59], v[54:55], s[0:1], v[70:71] op_sel_hi:[1,0,0]
	v_cmp_le_f32_e32 vcc, 0, v53
	v_pk_fma_f32 v[58:59], v[54:55], v[58:59], s[48:49] op_sel_hi:[1,1,0]
	s_nop 0
	v_pk_fma_f32 v[58:59], v[54:55], v[58:59], s[50:51] op_sel_hi:[1,1,0]
	s_nop 0
	v_pk_fma_f32 v[58:59], v[54:55], v[58:59], s[52:53] op_sel_hi:[1,1,0]
	s_nop 0
	v_pk_mul_f32 v[54:55], v[54:55], v[58:59]
	s_nop 0
	v_pk_mul_f32 v[54:55], v[54:55], 0.5 op_sel_hi:[1,0]
	s_nop 0
	v_pk_mul_f32 v[54:55], v[56:57], v[54:55]
	s_nop 0
	v_pk_mul_f32 v[56:57], v[52:53], v[54:55]
	v_pk_fma_f32 v[54:55], v[52:53], v[54:55], v[52:53] neg_lo:[1,0,0] neg_hi:[1,0,0]
	v_mul_f32_e64 v53, |v47|, s1
	v_cndmask_b32_e32 v51, v57, v55, vcc
	v_cmp_le_f32_e32 vcc, 0, v52
	s_nop 1
	v_cndmask_b32_e32 v52, v56, v54, vcc
	v_cvt_pk_f16_f32 v51, v52, v51
	global_store_dwordx2 v[72:73], v[50:51], off offset:224
	v_mul_f32_e64 v51, |v46|, s1
	v_mul_f32_e32 v52, 0xbfb8aa3b, v51
	v_fma_f32 v50, v51, s33, 1.0
	v_mul_f32_e32 v51, v51, v52
	v_exp_f32_e32 v52, v51
	v_fma_f32 v51, v53, s33, 1.0
	v_rcp_f32_e32 v50, v50
	v_rcp_f32_e32 v51, v51
	v_mul_f32_e32 v54, 0xbfb8aa3b, v53
	v_mul_f32_e32 v53, v53, v54
	v_exp_f32_e32 v53, v53
	v_pk_fma_f32 v[54:55], v[50:51], s[0:1], v[70:71] op_sel_hi:[1,0,0]
	v_cmp_le_f32_e32 vcc, 0, v47
	v_pk_fma_f32 v[54:55], v[50:51], v[54:55], s[48:49] op_sel_hi:[1,1,0]
	s_nop 0
	v_pk_fma_f32 v[54:55], v[50:51], v[54:55], s[50:51] op_sel_hi:[1,1,0]
	s_nop 0
	v_pk_fma_f32 v[54:55], v[50:51], v[54:55], s[52:53] op_sel_hi:[1,1,0]
	s_nop 0
	v_pk_mul_f32 v[50:51], v[50:51], v[54:55]
	s_nop 0
	v_pk_mul_f32 v[50:51], v[50:51], 0.5 op_sel_hi:[1,0]
	s_nop 0
	v_pk_mul_f32 v[50:51], v[52:53], v[50:51]
	s_nop 0
	v_pk_mul_f32 v[52:53], v[46:47], v[50:51]
	v_pk_fma_f32 v[50:51], v[46:47], v[50:51], v[46:47] neg_lo:[1,0,0] neg_hi:[1,0,0]
	s_nop 0
	v_cndmask_b32_e32 v47, v53, v51, vcc
	v_cmp_le_f32_e32 vcc, 0, v46
	s_nop 1
	v_cndmask_b32_e32 v46, v52, v50, vcc
	v_cvt_pk_f16_f32 v46, v46, v47
	v_mul_f32_e64 v47, |v48|, s1
	v_mul_f32_e32 v51, 0xbfb8aa3b, v47
	v_fma_f32 v50, v47, s33, 1.0
	v_mul_f32_e32 v47, v47, v51
	v_exp_f32_e32 v52, v47
	v_mul_f32_e64 v47, |v49|, s1
	v_fma_f32 v51, v47, s33, 1.0
	v_rcp_f32_e32 v50, v50
	v_rcp_f32_e32 v51, v51
	v_mul_f32_e32 v53, 0xbfb8aa3b, v47
	v_mul_f32_e32 v47, v47, v53
	v_exp_f32_e32 v53, v47
	v_pk_fma_f32 v[54:55], v[50:51], s[0:1], v[70:71] op_sel_hi:[1,0,0]
	v_cmp_le_f32_e32 vcc, 0, v49
	v_pk_fma_f32 v[54:55], v[50:51], v[54:55], s[48:49] op_sel_hi:[1,1,0]
	s_nop 0
	v_pk_fma_f32 v[54:55], v[50:51], v[54:55], s[50:51] op_sel_hi:[1,1,0]
	s_nop 0
	v_pk_fma_f32 v[54:55], v[50:51], v[54:55], s[52:53] op_sel_hi:[1,1,0]
	s_nop 0
	v_pk_mul_f32 v[50:51], v[50:51], v[54:55]
	s_nop 0
	v_pk_mul_f32 v[50:51], v[50:51], 0.5 op_sel_hi:[1,0]
	s_nop 0
	v_pk_mul_f32 v[50:51], v[52:53], v[50:51]
	s_nop 0
	v_pk_mul_f32 v[52:53], v[48:49], v[50:51]
	v_pk_fma_f32 v[50:51], v[48:49], v[50:51], v[48:49] neg_lo:[1,0,0] neg_hi:[1,0,0]
	v_mul_f32_e64 v49, |v43|, s1
	v_cndmask_b32_e32 v47, v53, v51, vcc
	v_cmp_le_f32_e32 vcc, 0, v48
	s_nop 1
	v_cndmask_b32_e32 v48, v52, v50, vcc
	v_cvt_pk_f16_f32 v47, v48, v47
	global_store_dwordx2 v[72:73], v[46:47], off offset:352
	v_mul_f32_e64 v47, |v42|, s1
	v_mul_f32_e32 v48, 0xbfb8aa3b, v47
	v_fma_f32 v46, v47, s33, 1.0
	v_mul_f32_e32 v47, v47, v48
	v_exp_f32_e32 v48, v47
	v_fma_f32 v47, v49, s33, 1.0
	v_rcp_f32_e32 v46, v46
	v_rcp_f32_e32 v47, v47
	v_mul_f32_e32 v50, 0xbfb8aa3b, v49
	v_mul_f32_e32 v49, v49, v50
	v_exp_f32_e32 v49, v49
	v_pk_fma_f32 v[50:51], v[46:47], s[0:1], v[70:71] op_sel_hi:[1,0,0]
	v_cmp_le_f32_e32 vcc, 0, v43
	v_pk_fma_f32 v[50:51], v[46:47], v[50:51], s[48:49] op_sel_hi:[1,1,0]
	s_nop 0
	v_pk_fma_f32 v[50:51], v[46:47], v[50:51], s[50:51] op_sel_hi:[1,1,0]
	s_nop 0
	v_pk_fma_f32 v[50:51], v[46:47], v[50:51], s[52:53] op_sel_hi:[1,1,0]
	s_nop 0
	v_pk_mul_f32 v[46:47], v[46:47], v[50:51]
	s_nop 0
	v_pk_mul_f32 v[46:47], v[46:47], 0.5 op_sel_hi:[1,0]
	s_nop 0
	v_pk_mul_f32 v[46:47], v[48:49], v[46:47]
	s_nop 0
	v_pk_mul_f32 v[48:49], v[42:43], v[46:47]
	v_pk_fma_f32 v[46:47], v[42:43], v[46:47], v[42:43] neg_lo:[1,0,0] neg_hi:[1,0,0]
	s_nop 0
	v_cndmask_b32_e32 v43, v49, v47, vcc
	v_cmp_le_f32_e32 vcc, 0, v42
	s_nop 1
	v_cndmask_b32_e32 v42, v48, v46, vcc
	v_cvt_pk_f16_f32 v42, v42, v43
	v_mul_f32_e64 v43, |v44|, s1
	v_mul_f32_e32 v47, 0xbfb8aa3b, v43
	v_fma_f32 v46, v43, s33, 1.0
	v_mul_f32_e32 v43, v43, v47
	v_exp_f32_e32 v48, v43
	v_mul_f32_e64 v43, |v45|, s1
	v_fma_f32 v47, v43, s33, 1.0
	v_rcp_f32_e32 v46, v46
	v_rcp_f32_e32 v47, v47
	v_mul_f32_e32 v49, 0xbfb8aa3b, v43
	v_mul_f32_e32 v43, v43, v49
	v_exp_f32_e32 v49, v43
	v_pk_fma_f32 v[50:51], v[46:47], s[0:1], v[70:71] op_sel_hi:[1,0,0]
	v_cmp_le_f32_e32 vcc, 0, v45
	v_pk_fma_f32 v[50:51], v[46:47], v[50:51], s[48:49] op_sel_hi:[1,1,0]
	s_nop 0
	v_pk_fma_f32 v[50:51], v[46:47], v[50:51], s[50:51] op_sel_hi:[1,1,0]
	s_nop 0
	v_pk_fma_f32 v[50:51], v[46:47], v[50:51], s[52:53] op_sel_hi:[1,1,0]
	s_nop 0
	v_pk_mul_f32 v[46:47], v[46:47], v[50:51]
	s_nop 0
	v_pk_mul_f32 v[46:47], v[46:47], 0.5 op_sel_hi:[1,0]
	s_nop 0
	v_pk_mul_f32 v[46:47], v[48:49], v[46:47]
	s_nop 0
	v_pk_mul_f32 v[48:49], v[44:45], v[46:47]
	v_pk_fma_f32 v[46:47], v[44:45], v[46:47], v[44:45] neg_lo:[1,0,0] neg_hi:[1,0,0]
	s_nop 0
	v_cndmask_b32_e32 v43, v49, v47, vcc
	v_cmp_le_f32_e32 vcc, 0, v44
	s_nop 1
	v_cndmask_b32_e32 v44, v48, v46, vcc
	v_cvt_pk_f16_f32 v43, v44, v43
	global_store_dwordx2 v[72:73], v[42:43], off offset:480
	v_or_b32_e32 v42, 0x200, v178
	v_mov_b32_e32 v43, v137
	v_lshl_add_u64 v[42:43], v[182:183], 0, v[42:43]
	s_barrier
	global_load_dwordx4 v[86:89], v[42:43], off offset:16
	global_load_dwordx4 v[68:71], v[42:43], off
	v_or_b32_e32 v42, 0x280, v178
	v_mov_b32_e32 v43, v137
	v_lshl_add_u64 v[42:43], v[182:183], 0, v[42:43]
	global_load_dwordx4 v[78:81], v[42:43], off offset:16
	global_load_dwordx4 v[82:85], v[42:43], off
	v_or_b32_e32 v42, 0x300, v178
	v_mov_b32_e32 v43, v137
	v_lshl_add_u64 v[42:43], v[182:183], 0, v[42:43]
	global_load_dwordx4 v[64:67], v[42:43], off offset:16
	global_load_dwordx4 v[72:75], v[42:43], off
	v_or_b32_e32 v42, 0x380, v178
	v_mov_b32_e32 v43, v137
	v_lshl_add_u64 v[42:43], v[182:183], 0, v[42:43]
	global_load_dwordx4 v[48:51], v[42:43], off offset:16
	global_load_dwordx4 v[56:59], v[42:43], off
	s_load_dword s33, s[46:47], 0x400
	s_and_saveexec_b64 s[0:1], s[38:39]
	s_cbranch_execz .LBB3_36
	s_movk_i32 s38, 0x1ff
	v_cmp_lt_u32_e32 vcc, s38, v0
	s_and_saveexec_b64 s[38:39], vcc
	s_cbranch_execz .LBB3_35
	s_movk_i32 s45, 0x2ff
	v_cmp_lt_u32_e32 vcc, s45, v0
	s_and_saveexec_b64 s[46:47], vcc
	s_xor_b64 s[46:47], exec, s[46:47]
	v_add_u32_e32 v193, 0xf000, v191
	s_andn2_saveexec_b64 s[46:47], s[46:47]
	v_add_u32_e32 v193, 0x10600, v191
	s_or_b64 exec, exec, s[46:47]

.LBB3_44:
	s_or_b64 exec, exec, s[0:1]
	s_waitcnt lgkmcnt(0)
	s_barrier
	global_load_dwordx4 v[42:45], v[180:181], off
	global_load_dwordx4 v[52:55], v[180:181], off offset:16
	global_load_dwordx4 v[118:121], v[180:181], off offset:128
	s_load_dword s0, s[2:3], 0x400
	ds_read_b32 v8, v227
	ds_read_b32 v9, v228
	ds_read_b32 v46, v229
	ds_read_b32 v47, v230
	ds_read_b32 v76, v231
	ds_read_b32 v77, v233
	ds_read_b32 v134, v234
	ds_read_b32 v135, v235
	global_load_dwordx4 v[122:125], v[180:181], off offset:144
	global_load_dwordx4 v[126:129], v[180:181], off offset:256
	global_load_dwordx4 v[130:133], v[180:181], off offset:272
	global_load_dwordx4 v[60:63], v[180:181], off offset:384
	global_load_dwordx4 v[114:117], v[180:181], off offset:400
	global_load_dwordx4 v[110:113], v[180:181], off offset:512
	global_load_dwordx4 v[106:109], v[180:181], off offset:528
	global_load_dwordx4 v[102:105], v[180:181], off offset:640
	global_load_dwordx4 v[98:101], v[180:181], off offset:656
	global_load_dwordx4 v[94:97], v[180:181], off offset:768
	global_load_dwordx4 v[90:93], v[180:181], off offset:784
	global_load_dwordx4 v[4:7], v[180:181], off offset:896
	global_load_dwordx4 v[0:3], v[180:181], off offset:912
	s_waitcnt lgkmcnt(0)
	v_add_f32_e32 v137, s0, v8
	v_add_f32_e32 v140, s0, v9
	v_add_f32_e32 v141, s0, v46
	v_add_f32_e32 v142, s0, v47
	v_add_f32_e32 v143, s0, v76
	v_add_f32_e32 v144, s0, v77
	v_add_f32_e32 v145, s0, v134
	v_add_f32_e32 v146, s0, v135
	v_cndmask_b32_e64 v8, v8, v137, s[18:19]
	v_cndmask_b32_e64 v9, v9, v140, s[20:21]
	v_cndmask_b32_e64 v46, v46, v141, s[22:23]
	v_cndmask_b32_e64 v47, v47, v142, s[24:25]
	v_cndmask_b32_e64 v76, v76, v143, s[26:27]
	v_cndmask_b32_e64 v77, v77, v144, s[28:29]
	v_cndmask_b32_e64 v134, v134, v145, s[30:31]
	v_cndmask_b32_e64 v135, v135, v146, s[34:35]
	v_cvt_pk_f16_f32 v143, v134, v135
	v_cvt_pk_f16_f32 v142, v76, v77
	v_cvt_pk_f16_f32 v141, v46, v47
	v_cvt_pk_f16_f32 v140, v8, v9
	ds_write_b128 v232, v[140:143]
	s_waitcnt lgkmcnt(0)
	s_barrier
	s_load_dword s2, s[42:43], 0x400
	s_load_dword s0, s[40:41], 0x400
	s_waitcnt lgkmcnt(0)
	v_mov_b64_e32 v[8:9], s[2:3]
	s_waitcnt vmcnt(15)
	v_cvt_f32_f16_e32 v47, v43
	v_cvt_f32_f16_e32 v46, v42
	v_cvt_f32_f16_e32 v77, v45
	v_cvt_f32_f16_e32 v76, v44
	s_waitcnt vmcnt(14)
	v_cvt_f32_f16_e32 v135, v53
	v_cvt_f32_f16_e32 v134, v52
	v_cvt_f32_f16_sdwa v43, v43 dst_sel:DWORD dst_unused:UNUSED_PAD src0_sel:WORD_1
	v_cvt_f32_f16_sdwa v42, v42 dst_sel:DWORD dst_unused:UNUSED_PAD src0_sel:WORD_1
	v_cvt_f32_f16_sdwa v45, v45 dst_sel:DWORD dst_unused:UNUSED_PAD src0_sel:WORD_1
	v_cvt_f32_f16_sdwa v44, v44 dst_sel:DWORD dst_unused:UNUSED_PAD src0_sel:WORD_1
	v_cvt_f32_f16_sdwa v53, v53 dst_sel:DWORD dst_unused:UNUSED_PAD src0_sel:WORD_1
	v_cvt_f32_f16_sdwa v52, v52 dst_sel:DWORD dst_unused:UNUSED_PAD src0_sel:WORD_1
	v_cvt_f32_f16_e32 v141, v55
	v_cvt_f32_f16_e32 v140, v54
	v_cvt_f32_f16_sdwa v55, v55 dst_sel:DWORD dst_unused:UNUSED_PAD src0_sel:WORD_1
	v_cvt_f32_f16_sdwa v54, v54 dst_sel:DWORD dst_unused:UNUSED_PAD src0_sel:WORD_1
	s_waitcnt vmcnt(13)
	v_cvt_f32_f16_e32 v143, v119
	v_cvt_f32_f16_e32 v142, v118
	v_pk_add_f32 v[46:47], v[46:47], 1.0 op_sel_hi:[1,0]
	v_pk_add_f32 v[76:77], v[76:77], 1.0 op_sel_hi:[1,0]
	v_pk_add_f32 v[134:135], v[134:135], 1.0 op_sel_hi:[1,0]
	v_cvt_f32_f16_sdwa v119, v119 dst_sel:DWORD dst_unused:UNUSED_PAD src0_sel:WORD_1
	v_pk_add_f32 v[140:141], v[140:141], 1.0 op_sel_hi:[1,0]
	v_pk_fma_f32 v[38:39], v[38:39], v[46:47], v[42:43]
	v_pk_fma_f32 v[40:41], v[40:41], v[76:77], v[44:45]
	v_pk_fma_f32 v[34:35], v[34:35], v[134:135], v[52:53]
	v_cvt_f32_f16_sdwa v118, v118 dst_sel:DWORD dst_unused:UNUSED_PAD src0_sel:WORD_1
	v_pk_fma_f32 v[42:43], v[36:37], v[140:141], v[54:55]
	v_pk_fma_f32 v[36:37], v[38:39], s[0:1], v[8:9] op_sel_hi:[1,0,0]
	v_pk_fma_f32 v[38:39], v[40:41], s[0:1], v[8:9] op_sel_hi:[1,0,0]
	v_pk_fma_f32 v[34:35], v[34:35], s[0:1], v[8:9] op_sel_hi:[1,0,0]
	v_cvt_pk_f16_f32 v36, v36, v37
	v_cvt_pk_f16_f32 v37, v38, v39
	v_cvt_pk_f16_f32 v38, v34, v35
	v_pk_fma_f32 v[34:35], v[42:43], s[0:1], v[8:9] op_sel_hi:[1,0,0]
	v_cvt_f32_f16_sdwa v41, v121 dst_sel:DWORD dst_unused:UNUSED_PAD src0_sel:WORD_1
	v_cvt_pk_f16_f32 v39, v34, v35
	v_pk_add_f32 v[34:35], v[142:143], 1.0 op_sel_hi:[1,0]
	v_cvt_f32_f16_sdwa v40, v120 dst_sel:DWORD dst_unused:UNUSED_PAD src0_sel:WORD_1
	v_pk_fma_f32 v[30:31], v[30:31], v[34:35], v[118:119]
	v_cvt_f32_f16_e32 v35, v121
	v_cvt_f32_f16_e32 v34, v120
	v_pk_fma_f32 v[30:31], v[30:31], s[0:1], v[8:9] op_sel_hi:[1,0,0]
	s_nop 0
	v_cvt_pk_f16_f32 v44, v30, v31
	v_pk_add_f32 v[30:31], v[34:35], 1.0 op_sel_hi:[1,0]
	s_waitcnt vmcnt(12)
	v_cvt_f32_f16_sdwa v35, v123 dst_sel:DWORD dst_unused:UNUSED_PAD src0_sel:WORD_1
	v_pk_fma_f32 v[30:31], v[32:33], v[30:31], v[40:41]
	v_cvt_f32_f16_e32 v33, v123
	v_cvt_f32_f16_e32 v32, v122
	v_cvt_f32_f16_sdwa v34, v122 dst_sel:DWORD dst_unused:UNUSED_PAD src0_sel:WORD_1
	v_pk_fma_f32 v[30:31], v[30:31], s[0:1], v[8:9] op_sel_hi:[1,0,0]
	s_nop 0
	v_cvt_pk_f16_f32 v45, v30, v31
	v_pk_add_f32 v[30:31], v[32:33], 1.0 op_sel_hi:[1,0]
	v_cvt_f32_f16_sdwa v33, v125 dst_sel:DWORD dst_unused:UNUSED_PAD src0_sel:WORD_1
	v_pk_fma_f32 v[26:27], v[26:27], v[30:31], v[34:35]
	v_cvt_f32_f16_e32 v31, v125
	v_cvt_f32_f16_e32 v30, v124
	v_cvt_f32_f16_sdwa v32, v124 dst_sel:DWORD dst_unused:UNUSED_PAD src0_sel:WORD_1
	v_pk_fma_f32 v[26:27], v[26:27], s[0:1], v[8:9] op_sel_hi:[1,0,0]
	s_nop 0
	v_cvt_pk_f16_f32 v46, v26, v27
	v_pk_add_f32 v[26:27], v[30:31], 1.0 op_sel_hi:[1,0]
	s_waitcnt vmcnt(11)
	v_cvt_f32_f16_sdwa v31, v127 dst_sel:DWORD dst_unused:UNUSED_PAD src0_sel:WORD_1
	v_pk_fma_f32 v[26:27], v[28:29], v[26:27], v[32:33]
	v_cvt_f32_f16_e32 v29, v127
	v_cvt_f32_f16_e32 v28, v126
	v_cvt_f32_f16_sdwa v30, v126 dst_sel:DWORD dst_unused:UNUSED_PAD src0_sel:WORD_1
	v_pk_fma_f32 v[26:27], v[26:27], s[0:1], v[8:9] op_sel_hi:[1,0,0]
	s_nop 0
	v_cvt_pk_f16_f32 v47, v26, v27
	v_pk_add_f32 v[26:27], v[28:29], 1.0 op_sel_hi:[1,0]
	v_cvt_f32_f16_sdwa v29, v129 dst_sel:DWORD dst_unused:UNUSED_PAD src0_sel:WORD_1
	v_pk_fma_f32 v[22:23], v[22:23], v[26:27], v[30:31]
	v_cvt_f32_f16_e32 v27, v129
	v_cvt_f32_f16_e32 v26, v128
	v_cvt_f32_f16_sdwa v28, v128 dst_sel:DWORD dst_unused:UNUSED_PAD src0_sel:WORD_1
	v_pk_fma_f32 v[22:23], v[22:23], s[0:1], v[8:9] op_sel_hi:[1,0,0]
	s_nop 0
	v_cvt_pk_f16_f32 v52, v22, v23
	v_pk_add_f32 v[22:23], v[26:27], 1.0 op_sel_hi:[1,0]
	s_waitcnt vmcnt(10)
	v_cvt_f32_f16_sdwa v27, v131 dst_sel:DWORD dst_unused:UNUSED_PAD src0_sel:WORD_1
	v_pk_fma_f32 v[22:23], v[24:25], v[22:23], v[28:29]
	v_cvt_f32_f16_e32 v25, v131
	v_cvt_f32_f16_e32 v24, v130
	v_cvt_f32_f16_sdwa v26, v130 dst_sel:DWORD dst_unused:UNUSED_PAD src0_sel:WORD_1
	v_pk_fma_f32 v[22:23], v[22:23], s[0:1], v[8:9] op_sel_hi:[1,0,0]
	s_nop 0
	v_cvt_pk_f16_f32 v53, v22, v23
	v_pk_add_f32 v[22:23], v[24:25], 1.0 op_sel_hi:[1,0]
	v_cvt_f32_f16_sdwa v25, v133 dst_sel:DWORD dst_unused:UNUSED_PAD src0_sel:WORD_1
	v_pk_fma_f32 v[18:19], v[18:19], v[22:23], v[26:27]
	v_cvt_f32_f16_e32 v23, v133
	v_cvt_f32_f16_e32 v22, v132
	v_cvt_f32_f16_sdwa v24, v132 dst_sel:DWORD dst_unused:UNUSED_PAD src0_sel:WORD_1
	v_pk_fma_f32 v[18:19], v[18:19], s[0:1], v[8:9] op_sel_hi:[1,0,0]
	s_nop 0
	v_cvt_pk_f16_f32 v54, v18, v19
	v_pk_add_f32 v[18:19], v[22:23], 1.0 op_sel_hi:[1,0]
	s_waitcnt vmcnt(9)
	v_cvt_f32_f16_sdwa v23, v61 dst_sel:DWORD dst_unused:UNUSED_PAD src0_sel:WORD_1
	v_pk_fma_f32 v[18:19], v[20:21], v[18:19], v[24:25]
	v_cvt_f32_f16_e32 v21, v61
	v_cvt_f32_f16_e32 v20, v60
	v_cvt_f32_f16_sdwa v22, v60 dst_sel:DWORD dst_unused:UNUSED_PAD src0_sel:WORD_1
	v_pk_fma_f32 v[18:19], v[18:19], s[0:1], v[8:9] op_sel_hi:[1,0,0]
	s_nop 0
	v_cvt_pk_f16_f32 v55, v18, v19
	v_pk_add_f32 v[18:19], v[20:21], 1.0 op_sel_hi:[1,0]
	v_cvt_f32_f16_sdwa v21, v63 dst_sel:DWORD dst_unused:UNUSED_PAD src0_sel:WORD_1
	v_pk_fma_f32 v[14:15], v[14:15], v[18:19], v[22:23]
	v_cvt_f32_f16_e32 v19, v63
	v_cvt_f32_f16_e32 v18, v62
	v_cvt_f32_f16_sdwa v20, v62 dst_sel:DWORD dst_unused:UNUSED_PAD src0_sel:WORD_1
	v_pk_fma_f32 v[14:15], v[14:15], s[0:1], v[8:9] op_sel_hi:[1,0,0]
	s_nop 0
	v_cvt_pk_f16_f32 v60, v14, v15
	v_pk_add_f32 v[14:15], v[18:19], 1.0 op_sel_hi:[1,0]
	s_waitcnt vmcnt(8)
	v_cvt_f32_f16_sdwa v19, v115 dst_sel:DWORD dst_unused:UNUSED_PAD src0_sel:WORD_1
	v_pk_fma_f32 v[14:15], v[16:17], v[14:15], v[20:21]
	v_cvt_f32_f16_e32 v17, v115
	v_cvt_f32_f16_e32 v16, v114
	v_cvt_f32_f16_sdwa v18, v114 dst_sel:DWORD dst_unused:UNUSED_PAD src0_sel:WORD_1
	v_pk_fma_f32 v[14:15], v[14:15], s[0:1], v[8:9] op_sel_hi:[1,0,0]
	s_nop 0
	v_cvt_pk_f16_f32 v61, v14, v15
	v_pk_add_f32 v[14:15], v[16:17], 1.0 op_sel_hi:[1,0]
	v_cvt_f32_f16_sdwa v17, v117 dst_sel:DWORD dst_unused:UNUSED_PAD src0_sel:WORD_1
	v_pk_fma_f32 v[10:11], v[10:11], v[14:15], v[18:19]
	v_cvt_f32_f16_e32 v15, v117
	v_cvt_f32_f16_e32 v14, v116
	v_cvt_f32_f16_sdwa v16, v116 dst_sel:DWORD dst_unused:UNUSED_PAD src0_sel:WORD_1
	v_pk_fma_f32 v[10:11], v[10:11], s[0:1], v[8:9] op_sel_hi:[1,0,0]
	s_nop 0
	v_cvt_pk_f16_f32 v62, v10, v11
	v_pk_add_f32 v[10:11], v[14:15], 1.0 op_sel_hi:[1,0]
	s_waitcnt vmcnt(7)
	v_cvt_f32_f16_sdwa v15, v111 dst_sel:DWORD dst_unused:UNUSED_PAD src0_sel:WORD_1
	v_pk_fma_f32 v[10:11], v[12:13], v[10:11], v[16:17]
	v_cvt_f32_f16_e32 v13, v111
	v_cvt_f32_f16_e32 v12, v110
	v_cvt_f32_f16_sdwa v14, v110 dst_sel:DWORD dst_unused:UNUSED_PAD src0_sel:WORD_1
	v_pk_fma_f32 v[10:11], v[10:11], s[0:1], v[8:9] op_sel_hi:[1,0,0]
	s_nop 0
	v_cvt_pk_f16_f32 v63, v10, v11
	v_pk_add_f32 v[10:11], v[12:13], 1.0 op_sel_hi:[1,0]
	v_cvt_f32_f16_e32 v13, v113
	v_cvt_f32_f16_e32 v12, v112
	v_pk_fma_f32 v[10:11], v[68:69], v[10:11], v[14:15]
	v_cvt_f32_f16_sdwa v15, v113 dst_sel:DWORD dst_unused:UNUSED_PAD src0_sel:WORD_1
	v_cvt_f32_f16_sdwa v14, v112 dst_sel:DWORD dst_unused:UNUSED_PAD src0_sel:WORD_1
	v_pk_fma_f32 v[10:11], v[10:11], s[0:1], v[8:9] op_sel_hi:[1,0,0]
	s_nop 0
	v_cvt_pk_f16_f32 v68, v10, v11
	v_pk_add_f32 v[10:11], v[12:13], 1.0 op_sel_hi:[1,0]
	s_waitcnt vmcnt(6)
	v_cvt_f32_f16_e32 v13, v107
	v_cvt_f32_f16_e32 v12, v106
	v_pk_fma_f32 v[10:11], v[70:71], v[10:11], v[14:15]
	v_cvt_f32_f16_sdwa v15, v107 dst_sel:DWORD dst_unused:UNUSED_PAD src0_sel:WORD_1
	v_cvt_f32_f16_sdwa v14, v106 dst_sel:DWORD dst_unused:UNUSED_PAD src0_sel:WORD_1
	v_pk_fma_f32 v[10:11], v[10:11], s[0:1], v[8:9] op_sel_hi:[1,0,0]
	s_nop 0
	v_cvt_pk_f16_f32 v69, v10, v11
	v_pk_add_f32 v[10:11], v[12:13], 1.0 op_sel_hi:[1,0]
	v_cvt_f32_f16_e32 v13, v109
	v_cvt_f32_f16_e32 v12, v108
	v_pk_fma_f32 v[10:11], v[86:87], v[10:11], v[14:15]
	v_cvt_f32_f16_sdwa v15, v109 dst_sel:DWORD dst_unused:UNUSED_PAD src0_sel:WORD_1
	v_cvt_f32_f16_sdwa v14, v108 dst_sel:DWORD dst_unused:UNUSED_PAD src0_sel:WORD_1
	v_pk_fma_f32 v[10:11], v[10:11], s[0:1], v[8:9] op_sel_hi:[1,0,0]
	s_nop 0
	v_cvt_pk_f16_f32 v70, v10, v11
	v_pk_add_f32 v[10:11], v[12:13], 1.0 op_sel_hi:[1,0]
	s_waitcnt vmcnt(5)
	v_cvt_f32_f16_e32 v13, v103
	v_cvt_f32_f16_e32 v12, v102
	v_pk_fma_f32 v[10:11], v[88:89], v[10:11], v[14:15]
	v_cvt_f32_f16_sdwa v15, v103 dst_sel:DWORD dst_unused:UNUSED_PAD src0_sel:WORD_1
	v_cvt_f32_f16_sdwa v14, v102 dst_sel:DWORD dst_unused:UNUSED_PAD src0_sel:WORD_1
	v_pk_fma_f32 v[10:11], v[10:11], s[0:1], v[8:9] op_sel_hi:[1,0,0]
	s_nop 0
	v_cvt_pk_f16_f32 v71, v10, v11
	v_pk_add_f32 v[10:11], v[12:13], 1.0 op_sel_hi:[1,0]
	v_cvt_f32_f16_e32 v13, v105
	v_cvt_f32_f16_e32 v12, v104
	v_pk_fma_f32 v[10:11], v[82:83], v[10:11], v[14:15]
	v_cvt_f32_f16_sdwa v15, v105 dst_sel:DWORD dst_unused:UNUSED_PAD src0_sel:WORD_1
	v_cvt_f32_f16_sdwa v14, v104 dst_sel:DWORD dst_unused:UNUSED_PAD src0_sel:WORD_1
	v_pk_fma_f32 v[10:11], v[10:11], s[0:1], v[8:9] op_sel_hi:[1,0,0]
	s_nop 0
	v_cvt_pk_f16_f32 v76, v10, v11
	v_pk_add_f32 v[10:11], v[12:13], 1.0 op_sel_hi:[1,0]
	s_waitcnt vmcnt(4)
	v_cvt_f32_f16_e32 v13, v99
	v_cvt_f32_f16_e32 v12, v98
	v_pk_fma_f32 v[10:11], v[84:85], v[10:11], v[14:15]
	v_cvt_f32_f16_sdwa v15, v99 dst_sel:DWORD dst_unused:UNUSED_PAD src0_sel:WORD_1
	v_cvt_f32_f16_sdwa v14, v98 dst_sel:DWORD dst_unused:UNUSED_PAD src0_sel:WORD_1
	v_pk_fma_f32 v[10:11], v[10:11], s[0:1], v[8:9] op_sel_hi:[1,0,0]
	s_nop 0
	v_cvt_pk_f16_f32 v77, v10, v11
	v_pk_add_f32 v[10:11], v[12:13], 1.0 op_sel_hi:[1,0]
	v_cvt_f32_f16_e32 v13, v101
	v_cvt_f32_f16_e32 v12, v100
	v_pk_fma_f32 v[10:11], v[78:79], v[10:11], v[14:15]
	v_cvt_f32_f16_sdwa v15, v101 dst_sel:DWORD dst_unused:UNUSED_PAD src0_sel:WORD_1
	v_cvt_f32_f16_sdwa v14, v100 dst_sel:DWORD dst_unused:UNUSED_PAD src0_sel:WORD_1
	v_pk_fma_f32 v[10:11], v[10:11], s[0:1], v[8:9] op_sel_hi:[1,0,0]
	s_nop 0
	v_cvt_pk_f16_f32 v78, v10, v11
	v_pk_add_f32 v[10:11], v[12:13], 1.0 op_sel_hi:[1,0]
	s_waitcnt vmcnt(3)
	v_cvt_f32_f16_e32 v13, v95
	v_cvt_f32_f16_e32 v12, v94
	v_pk_fma_f32 v[10:11], v[80:81], v[10:11], v[14:15]
	v_cvt_f32_f16_sdwa v15, v95 dst_sel:DWORD dst_unused:UNUSED_PAD src0_sel:WORD_1
	v_cvt_f32_f16_sdwa v14, v94 dst_sel:DWORD dst_unused:UNUSED_PAD src0_sel:WORD_1
	v_pk_fma_f32 v[10:11], v[10:11], s[0:1], v[8:9] op_sel_hi:[1,0,0]
	s_nop 0
	v_cvt_pk_f16_f32 v79, v10, v11
	v_pk_add_f32 v[10:11], v[12:13], 1.0 op_sel_hi:[1,0]
	v_cvt_f32_f16_e32 v13, v97
	v_cvt_f32_f16_e32 v12, v96
	v_pk_fma_f32 v[10:11], v[72:73], v[10:11], v[14:15]
	v_cvt_f32_f16_sdwa v15, v97 dst_sel:DWORD dst_unused:UNUSED_PAD src0_sel:WORD_1
	v_cvt_f32_f16_sdwa v14, v96 dst_sel:DWORD dst_unused:UNUSED_PAD src0_sel:WORD_1
	v_pk_fma_f32 v[10:11], v[10:11], s[0:1], v[8:9] op_sel_hi:[1,0,0]
	s_nop 0
	v_cvt_pk_f16_f32 v84, v10, v11
	v_pk_add_f32 v[10:11], v[12:13], 1.0 op_sel_hi:[1,0]
	s_waitcnt vmcnt(2)
	v_cvt_f32_f16_e32 v13, v91
	v_cvt_f32_f16_e32 v12, v90
	v_pk_fma_f32 v[10:11], v[74:75], v[10:11], v[14:15]
	v_cvt_f32_f16_sdwa v15, v91 dst_sel:DWORD dst_unused:UNUSED_PAD src0_sel:WORD_1
	v_cvt_f32_f16_sdwa v14, v90 dst_sel:DWORD dst_unused:UNUSED_PAD src0_sel:WORD_1
	v_pk_fma_f32 v[10:11], v[10:11], s[0:1], v[8:9] op_sel_hi:[1,0,0]
	s_nop 0
	v_cvt_pk_f16_f32 v85, v10, v11
	v_pk_add_f32 v[10:11], v[12:13], 1.0 op_sel_hi:[1,0]
	v_cvt_f32_f16_e32 v13, v93
	v_cvt_f32_f16_e32 v12, v92
	v_pk_fma_f32 v[10:11], v[64:65], v[10:11], v[14:15]
	v_cvt_f32_f16_sdwa v15, v93 dst_sel:DWORD dst_unused:UNUSED_PAD src0_sel:WORD_1
	v_cvt_f32_f16_sdwa v14, v92 dst_sel:DWORD dst_unused:UNUSED_PAD src0_sel:WORD_1
	v_pk_fma_f32 v[10:11], v[10:11], s[0:1], v[8:9] op_sel_hi:[1,0,0]
	s_nop 0
	v_cvt_pk_f16_f32 v86, v10, v11
	v_pk_add_f32 v[10:11], v[12:13], 1.0 op_sel_hi:[1,0]
	s_waitcnt vmcnt(1)
	v_cvt_f32_f16_e32 v13, v5
	v_cvt_f32_f16_e32 v12, v4
	v_cvt_f32_f16_sdwa v5, v5 dst_sel:DWORD dst_unused:UNUSED_PAD src0_sel:WORD_1
	v_cvt_f32_f16_sdwa v4, v4 dst_sel:DWORD dst_unused:UNUSED_PAD src0_sel:WORD_1
	v_pk_fma_f32 v[10:11], v[66:67], v[10:11], v[14:15]
	s_nop 0
	v_pk_fma_f32 v[10:11], v[10:11], s[0:1], v[8:9] op_sel_hi:[1,0,0]
	s_nop 0
	v_cvt_pk_f16_f32 v87, v10, v11
	v_pk_add_f32 v[10:11], v[12:13], 1.0 op_sel_hi:[1,0]
	s_nop 0
	v_pk_fma_f32 v[4:5], v[56:57], v[10:11], v[4:5]
	v_cvt_f32_f16_e32 v11, v7
	v_cvt_f32_f16_e32 v10, v6
	v_cvt_f32_f16_sdwa v7, v7 dst_sel:DWORD dst_unused:UNUSED_PAD src0_sel:WORD_1
	v_cvt_f32_f16_sdwa v6, v6 dst_sel:DWORD dst_unused:UNUSED_PAD src0_sel:WORD_1
	v_pk_fma_f32 v[4:5], v[4:5], s[0:1], v[8:9] op_sel_hi:[1,0,0]
	s_nop 0
	v_cvt_pk_f16_f32 v92, v4, v5
	v_pk_add_f32 v[4:5], v[10:11], 1.0 op_sel_hi:[1,0]
	s_nop 0
	v_pk_fma_f32 v[4:5], v[58:59], v[4:5], v[6:7]
	s_waitcnt vmcnt(0)
	v_cvt_f32_f16_e32 v7, v1
	v_cvt_f32_f16_e32 v6, v0
	v_cvt_f32_f16_sdwa v1, v1 dst_sel:DWORD dst_unused:UNUSED_PAD src0_sel:WORD_1
	v_cvt_f32_f16_sdwa v0, v0 dst_sel:DWORD dst_unused:UNUSED_PAD src0_sel:WORD_1
	v_pk_fma_f32 v[4:5], v[4:5], s[0:1], v[8:9] op_sel_hi:[1,0,0]
	s_nop 0
	v_cvt_pk_f16_f32 v93, v4, v5
	v_pk_add_f32 v[4:5], v[6:7], 1.0 op_sel_hi:[1,0]
	s_nop 0
	v_pk_fma_f32 v[0:1], v[48:49], v[4:5], v[0:1]
	v_cvt_f32_f16_e32 v5, v3
	v_cvt_f32_f16_e32 v4, v2
	v_cvt_f32_f16_sdwa v3, v3 dst_sel:DWORD dst_unused:UNUSED_PAD src0_sel:WORD_1
	v_cvt_f32_f16_sdwa v2, v2 dst_sel:DWORD dst_unused:UNUSED_PAD src0_sel:WORD_1
	v_pk_fma_f32 v[0:1], v[0:1], s[0:1], v[8:9] op_sel_hi:[1,0,0]
	s_nop 0
	v_cvt_pk_f16_f32 v94, v0, v1
	v_pk_add_f32 v[0:1], v[4:5], 1.0 op_sel_hi:[1,0]
	s_nop 0
	v_pk_fma_f32 v[0:1], v[50:51], v[0:1], v[2:3]
	s_nop 0
	v_pk_fma_f32 v[0:1], v[0:1], s[0:1], v[8:9] op_sel_hi:[1,0,0]
	s_nop 0
	v_cvt_pk_f16_f32 v95, v0, v1
	ds_read_b128 v[0:3], v236
	ds_read_b128 v[4:7], v236 offset:2048
	ds_read_b128 v[20:23], v237
	ds_read_b128 v[24:27], v237 offset:2048
	s_mov_b32 s0, 0
	v_mov_b32_e32 v137, v179
	s_waitcnt lgkmcnt(3)
	v_mfma_f32_16x16x32_f16 v[8:11], v[0:3], v[36:39], 0
	v_mfma_f32_16x16x32_f16 v[12:15], v[0:3], v[52:55], 0
	v_mfma_f32_16x16x32_f16 v[16:19], v[0:3], v[68:71], 0
	v_mfma_f32_16x16x32_f16 v[0:3], v[0:3], v[84:87], 0
	s_waitcnt lgkmcnt(1)
	v_mfma_f32_16x16x32_f16 v[88:91], v[20:23], v[44:47], v[8:11]
	v_mfma_f32_16x16x32_f16 v[80:83], v[20:23], v[60:63], v[12:15]
	v_mfma_f32_16x16x32_f16 v[64:67], v[20:23], v[92:95], v[0:3]
	v_mfma_f32_16x16x32_f16 v[0:3], v[4:7], v[36:39], 0
	v_mfma_f32_16x16x32_f16 v[8:11], v[4:7], v[52:55], 0
	v_mfma_f32_16x16x32_f16 v[12:15], v[4:7], v[68:71], 0
	v_mfma_f32_16x16x32_f16 v[4:7], v[4:7], v[84:87], 0
	s_waitcnt lgkmcnt(0)
	v_mfma_f32_16x16x32_f16 v[56:59], v[24:27], v[44:47], v[0:3]
	v_mfma_f32_16x16x32_f16 v[32:35], v[24:27], v[92:95], v[4:7]
	s_nop 1
	ds_read_b128 v[0:3], v236 offset:4096
	s_nop 1
	ds_read_b128 v[4:7], v236 offset:6144
	ds_read_b128 v[96:99], v237 offset:4096
	ds_read_b128 v[100:103], v237 offset:6144
	v_mfma_f32_16x16x32_f16 v[72:75], v[20:23], v[76:79], v[16:19]
	v_mfma_f32_16x16x32_f16 v[48:51], v[24:27], v[60:63], v[8:11]
	v_mfma_f32_16x16x32_f16 v[40:43], v[24:27], v[76:79], v[12:15]
	s_waitcnt lgkmcnt(3)
	v_mfma_f32_16x16x32_f16 v[8:11], v[0:3], v[36:39], 0
	v_mfma_f32_16x16x32_f16 v[12:15], v[0:3], v[52:55], 0
	v_mfma_f32_16x16x32_f16 v[16:19], v[0:3], v[68:71], 0
	v_mfma_f32_16x16x32_f16 v[0:3], v[0:3], v[84:87], 0
	s_waitcnt lgkmcnt(1)
	v_mfma_f32_16x16x32_f16 v[28:31], v[96:99], v[44:47], v[8:11]
	v_mfma_f32_16x16x32_f16 v[24:27], v[96:99], v[60:63], v[12:15]
	v_mfma_f32_16x16x32_f16 v[20:23], v[96:99], v[76:79], v[16:19]
	v_mfma_f32_16x16x32_f16 v[16:19], v[96:99], v[92:95], v[0:3]
	v_mfma_f32_16x16x32_f16 v[0:3], v[4:7], v[36:39], 0
	v_mfma_f32_16x16x32_f16 v[8:11], v[4:7], v[52:55], 0
	v_mfma_f32_16x16x32_f16 v[96:99], v[4:7], v[68:71], 0
	v_mfma_f32_16x16x32_f16 v[104:107], v[4:7], v[84:87], 0
	s_waitcnt lgkmcnt(0)
	v_mfma_f32_16x16x32_f16 v[12:15], v[100:103], v[44:47], v[0:3]
	v_mfma_f32_16x16x32_f16 v[8:11], v[100:103], v[60:63], v[8:11]
	v_mfma_f32_16x16x32_f16 v[4:7], v[100:103], v[76:79], v[96:99]
	v_mfma_f32_16x16x32_f16 v[0:3], v[100:103], v[92:95], v[104:107]
.LBB3_45:
	v_add_u32_e32 v100, 0, v194
	s_nop 0
	ds_read_b128 v[96:99], v100
	ds_read_b128 v[100:103], v100 offset:2048
	s_waitcnt lgkmcnt(1)
	v_mfma_f32_16x16x32_f16 v[104:107], v[96:99], v[36:39], 0
	v_mfma_f32_16x16x32_f16 v[108:111], v[96:99], v[52:55], 0
	v_mfma_f32_16x16x32_f16 v[112:115], v[96:99], v[68:71], 0
	v_mfma_f32_16x16x32_f16 v[116:119], v[96:99], v[84:87], 0
	v_add_u32_e32 v96, 0, v195
	ds_read_b128 v[124:127], v96
	ds_read_b128 v[128:131], v96 offset:2048
	s_waitcnt lgkmcnt(1)
	v_mfma_f32_16x16x32_f16 v[120:123], v[124:127], v[44:47], v[104:107]
	v_mfma_f32_16x16x32_f16 v[108:111], v[124:127], v[60:63], v[108:111]
	v_mfma_f32_16x16x32_f16 v[96:99], v[124:127], v[76:79], v[112:115]
	v_mfma_f32_16x16x32_f16 v[142:145], v[124:127], v[92:95], v[116:119]
	v_mfma_f32_16x16x32_f16 v[104:107], v[100:103], v[36:39], 0
	v_mfma_f32_16x16x32_f16 v[112:115], v[100:103], v[52:55], 0
	v_mfma_f32_16x16x32_f16 v[124:127], v[100:103], v[68:71], 0
	v_mfma_f32_16x16x32_f16 v[132:135], v[100:103], v[84:87], 0
	s_waitcnt lgkmcnt(0)
	v_mfma_f32_16x16x32_f16 v[116:119], v[128:131], v[44:47], v[104:107]
	v_mfma_f32_16x16x32_f16 v[112:115], v[128:131], v[60:63], v[112:115]
	v_mfma_f32_16x16x32_f16 v[100:103], v[128:131], v[76:79], v[124:127]
	v_mfma_f32_16x16x32_f16 v[128:131], v[128:131], v[92:95], v[132:135]
	v_add_u32_e32 v140, 0, v137
	v_add_u32_e32 v104, 0x12600, v140
	ds_read_b128 v[104:107], v104
	v_add_u32_e32 v124, 0x12620, v140
	ds_read_b64 v[146:147], v124
	v_add_u32_e32 v124, 0x12610, v140
	ds_read_b128 v[124:127], v124
	s_waitcnt lgkmcnt(2)
	v_fma_f32 v132, v104, v120, v108
	v_fma_f32 v132, -v105, v121, v132
	v_fma_f32 v133, v104, v121, v109
	v_fmac_f32_e32 v133, v105, v120
	v_fma_f32 v134, v104, v132, v96
	v_fma_f32 v134, -v105, v133, v134
	v_fma_f32 v133, v104, v133, v97
	v_fmac_f32_e32 v133, v105, v132
	v_fma_f32 v132, v104, v134, v142
	v_fma_f32 v132, -v105, v133, v132
	v_fma_f32 v143, v104, v133, v143
	v_fmac_f32_e32 v143, v105, v134
	v_mov_b32_dpp v133, v132 row_shr:1 row_mask:0xf bank_mask:0xf bound_ctrl:1
	v_fmac_f32_e32 v132, v106, v133
	v_mov_b32_dpp v134, v143 row_shr:1 row_mask:0xf bank_mask:0xf bound_ctrl:1
	v_fma_f32 v132, -v107, v134, v132
	v_fmac_f32_e32 v143, v106, v134
	v_fmac_f32_e32 v143, v107, v133
	v_mov_b32_dpp v106, v132 row_shr:2 row_mask:0xf bank_mask:0xf bound_ctrl:1
	v_add_u32_e32 v133, 0x12660, v140
	v_mov_b32_dpp v107, v143 row_shr:2 row_mask:0xf bank_mask:0xf bound_ctrl:1
	ds_read_b64 v[148:149], v133
	s_waitcnt lgkmcnt(1)
	v_fmac_f32_e32 v132, v124, v106
	v_fma_f32 v132, -v125, v107, v132
	v_fmac_f32_e32 v143, v124, v107
	v_fmac_f32_e32 v143, v125, v106
	v_mov_b32_dpp v106, v132 row_shr:4 row_mask:0xf bank_mask:0xf bound_ctrl:1
	v_fmac_f32_e32 v132, v126, v106
	v_mov_b32_dpp v107, v143 row_shr:4 row_mask:0xf bank_mask:0xf bound_ctrl:1
	v_fma_f32 v124, -v127, v107, v132
	v_fmac_f32_e32 v143, v126, v107
	v_fmac_f32_e32 v143, v127, v106
	v_mov_b32_dpp v106, v124 row_shr:8 row_mask:0xf bank_mask:0xf bound_ctrl:1
	v_fmac_f32_e32 v124, v146, v106
	v_mov_b32_dpp v107, v143 row_shr:8 row_mask:0xf bank_mask:0xf bound_ctrl:1
	v_fma_f32 v142, -v147, v107, v124
	v_add_u32_e32 v124, 0x12640, v140
	v_add_u32_e32 v125, 0x12650, v140
	ds_read_b128 v[132:135], v125
	ds_read_b128 v[124:127], v124
	v_fmac_f32_e32 v143, v146, v107
	v_fmac_f32_e32 v143, v147, v106
	v_xor_b32_e32 v141, 0x80000000, v105
	v_mov_b32_dpp v142, v142 row_shr:1 row_mask:0xf bank_mask:0xf bound_ctrl:1
	s_waitcnt lgkmcnt(0)
	v_fma_f32 v106, v124, v122, v110
	v_fma_f32 v106, -v125, v123, v106
	v_fma_f32 v146, v124, v123, v111
	v_fmac_f32_e32 v146, v125, v122
	v_fma_f32 v147, v124, v106, v98
	v_fma_f32 v147, -v125, v146, v147
	v_fma_f32 v146, v124, v146, v99
	v_fmac_f32_e32 v146, v125, v106
	v_fma_f32 v106, v124, v147, v144
	v_fma_f32 v106, -v125, v146, v106
	v_fmac_f32_e32 v145, v124, v146
	v_fmac_f32_e32 v145, v125, v147
	v_mov_b32_dpp v144, v106 row_shr:1 row_mask:0xf bank_mask:0xf bound_ctrl:1
	v_fmac_f32_e32 v106, v126, v144
	v_mov_b32_dpp v146, v145 row_shr:1 row_mask:0xf bank_mask:0xf bound_ctrl:1
	v_fma_f32 v106, -v127, v146, v106
	v_fmac_f32_e32 v145, v126, v146
	v_fmac_f32_e32 v145, v127, v144
	v_mov_b32_dpp v126, v106 row_shr:2 row_mask:0xf bank_mask:0xf bound_ctrl:1
	v_fmac_f32_e32 v106, v132, v126
	v_mov_b32_dpp v127, v145 row_shr:2 row_mask:0xf bank_mask:0xf bound_ctrl:1
	v_fma_f32 v106, -v133, v127, v106
	v_fmac_f32_e32 v145, v132, v127
	v_fmac_f32_e32 v145, v133, v126
	v_mov_b32_dpp v126, v106 row_shr:4 row_mask:0xf bank_mask:0xf bound_ctrl:1
	v_fmac_f32_e32 v106, v134, v126
	v_mov_b32_dpp v127, v145 row_shr:4 row_mask:0xf bank_mask:0xf bound_ctrl:1
	v_fma_f32 v106, -v135, v127, v106
	v_fmac_f32_e32 v145, v134, v127
	v_fmac_f32_e32 v145, v135, v126
	v_mov_b32_dpp v126, v106 row_shr:8 row_mask:0xf bank_mask:0xf bound_ctrl:1
	v_fmac_f32_e32 v106, v148, v126
	v_mov_b32_dpp v127, v145 row_shr:8 row_mask:0xf bank_mask:0xf bound_ctrl:1
	v_fma_f32 v106, -v149, v127, v106
	v_fmac_f32_e32 v145, v148, v127
	v_add_u32_e32 v127, 0x12820, v140
	v_fmac_f32_e32 v145, v149, v126
	v_add_u32_e32 v126, 0x12800, v140
	ds_read_b64 v[148:149], v127
	ds_read_b128 v[132:135], v126
	v_mov_b32_dpp v150, v106 row_shr:1 row_mask:0xf bank_mask:0xf bound_ctrl:1
	v_add_u32_e32 v106, 0x12810, v140
	v_mov_b32_dpp v151, v145 row_shr:1 row_mask:0xf bank_mask:0xf bound_ctrl:1
	ds_read_b128 v[144:147], v106
	s_waitcnt lgkmcnt(1)
	v_fma_f32 v106, v132, v116, v112
	v_fma_f32 v106, -v133, v117, v106
	v_fma_f32 v126, v132, v117, v113
	v_fmac_f32_e32 v126, v133, v116
	v_fma_f32 v127, v132, v106, v100
	v_fma_f32 v127, -v133, v126, v127
	v_fma_f32 v126, v132, v126, v101
	v_fmac_f32_e32 v126, v133, v106
	v_fma_f32 v152, v132, v126, v129
	v_fma_f32 v106, v132, v127, v128
	v_fmac_f32_e32 v152, v133, v127
	v_fma_f32 v106, -v133, v126, v106
	v_add_u32_e32 v128, 0x12860, v140
	v_mov_b32_dpp v127, v152 row_shr:1 row_mask:0xf bank_mask:0xf bound_ctrl:1
	v_mov_b32_dpp v126, v106 row_shr:1 row_mask:0xf bank_mask:0xf bound_ctrl:1
	v_fmac_f32_e32 v152, v134, v127
	v_fmac_f32_e32 v106, v134, v126
	v_fmac_f32_e32 v152, v135, v126
	v_fma_f32 v106, -v135, v127, v106
	ds_read_b64 v[134:135], v128
	v_mov_b32_dpp v127, v152 row_shr:2 row_mask:0xf bank_mask:0xf bound_ctrl:1
	v_mov_b32_dpp v126, v106 row_shr:2 row_mask:0xf bank_mask:0xf bound_ctrl:1
	s_waitcnt lgkmcnt(1)
	v_fmac_f32_e32 v152, v144, v127
	v_fmac_f32_e32 v106, v144, v126
	v_fmac_f32_e32 v152, v145, v126
	v_fma_f32 v106, -v145, v127, v106
	v_add_u32_e32 v144, 0x12840, v140
	v_mov_b32_dpp v127, v152 row_shr:4 row_mask:0xf bank_mask:0xf bound_ctrl:1
	v_mov_b32_dpp v126, v106 row_shr:4 row_mask:0xf bank_mask:0xf bound_ctrl:1
	v_fmac_f32_e32 v152, v146, v127
	v_fmac_f32_e32 v106, v146, v126
	v_fmac_f32_e32 v152, v147, v126
	v_add_u32_e32 v126, 0x12850, v140
	v_fma_f32 v106, -v147, v127, v106
	ds_read_b128 v[126:129], v126
	ds_read_b128 v[144:147], v144
	v_mov_b32_dpp v154, v106 row_shr:8 row_mask:0xf bank_mask:0xf bound_ctrl:1
	v_mov_b32_dpp v155, v152 row_shr:8 row_mask:0xf bank_mask:0xf bound_ctrl:1
	v_fmac_f32_e32 v106, v148, v154
	v_fma_f32 v106, -v149, v155, v106
	v_fmac_f32_e32 v152, v148, v155
	v_fmac_f32_e32 v152, v149, v154
	v_mov_b32_dpp v148, v106 row_shr:1 row_mask:0xf bank_mask:0xf bound_ctrl:1
	s_waitcnt lgkmcnt(0)
	v_fma_f32 v106, v144, v118, v114
	v_fma_f32 v106, -v145, v119, v106
	v_fma_f32 v140, v144, v119, v115
	v_mov_b32_dpp v149, v152 row_shr:1 row_mask:0xf bank_mask:0xf bound_ctrl:1
	v_fmac_f32_e32 v140, v145, v118
	v_fma_f32 v152, v144, v106, v102
	v_fma_f32 v152, -v145, v140, v152
	v_fma_f32 v140, v144, v140, v103
	v_fmac_f32_e32 v140, v145, v106
	v_fma_f32 v106, v144, v152, v130
	v_fmac_f32_e32 v131, v144, v140
	v_fma_f32 v106, -v145, v140, v106
	v_fmac_f32_e32 v131, v145, v152
	v_mov_b32_dpp v143, v143 row_shr:1 row_mask:0xf bank_mask:0xf bound_ctrl:1
	v_mov_b32_dpp v130, v106 row_shr:1 row_mask:0xf bank_mask:0xf bound_ctrl:1
	v_mov_b32_dpp v140, v131 row_shr:1 row_mask:0xf bank_mask:0xf bound_ctrl:1
	v_fmac_f32_e32 v106, v146, v130
	v_fmac_f32_e32 v131, v146, v140
	v_fma_f32 v106, -v147, v140, v106
	v_fmac_f32_e32 v131, v147, v130
	v_xor_b32_e32 v107, 0x80000000, v125
	v_mov_b32_dpp v130, v106 row_shr:2 row_mask:0xf bank_mask:0xf bound_ctrl:1
	v_mov_b32_dpp v140, v131 row_shr:2 row_mask:0xf bank_mask:0xf bound_ctrl:1
	v_fmac_f32_e32 v106, v126, v130
	v_fmac_f32_e32 v131, v126, v140
	v_fma_f32 v106, -v127, v140, v106
	v_fmac_f32_e32 v131, v127, v130
	v_xor_b32_e32 v153, 0x80000000, v133
	v_mov_b32_dpp v126, v106 row_shr:4 row_mask:0xf bank_mask:0xf bound_ctrl:1
	v_mov_b32_dpp v127, v131 row_shr:4 row_mask:0xf bank_mask:0xf bound_ctrl:1
	v_fmac_f32_e32 v106, v128, v126
	v_fmac_f32_e32 v131, v128, v127
	v_fma_f32 v106, -v129, v127, v106
	v_fmac_f32_e32 v131, v129, v126
	v_xor_b32_e32 v155, 0x80000000, v145
	v_mov_b32_dpp v126, v106 row_shr:8 row_mask:0xf bank_mask:0xf bound_ctrl:1
	v_mov_b32_dpp v127, v131 row_shr:8 row_mask:0xf bank_mask:0xf bound_ctrl:1
	v_fmac_f32_e32 v106, v134, v126
	v_fmac_f32_e32 v131, v134, v127
	v_fma_f32 v106, -v135, v127, v106
	v_fmac_f32_e32 v131, v135, v126
	s_nop 0
	v_mov_b32_dpp v126, v106 row_shr:1 row_mask:0xf bank_mask:0xf bound_ctrl:1
	v_mov_b32_dpp v127, v131 row_shr:1 row_mask:0xf bank_mask:0xf bound_ctrl:1
	v_pk_fma_f32 v[120:121], v[104:105], v[142:143], v[120:121] op_sel_hi:[0,1,1]
	v_pk_fma_f32 v[128:129], v[132:133], v[148:149], v[116:117] op_sel_hi:[0,1,1]
	v_pk_fma_f32 v[122:123], v[124:125], v[150:151], v[122:123] op_sel_hi:[0,1,1]
	v_pk_fma_f32 v[130:131], v[144:145], v[126:127], v[118:119] op_sel_hi:[0,1,1]
	v_cvt_pk_f16_f32 v119, v126, v127
	v_add_u32_e32 v134, s0, v189
	v_pk_fma_f32 v[120:121], v[104:105], v[142:143], v[120:121] op_sel:[1,0,1] op_sel_hi:[1,1,0] neg_hi:[1,0,0]
	v_pk_fma_f32 v[128:129], v[132:133], v[148:149], v[128:129] op_sel:[1,0,1] op_sel_hi:[1,1,0] neg_hi:[1,0,0]
	v_pk_fma_f32 v[122:123], v[124:125], v[150:151], v[122:123] op_sel:[1,0,1] op_sel_hi:[1,1,0] neg_hi:[1,0,0]
	v_pk_fma_f32 v[126:127], v[144:145], v[126:127], v[130:131] op_sel:[1,0,1] op_sel_hi:[1,1,0] neg_hi:[1,0,0]
	v_mov_b32_e32 v140, v105
	v_mov_b32_e32 v152, v133
	v_mov_b32_e32 v106, v125
	v_mov_b32_e32 v154, v145
	v_cvt_pk_f16_f32 v116, v142, v143
	v_xor_b32_e32 v142, v134, v188
	v_pk_fma_f32 v[130:131], v[104:105], v[120:121], v[108:109] op_sel:[0,1,0] op_sel_hi:[0,0,1]
	v_pk_fma_f32 v[112:113], v[132:133], v[128:129], v[112:113] op_sel:[0,1,0] op_sel_hi:[0,0,1]
	v_pk_fma_f32 v[134:135], v[124:125], v[122:123], v[110:111] op_sel:[0,1,0] op_sel_hi:[0,0,1]
	v_pk_fma_f32 v[114:115], v[144:145], v[126:127], v[114:115] op_sel:[0,1,0] op_sel_hi:[0,0,1]
	v_cvt_pk_f16_f32 v111, v127, v126
	v_cvt_pk_f16_f32 v110, v129, v128
	v_lshl_add_u32 v142, v142, 4, v190
	v_pk_fma_f32 v[130:131], v[140:141], v[120:121], v[130:131] op_sel:[1,0,0] op_sel_hi:[0,1,1]
	v_pk_fma_f32 v[128:129], v[152:153], v[128:129], v[112:113] op_sel:[1,0,0] op_sel_hi:[0,1,1]
	v_pk_fma_f32 v[106:107], v[106:107], v[122:123], v[134:135] op_sel:[1,0,0] op_sel_hi:[0,1,1]
	v_pk_fma_f32 v[126:127], v[154:155], v[126:127], v[114:115] op_sel:[1,0,0] op_sel_hi:[0,1,1]
	v_cvt_pk_f16_f32 v109, v123, v122
	v_cvt_pk_f16_f32 v108, v121, v120
	ds_read_b128 v[112:115], v142 offset:32768
	ds_read_b128 v[120:123], v142 offset:36864
	v_pk_fma_f32 v[134:135], v[104:105], v[130:131], v[96:97] op_sel_hi:[0,1,1]
	v_pk_fma_f32 v[100:101], v[132:133], v[128:129], v[100:101] op_sel_hi:[0,1,1]
	v_pk_fma_f32 v[140:141], v[124:125], v[106:107], v[98:99] op_sel_hi:[0,1,1]
	v_pk_fma_f32 v[102:103], v[144:145], v[126:127], v[102:103] op_sel_hi:[0,1,1]
	v_cvt_pk_f16_f32 v97, v106, v107
	v_pk_fma_f32 v[104:105], v[104:105], v[130:131], v[134:135] op_sel:[1,0,1] op_sel_hi:[1,1,0] neg_hi:[1,0,0]
	v_pk_fma_f32 v[100:101], v[132:133], v[128:129], v[100:101] op_sel:[1,0,1] op_sel_hi:[1,1,0] neg_hi:[1,0,0]
	v_pk_fma_f32 v[106:107], v[124:125], v[106:107], v[140:141] op_sel:[1,0,1] op_sel_hi:[1,1,0] neg_hi:[1,0,0]
	v_pk_fma_f32 v[102:103], v[144:145], v[126:127], v[102:103] op_sel:[1,0,1] op_sel_hi:[1,1,0] neg_hi:[1,0,0]
	v_cvt_pk_f16_f32 v104, v104, v105
	v_cvt_pk_f16_f32 v105, v100, v101
	v_cvt_pk_f16_f32 v100, v106, v107
	v_cvt_pk_f16_f32 v103, v102, v103
	v_cvt_pk_f16_f32 v118, v148, v149
	v_cvt_pk_f16_f32 v117, v150, v151
	v_cvt_pk_f16_f32 v99, v126, v127
	v_cvt_pk_f16_f32 v98, v128, v129
	v_cvt_pk_f16_f32 v96, v130, v131
	v_alignbit_b32 v101, v100, v100, 16
	v_alignbit_b32 v100, v104, v104, 16
	v_alignbit_b32 v102, v105, v105, 16
	v_alignbit_b32 v103, v103, v103, 16
	s_waitcnt lgkmcnt(1)
	v_mfma_f32_16x16x32_f16 v[88:91], v[112:115], v[116:119], v[88:91]
	s_add_i32 s0, s0, 4
	v_add_u32_e32 v137, 0x400, v137
	v_add_u32_e32 v194, 0x1000, v194
	v_mfma_f32_16x16x32_f16 v[80:83], v[112:115], v[108:111], v[80:83]
	s_cmp_lg_u32 s0, 16
	v_add_u32_e32 v195, 0x1000, v195
	v_mfma_f32_16x16x32_f16 v[72:75], v[112:115], v[96:99], v[72:75]
	v_mfma_f32_16x16x32_f16 v[64:67], v[112:115], v[100:103], v[64:67]
	ds_read_b128 v[104:107], v142 offset:40960
	ds_read_b128 v[112:115], v142 offset:45056
	s_waitcnt lgkmcnt(2)
	v_mfma_f32_16x16x32_f16 v[56:59], v[120:123], v[116:119], v[56:59]
	v_mfma_f32_16x16x32_f16 v[48:51], v[120:123], v[108:111], v[48:51]
	v_mfma_f32_16x16x32_f16 v[40:43], v[120:123], v[96:99], v[40:43]
	v_mfma_f32_16x16x32_f16 v[32:35], v[120:123], v[100:103], v[32:35]
	s_waitcnt lgkmcnt(1)
	v_mfma_f32_16x16x32_f16 v[28:31], v[104:107], v[116:119], v[28:31]
	v_mfma_f32_16x16x32_f16 v[24:27], v[104:107], v[108:111], v[24:27]
	v_mfma_f32_16x16x32_f16 v[20:23], v[104:107], v[96:99], v[20:23]
	v_mfma_f32_16x16x32_f16 v[16:19], v[104:107], v[100:103], v[16:19]
	s_waitcnt lgkmcnt(0)
	v_mfma_f32_16x16x32_f16 v[12:15], v[112:115], v[116:119], v[12:15]
	v_mfma_f32_16x16x32_f16 v[8:11], v[112:115], v[108:111], v[8:11]
	v_mfma_f32_16x16x32_f16 v[4:7], v[112:115], v[96:99], v[4:7]
	v_mfma_f32_16x16x32_f16 v[0:3], v[112:115], v[100:103], v[0:3]
	s_cbranch_scc1 .LBB3_45
	s_mov_b32 s0, 0
.LBB3_47:
	v_add_u32_e32 v100, 0, v175
	ds_read_b128 v[96:99], v100
	ds_read_b128 v[100:103], v100 offset:2048
	s_waitcnt lgkmcnt(1)
	v_mfma_f32_16x16x32_f16 v[104:107], v[96:99], v[36:39], 0
	v_mfma_f32_16x16x32_f16 v[108:111], v[96:99], v[52:55], 0
	v_mfma_f32_16x16x32_f16 v[112:115], v[96:99], v[68:71], 0
	v_mfma_f32_16x16x32_f16 v[116:119], v[96:99], v[84:87], 0
	v_add_u32_e32 v96, 0, v174
	ds_read_b128 v[120:123], v96
	ds_read_b128 v[124:127], v96 offset:2048
	s_waitcnt lgkmcnt(1)
	v_mfma_f32_16x16x32_f16 v[132:135], v[120:123], v[44:47], v[104:107]
	v_mfma_f32_16x16x32_f16 v[96:99], v[120:123], v[60:63], v[108:111]
	v_mfma_f32_16x16x32_f16 v[104:107], v[120:123], v[76:79], v[112:115]
	v_mfma_f32_16x16x32_f16 v[120:123], v[120:123], v[92:95], v[116:119]
	v_mfma_f32_16x16x32_f16 v[108:111], v[100:103], v[36:39], 0
	v_mfma_f32_16x16x32_f16 v[112:115], v[100:103], v[52:55], 0
	v_mfma_f32_16x16x32_f16 v[116:119], v[100:103], v[68:71], 0
	v_mfma_f32_16x16x32_f16 v[140:143], v[100:103], v[84:87], 0
	s_waitcnt lgkmcnt(0)
	v_mfma_f32_16x16x32_f16 v[128:131], v[124:127], v[44:47], v[108:111]
	v_mfma_f32_16x16x32_f16 v[100:103], v[124:127], v[60:63], v[112:115]
	v_mfma_f32_16x16x32_f16 v[112:115], v[124:127], v[76:79], v[116:119]
	v_mfma_f32_16x16x32_f16 v[116:119], v[124:127], v[92:95], v[140:143]
	v_add_u32_e32 v137, 0, v179
	v_add_u32_e32 v108, 0x12600, v137
	ds_read_b128 v[108:111], v108
	v_add_u32_e32 v124, 0x12620, v137
	ds_read_b64 v[144:145], v124
	v_add_u32_e32 v124, 0x12610, v137
	ds_read_b128 v[124:127], v124
	s_waitcnt lgkmcnt(2)
	v_fma_f32 v140, v108, v120, v104
	v_fma_f32 v140, -v109, v121, v140
	v_fma_f32 v141, v108, v121, v105
	v_fmac_f32_e32 v141, v109, v120
	v_fma_f32 v142, v108, v140, v96
	v_fma_f32 v142, -v109, v141, v142
	v_fma_f32 v141, v108, v141, v97
	v_fmac_f32_e32 v141, v109, v140
	v_fma_f32 v132, v108, v142, v132
	v_fma_f32 v132, -v109, v141, v132
	v_fma_f32 v146, v108, v141, v133
	v_fmac_f32_e32 v146, v109, v142
	v_mov_b32_dpp v133, v132 row_shl:1 row_mask:0xf bank_mask:0xf bound_ctrl:1
	v_fmac_f32_e32 v132, v110, v133
	v_mov_b32_dpp v140, v146 row_shl:1 row_mask:0xf bank_mask:0xf bound_ctrl:1
	v_fma_f32 v141, -v111, v140, v132
	v_fmac_f32_e32 v146, v110, v140
	v_fmac_f32_e32 v146, v111, v133
	v_mov_b32_dpp v110, v141 row_shl:2 row_mask:0xf bank_mask:0xf bound_ctrl:1
	v_add_u32_e32 v132, 0x12660, v137
	v_mov_b32_dpp v111, v146 row_shl:2 row_mask:0xf bank_mask:0xf bound_ctrl:1
	ds_read_b64 v[132:133], v132
	s_waitcnt lgkmcnt(1)
	v_fmac_f32_e32 v141, v124, v110
	v_fma_f32 v140, -v125, v111, v141
	v_fmac_f32_e32 v146, v124, v111
	v_fmac_f32_e32 v146, v125, v110
	v_mov_b32_dpp v110, v140 row_shl:4 row_mask:0xf bank_mask:0xf bound_ctrl:1
	v_fmac_f32_e32 v140, v126, v110
	v_mov_b32_dpp v111, v146 row_shl:4 row_mask:0xf bank_mask:0xf bound_ctrl:1
	v_fma_f32 v124, -v127, v111, v140
	v_fmac_f32_e32 v146, v126, v111
	v_fmac_f32_e32 v146, v127, v110
	v_mov_b32_dpp v110, v124 row_shl:8 row_mask:0xf bank_mask:0xf bound_ctrl:1
	v_fmac_f32_e32 v124, v144, v110
	v_mov_b32_dpp v111, v146 row_shl:8 row_mask:0xf bank_mask:0xf bound_ctrl:1
	v_fma_f32 v147, -v145, v111, v124
	v_add_u32_e32 v124, 0x12640, v137
	v_add_u32_e32 v125, 0x12650, v137
	ds_read_b128 v[140:143], v125
	ds_read_b128 v[124:127], v124
	v_fmac_f32_e32 v146, v144, v111
	v_fmac_f32_e32 v146, v145, v110
	v_mov_b32_dpp v110, v147 row_shl:1 row_mask:0xf bank_mask:0xf bound_ctrl:1
	s_waitcnt lgkmcnt(0)
	v_fma_f32 v144, v124, v122, v106
	v_fma_f32 v144, -v125, v123, v144
	v_fma_f32 v145, v124, v123, v107
	v_mov_b32_dpp v111, v146 row_shl:1 row_mask:0xf bank_mask:0xf bound_ctrl:1
	v_fmac_f32_e32 v145, v125, v122
	v_fma_f32 v146, v124, v144, v98
	v_fma_f32 v146, -v125, v145, v146
	v_fma_f32 v145, v124, v145, v99
	v_fmac_f32_e32 v145, v125, v144
	v_fma_f32 v134, v124, v146, v134
	v_fma_f32 v134, -v125, v145, v134
	v_fmac_f32_e32 v135, v124, v145
	v_fmac_f32_e32 v135, v125, v146
	v_mov_b32_dpp v144, v134 row_shl:1 row_mask:0xf bank_mask:0xf bound_ctrl:1
	v_fmac_f32_e32 v134, v126, v144
	v_mov_b32_dpp v145, v135 row_shl:1 row_mask:0xf bank_mask:0xf bound_ctrl:1
	v_fma_f32 v134, -v127, v145, v134
	v_fmac_f32_e32 v135, v126, v145
	v_fmac_f32_e32 v135, v127, v144
	v_mov_b32_dpp v126, v134 row_shl:2 row_mask:0xf bank_mask:0xf bound_ctrl:1
	v_fmac_f32_e32 v134, v140, v126
	v_mov_b32_dpp v127, v135 row_shl:2 row_mask:0xf bank_mask:0xf bound_ctrl:1
	v_fma_f32 v134, -v141, v127, v134
	v_fmac_f32_e32 v135, v140, v127
	v_fmac_f32_e32 v135, v141, v126
	v_mov_b32_dpp v126, v134 row_shl:4 row_mask:0xf bank_mask:0xf bound_ctrl:1
	v_fmac_f32_e32 v134, v142, v126
	v_mov_b32_dpp v127, v135 row_shl:4 row_mask:0xf bank_mask:0xf bound_ctrl:1
	v_fma_f32 v134, -v143, v127, v134
	v_fmac_f32_e32 v135, v142, v127
	v_fmac_f32_e32 v135, v143, v126
	v_mov_b32_dpp v126, v134 row_shl:8 row_mask:0xf bank_mask:0xf bound_ctrl:1
	v_fmac_f32_e32 v134, v132, v126
	v_mov_b32_dpp v127, v135 row_shl:8 row_mask:0xf bank_mask:0xf bound_ctrl:1
	v_fma_f32 v134, -v133, v127, v134
	v_fmac_f32_e32 v135, v132, v127
	v_add_u32_e32 v127, 0x12820, v137
	v_fmac_f32_e32 v135, v133, v126
	v_add_u32_e32 v126, 0x12800, v137
	ds_read_b64 v[146:147], v127
	ds_read_b128 v[140:143], v126
	v_add_u32_e32 v132, 0x12810, v137
	v_mov_b32_dpp v126, v134 row_shl:1 row_mask:0xf bank_mask:0xf bound_ctrl:1
	v_mov_b32_dpp v127, v135 row_shl:1 row_mask:0xf bank_mask:0xf bound_ctrl:1
	ds_read_b128 v[132:135], v132
	s_waitcnt lgkmcnt(1)
	v_fma_f32 v144, v140, v116, v112
	v_fma_f32 v144, -v141, v117, v144
	v_fma_f32 v145, v140, v117, v113
	v_fmac_f32_e32 v145, v141, v116
	v_fma_f32 v148, v140, v144, v100
	v_fma_f32 v148, -v141, v145, v148
	v_fma_f32 v145, v140, v145, v101
	v_fmac_f32_e32 v145, v141, v144
	v_fma_f32 v128, v140, v148, v128
	v_fma_f32 v128, -v141, v145, v128
	v_fma_f32 v149, v140, v145, v129
	v_fmac_f32_e32 v149, v141, v148
	v_mov_b32_dpp v129, v128 row_shl:1 row_mask:0xf bank_mask:0xf bound_ctrl:1
	v_fmac_f32_e32 v128, v142, v129
	v_mov_b32_dpp v144, v149 row_shl:1 row_mask:0xf bank_mask:0xf bound_ctrl:1
	v_fma_f32 v145, -v143, v144, v128
	v_fmac_f32_e32 v149, v142, v144
	v_fmac_f32_e32 v149, v143, v129
	v_mov_b32_dpp v142, v145 row_shl:2 row_mask:0xf bank_mask:0xf bound_ctrl:1
	v_add_u32_e32 v128, 0x12860, v137
	v_mov_b32_dpp v143, v149 row_shl:2 row_mask:0xf bank_mask:0xf bound_ctrl:1
	ds_read_b64 v[128:129], v128
	s_waitcnt lgkmcnt(1)
	v_fmac_f32_e32 v145, v132, v142
	v_fma_f32 v144, -v133, v143, v145
	v_fmac_f32_e32 v149, v132, v143
	v_fmac_f32_e32 v149, v133, v142
	v_mov_b32_dpp v132, v144 row_shl:4 row_mask:0xf bank_mask:0xf bound_ctrl:1
	v_fmac_f32_e32 v144, v134, v132
	v_mov_b32_dpp v133, v149 row_shl:4 row_mask:0xf bank_mask:0xf bound_ctrl:1
	v_fma_f32 v142, -v135, v133, v144
	v_fmac_f32_e32 v149, v134, v133
	v_fmac_f32_e32 v149, v135, v132
	v_mov_b32_dpp v148, v142 row_shl:8 row_mask:0xf bank_mask:0xf bound_ctrl:1
	v_fmac_f32_e32 v142, v146, v148
	v_mov_b32_dpp v150, v149 row_shl:8 row_mask:0xf bank_mask:0xf bound_ctrl:1
	v_fma_f32 v151, -v147, v150, v142
	v_add_u32_e32 v142, 0x12840, v137
	v_add_u32_e32 v132, 0x12850, v137
	ds_read_b128 v[132:135], v132
	ds_read_b128 v[142:145], v142
	v_fmac_f32_e32 v149, v146, v150
	v_fmac_f32_e32 v149, v147, v148
	v_mov_b32_dpp v146, v151 row_shl:1 row_mask:0xf bank_mask:0xf bound_ctrl:1
	s_waitcnt lgkmcnt(0)
	v_fma_f32 v137, v142, v118, v114
	v_fma_f32 v137, -v143, v119, v137
	v_fma_f32 v148, v142, v119, v115
	v_mov_b32_dpp v147, v149 row_shl:1 row_mask:0xf bank_mask:0xf bound_ctrl:1
	v_fmac_f32_e32 v148, v143, v118
	v_fma_f32 v149, v142, v137, v102
	v_fma_f32 v149, -v143, v148, v149
	v_fma_f32 v148, v142, v148, v103
	v_fmac_f32_e32 v148, v143, v137
	v_fma_f32 v130, v142, v149, v130
	v_fmac_f32_e32 v131, v142, v148
	v_fma_f32 v130, -v143, v148, v130
	v_fmac_f32_e32 v131, v143, v149
	s_nop 0
	v_mov_b32_dpp v137, v130 row_shl:1 row_mask:0xf bank_mask:0xf bound_ctrl:1
	v_mov_b32_dpp v148, v131 row_shl:1 row_mask:0xf bank_mask:0xf bound_ctrl:1
	v_fmac_f32_e32 v130, v144, v137
	v_fmac_f32_e32 v131, v144, v148
	v_fma_f32 v130, -v145, v148, v130
	v_fmac_f32_e32 v131, v145, v137
	s_nop 0
	v_mov_b32_dpp v137, v130 row_shl:2 row_mask:0xf bank_mask:0xf bound_ctrl:1
	v_mov_b32_dpp v144, v131 row_shl:2 row_mask:0xf bank_mask:0xf bound_ctrl:1
	v_fmac_f32_e32 v130, v132, v137
	v_fmac_f32_e32 v131, v132, v144
	v_fma_f32 v130, -v133, v144, v130
	v_fmac_f32_e32 v131, v133, v137
	s_nop 0
	v_mov_b32_dpp v132, v130 row_shl:4 row_mask:0xf bank_mask:0xf bound_ctrl:1
	v_mov_b32_dpp v133, v131 row_shl:4 row_mask:0xf bank_mask:0xf bound_ctrl:1
	v_fmac_f32_e32 v130, v134, v132
	v_fmac_f32_e32 v131, v134, v133
	v_fma_f32 v130, -v135, v133, v130
	v_fmac_f32_e32 v131, v135, v132
	s_nop 0
	v_mov_b32_dpp v132, v130 row_shl:8 row_mask:0xf bank_mask:0xf bound_ctrl:1
	v_mov_b32_dpp v133, v131 row_shl:8 row_mask:0xf bank_mask:0xf bound_ctrl:1
	v_fmac_f32_e32 v130, v128, v132
	v_fmac_f32_e32 v131, v128, v133
	v_fma_f32 v130, -v129, v133, v130
	v_fmac_f32_e32 v131, v129, v132
	s_nop 0
	v_mov_b32_dpp v128, v130 row_shl:1 row_mask:0xf bank_mask:0xf bound_ctrl:1
	v_mov_b32_dpp v129, v131 row_shl:1 row_mask:0xf bank_mask:0xf bound_ctrl:1
	v_pk_fma_f32 v[130:131], v[108:109], v[110:111], v[120:121] op_sel_hi:[0,1,1]
	v_pk_fma_f32 v[116:117], v[140:141], v[146:147], v[116:117] op_sel_hi:[0,1,1]
	v_pk_fma_f32 v[118:119], v[142:143], v[128:129], v[118:119] op_sel_hi:[0,1,1]
	v_add_u32_e32 v121, s0, v189
	v_cvt_pk_f16_f32 v120, v110, v111
	v_pk_fma_f32 v[122:123], v[124:125], v[126:127], v[122:123] op_sel_hi:[0,1,1]
	v_pk_fma_f32 v[110:111], v[108:109], v[110:111], v[130:131] op_sel:[1,1,0] op_sel_hi:[1,0,1] neg_lo:[1,0,0]
	v_pk_fma_f32 v[130:131], v[140:141], v[146:147], v[116:117] op_sel:[1,1,0] op_sel_hi:[1,0,1] neg_lo:[1,0,0]
	v_pk_fma_f32 v[118:119], v[142:143], v[128:129], v[118:119] op_sel:[1,1,0] op_sel_hi:[1,0,1] neg_lo:[1,0,0]
	v_xor_b32_e32 v121, v121, v188
	v_pk_fma_f32 v[122:123], v[124:125], v[126:127], v[122:123] op_sel:[1,1,0] op_sel_hi:[1,0,1] neg_lo:[1,0,0]
	v_pk_fma_f32 v[116:117], v[108:109], v[110:111], v[104:105] op_sel_hi:[0,1,1]
	v_pk_fma_f32 v[112:113], v[140:141], v[130:131], v[112:113] op_sel_hi:[0,1,1]
	v_pk_fma_f32 v[114:115], v[142:143], v[118:119], v[114:115] op_sel_hi:[0,1,1]
	v_lshl_add_u32 v137, v121, 4, v190
	v_cvt_pk_f16_f32 v104, v110, v111
	v_pk_fma_f32 v[106:107], v[124:125], v[122:123], v[106:107] op_sel_hi:[0,1,1]
	v_pk_fma_f32 v[132:133], v[108:109], v[110:111], v[116:117] op_sel:[1,1,0] op_sel_hi:[1,0,1] neg_lo:[1,0,0]
	v_pk_fma_f32 v[134:135], v[140:141], v[130:131], v[112:113] op_sel:[1,1,0] op_sel_hi:[1,0,1] neg_lo:[1,0,0]
	v_pk_fma_f32 v[144:145], v[142:143], v[118:119], v[114:115] op_sel:[1,1,0] op_sel_hi:[1,0,1] neg_lo:[1,0,0]
	ds_read_b128 v[110:113], v137 offset:49152
	ds_read_b128 v[114:117], v137 offset:53248
	v_pk_fma_f32 v[106:107], v[124:125], v[122:123], v[106:107] op_sel:[1,1,0] op_sel_hi:[1,0,1] neg_lo:[1,0,0]
	v_pk_fma_f32 v[148:149], v[108:109], v[132:133], v[96:97] op_sel_hi:[0,1,1]
	v_pk_fma_f32 v[100:101], v[140:141], v[134:135], v[100:101] op_sel_hi:[0,1,1]
	v_pk_fma_f32 v[98:99], v[124:125], v[106:107], v[98:99] op_sel_hi:[0,1,1]
	v_pk_fma_f32 v[102:103], v[142:143], v[144:145], v[102:103] op_sel_hi:[0,1,1]
	v_cvt_pk_f16_f32 v96, v132, v133
	v_pk_fma_f32 v[108:109], v[108:109], v[132:133], v[148:149] op_sel:[1,1,0] op_sel_hi:[1,0,1] neg_lo:[1,0,0]
	v_pk_fma_f32 v[132:133], v[140:141], v[134:135], v[100:101] op_sel:[1,1,0] op_sel_hi:[1,0,1] neg_lo:[1,0,0]
	v_pk_fma_f32 v[98:99], v[124:125], v[106:107], v[98:99] op_sel:[1,1,0] op_sel_hi:[1,0,1] neg_lo:[1,0,0]
	v_pk_fma_f32 v[124:125], v[142:143], v[144:145], v[102:103] op_sel:[1,1,0] op_sel_hi:[1,0,1] neg_lo:[1,0,0]
	v_cvt_pk_f16_f32 v100, v108, v109
	v_cvt_pk_f16_f32 v102, v132, v133
	v_cvt_pk_f16_f32 v101, v98, v99
	v_cvt_pk_f16_f32 v103, v124, v125
	v_cvt_pk_f16_f32 v98, v134, v135
	v_cvt_pk_f16_f32 v97, v106, v107
	v_cvt_pk_f16_f32 v99, v144, v145
	v_cvt_pk_f16_f32 v106, v130, v131
	v_cvt_pk_f16_f32 v105, v122, v123
	v_cvt_pk_f16_f32 v107, v118, v119
	v_cvt_pk_f16_f32 v122, v146, v147
	v_cvt_pk_f16_f32 v121, v126, v127
	v_cvt_pk_f16_f32 v123, v128, v129
	s_waitcnt lgkmcnt(1)
	v_mfma_f32_16x16x32_f16 v[88:91], v[110:113], v[100:103], v[88:91]
	s_add_i32 s0, s0, 4
	v_add_u32_e32 v179, 0x400, v179
	v_add_u32_e32 v174, 0x1000, v174
	v_mfma_f32_16x16x32_f16 v[80:83], v[110:113], v[96:99], v[80:83]
	s_cmp_lg_u32 s0, 16
	v_add_u32_e32 v175, 0x1000, v175
	v_mfma_f32_16x16x32_f16 v[72:75], v[110:113], v[104:107], v[72:75]
	v_mfma_f32_16x16x32_f16 v[64:67], v[110:113], v[120:123], v[64:67]
	s_waitcnt lgkmcnt(0)
	v_mfma_f32_16x16x32_f16 v[56:59], v[114:117], v[100:103], v[56:59]
	v_mfma_f32_16x16x32_f16 v[48:51], v[114:117], v[96:99], v[48:51]
	v_mfma_f32_16x16x32_f16 v[40:43], v[114:117], v[104:107], v[40:43]
	v_mfma_f32_16x16x32_f16 v[32:35], v[114:117], v[120:123], v[32:35]
	ds_read_b128 v[108:111], v137 offset:57344
	ds_read_b128 v[112:115], v137 offset:61440
	s_waitcnt lgkmcnt(1)
	v_mfma_f32_16x16x32_f16 v[28:31], v[108:111], v[100:103], v[28:31]
	v_mfma_f32_16x16x32_f16 v[24:27], v[108:111], v[96:99], v[24:27]
	v_mfma_f32_16x16x32_f16 v[20:23], v[108:111], v[104:107], v[20:23]
	v_mfma_f32_16x16x32_f16 v[16:19], v[108:111], v[120:123], v[16:19]
	s_waitcnt lgkmcnt(0)
	v_mfma_f32_16x16x32_f16 v[12:15], v[112:115], v[100:103], v[12:15]
	v_mfma_f32_16x16x32_f16 v[8:11], v[112:115], v[96:99], v[8:11]
	v_mfma_f32_16x16x32_f16 v[4:7], v[112:115], v[104:107], v[4:7]
	v_mfma_f32_16x16x32_f16 v[0:3], v[112:115], v[120:123], v[0:3]
	s_cbranch_scc1 .LBB3_47
	s_ashr_i32 s45, s44, 31
	s_lshl_b64 s[0:1], s[44:45], 13
	v_lshl_add_u64 v[38:39], v[138:139], 0, s[0:1]
	s_mov_b32 s1, 0x3f3504f3
	v_mul_f32_e64 v36, |v88|, s1
	s_mov_b32 s3, 0x3ea7ba05
	v_fma_f32 v37, v36, s3, 1.0
	v_rcp_f32_e32 v44, v37
	v_mul_f32_e32 v37, 0xbfb8aa3b, v36
	v_mul_f32_e32 v36, v36, v37
	v_exp_f32_e32 v46, v36
	v_mul_f32_e64 v36, |v89|, s1
	v_fma_f32 v37, v36, s3, 1.0
	v_rcp_f32_e32 v45, v37
	v_mul_f32_e32 v37, 0xbfb8aa3b, v36
	v_mul_f32_e32 v36, v36, v37
	s_mov_b32 s2, 0xbfba00e3
	v_exp_f32_e32 v47, v36
	s_mov_b32 s0, 0x3f87dc22
	v_mov_b64_e32 v[36:37], s[2:3]
	v_pk_fma_f32 v[52:53], v[44:45], s[0:1], v[36:37] op_sel_hi:[1,0,0]
	s_mov_b32 s2, 0x3fb5f0e3
	v_pk_fma_f32 v[52:53], v[44:45], v[52:53], s[2:3] op_sel_hi:[1,1,0]
	s_mov_b32 s4, 0xbe91a98e
	v_pk_fma_f32 v[52:53], v[44:45], v[52:53], s[4:5] op_sel_hi:[1,1,0]
	s_mov_b32 s6, 0x3e827906
	v_pk_fma_f32 v[52:53], v[44:45], v[52:53], s[6:7] op_sel_hi:[1,1,0]
	v_cmp_le_f32_e32 vcc, 0, v89
	v_pk_mul_f32 v[44:45], v[44:45], v[52:53]
	v_mov_b32_e32 v137, 0
	v_pk_mul_f32 v[44:45], v[44:45], 0.5 op_sel_hi:[1,0]
	v_lshl_add_u64 v[38:39], v[38:39], 0, v[136:137]
	v_pk_mul_f32 v[44:45], v[46:47], v[44:45]
	s_nop 0
	v_pk_mul_f32 v[46:47], v[88:89], v[44:45]
	v_pk_fma_f32 v[44:45], v[88:89], v[44:45], v[88:89] neg_lo:[1,0,0] neg_hi:[1,0,0]
	s_nop 0
	v_cndmask_b32_e32 v45, v47, v45, vcc
	v_cmp_le_f32_e32 vcc, 0, v88
	s_nop 1
	v_cndmask_b32_e32 v44, v46, v44, vcc
	v_cvt_pk_f16_f32 v44, v44, v45
	v_mul_f32_e64 v45, |v90|, s1
	v_mul_f32_e32 v47, 0xbfb8aa3b, v45
	v_fma_f32 v46, v45, s3, 1.0
	v_mul_f32_e32 v45, v45, v47
	v_exp_f32_e32 v52, v45
	v_mul_f32_e64 v45, |v91|, s1
	v_fma_f32 v47, v45, s3, 1.0
	v_rcp_f32_e32 v46, v46
	v_rcp_f32_e32 v47, v47
	v_mul_f32_e32 v53, 0xbfb8aa3b, v45
	v_mul_f32_e32 v45, v45, v53
	v_exp_f32_e32 v53, v45
	v_pk_fma_f32 v[54:55], v[46:47], s[0:1], v[36:37] op_sel_hi:[1,0,0]
	v_cmp_le_f32_e32 vcc, 0, v91
	v_pk_fma_f32 v[54:55], v[46:47], v[54:55], s[2:3] op_sel_hi:[1,1,0]
	s_nop 0
	v_pk_fma_f32 v[54:55], v[46:47], v[54:55], s[4:5] op_sel_hi:[1,1,0]
	s_nop 0
	v_pk_fma_f32 v[54:55], v[46:47], v[54:55], s[6:7] op_sel_hi:[1,1,0]
	s_nop 0
	v_pk_mul_f32 v[46:47], v[46:47], v[54:55]
	s_nop 0
	v_pk_mul_f32 v[46:47], v[46:47], 0.5 op_sel_hi:[1,0]
	s_nop 0
	v_pk_mul_f32 v[46:47], v[52:53], v[46:47]
	s_nop 0
	v_pk_mul_f32 v[52:53], v[90:91], v[46:47]
	v_pk_fma_f32 v[46:47], v[90:91], v[46:47], v[90:91] neg_lo:[1,0,0] neg_hi:[1,0,0]
	s_nop 0
	v_cndmask_b32_e32 v45, v53, v47, vcc
	v_cmp_le_f32_e32 vcc, 0, v90
	v_mul_f32_e64 v47, |v81|, s1
	s_nop 0
	v_cndmask_b32_e32 v46, v52, v46, vcc
	v_cvt_pk_f16_f32 v45, v46, v45
	global_store_dwordx2 v[38:39], v[44:45], off
	v_mul_f32_e64 v45, |v80|, s1
	v_mul_f32_e32 v46, 0xbfb8aa3b, v45
	v_fma_f32 v44, v45, s3, 1.0
	v_mul_f32_e32 v45, v45, v46
	v_exp_f32_e32 v46, v45
	v_fma_f32 v45, v47, s3, 1.0
	v_rcp_f32_e32 v44, v44
	v_rcp_f32_e32 v45, v45
	v_mul_f32_e32 v52, 0xbfb8aa3b, v47
	v_mul_f32_e32 v47, v47, v52
	v_exp_f32_e32 v47, v47
	v_pk_fma_f32 v[52:53], v[44:45], s[0:1], v[36:37] op_sel_hi:[1,0,0]
	v_cmp_le_f32_e32 vcc, 0, v81
	v_pk_fma_f32 v[52:53], v[44:45], v[52:53], s[2:3] op_sel_hi:[1,1,0]
	s_nop 0
	v_pk_fma_f32 v[52:53], v[44:45], v[52:53], s[4:5] op_sel_hi:[1,1,0]
	s_nop 0
	v_pk_fma_f32 v[52:53], v[44:45], v[52:53], s[6:7] op_sel_hi:[1,1,0]
	s_nop 0
	v_pk_mul_f32 v[44:45], v[44:45], v[52:53]
	s_nop 0
	v_pk_mul_f32 v[44:45], v[44:45], 0.5 op_sel_hi:[1,0]
	s_nop 0
	v_pk_mul_f32 v[44:45], v[46:47], v[44:45]
	s_nop 0
	v_pk_mul_f32 v[46:47], v[80:81], v[44:45]
	v_pk_fma_f32 v[44:45], v[80:81], v[44:45], v[80:81] neg_lo:[1,0,0] neg_hi:[1,0,0]
	s_nop 0
	v_cndmask_b32_e32 v45, v47, v45, vcc
	v_cmp_le_f32_e32 vcc, 0, v80
	s_nop 1
	v_cndmask_b32_e32 v44, v46, v44, vcc
	v_cvt_pk_f16_f32 v44, v44, v45
	v_mul_f32_e64 v45, |v82|, s1
	v_mul_f32_e32 v47, 0xbfb8aa3b, v45
	v_fma_f32 v46, v45, s3, 1.0
	v_mul_f32_e32 v45, v45, v47
	v_exp_f32_e32 v52, v45
	v_mul_f32_e64 v45, |v83|, s1
	v_fma_f32 v47, v45, s3, 1.0
	v_rcp_f32_e32 v46, v46
	v_rcp_f32_e32 v47, v47
	v_mul_f32_e32 v53, 0xbfb8aa3b, v45
	v_mul_f32_e32 v45, v45, v53
	v_exp_f32_e32 v53, v45
	v_pk_fma_f32 v[54:55], v[46:47], s[0:1], v[36:37] op_sel_hi:[1,0,0]
	v_cmp_le_f32_e32 vcc, 0, v83
	v_pk_fma_f32 v[54:55], v[46:47], v[54:55], s[2:3] op_sel_hi:[1,1,0]
	s_nop 0
	v_pk_fma_f32 v[54:55], v[46:47], v[54:55], s[4:5] op_sel_hi:[1,1,0]
	s_nop 0
	v_pk_fma_f32 v[54:55], v[46:47], v[54:55], s[6:7] op_sel_hi:[1,1,0]
	s_nop 0
	v_pk_mul_f32 v[46:47], v[46:47], v[54:55]
	s_nop 0
	v_pk_mul_f32 v[46:47], v[46:47], 0.5 op_sel_hi:[1,0]
	s_nop 0
	v_pk_mul_f32 v[46:47], v[52:53], v[46:47]
	s_nop 0
	v_pk_mul_f32 v[52:53], v[82:83], v[46:47]
	v_pk_fma_f32 v[46:47], v[82:83], v[46:47], v[82:83] neg_lo:[1,0,0] neg_hi:[1,0,0]
	s_nop 0
	v_cndmask_b32_e32 v45, v53, v47, vcc
	v_cmp_le_f32_e32 vcc, 0, v82
	v_mul_f32_e64 v47, |v73|, s1
	s_nop 0
	v_cndmask_b32_e32 v46, v52, v46, vcc
	v_cvt_pk_f16_f32 v45, v46, v45
	global_store_dwordx2 v[38:39], v[44:45], off offset:128
	v_mul_f32_e64 v45, |v72|, s1
	v_mul_f32_e32 v46, 0xbfb8aa3b, v45
	v_fma_f32 v44, v45, s3, 1.0
	v_mul_f32_e32 v45, v45, v46
	v_exp_f32_e32 v46, v45
	v_fma_f32 v45, v47, s3, 1.0
	v_rcp_f32_e32 v44, v44
	v_rcp_f32_e32 v45, v45
	v_mul_f32_e32 v52, 0xbfb8aa3b, v47
	v_mul_f32_e32 v47, v47, v52
	v_exp_f32_e32 v47, v47
	v_pk_fma_f32 v[52:53], v[44:45], s[0:1], v[36:37] op_sel_hi:[1,0,0]
	v_cmp_le_f32_e32 vcc, 0, v73
	v_pk_fma_f32 v[52:53], v[44:45], v[52:53], s[2:3] op_sel_hi:[1,1,0]
	s_nop 0
	v_pk_fma_f32 v[52:53], v[44:45], v[52:53], s[4:5] op_sel_hi:[1,1,0]
	s_nop 0
	v_pk_fma_f32 v[52:53], v[44:45], v[52:53], s[6:7] op_sel_hi:[1,1,0]
	s_nop 0
	v_pk_mul_f32 v[44:45], v[44:45], v[52:53]
	s_nop 0
	v_pk_mul_f32 v[44:45], v[44:45], 0.5 op_sel_hi:[1,0]
	s_nop 0
	v_pk_mul_f32 v[44:45], v[46:47], v[44:45]
	s_nop 0
	v_pk_mul_f32 v[46:47], v[72:73], v[44:45]
	v_pk_fma_f32 v[44:45], v[72:73], v[44:45], v[72:73] neg_lo:[1,0,0] neg_hi:[1,0,0]
	s_nop 0
	v_cndmask_b32_e32 v45, v47, v45, vcc
	v_cmp_le_f32_e32 vcc, 0, v72
	s_nop 1
	v_cndmask_b32_e32 v44, v46, v44, vcc
	v_cvt_pk_f16_f32 v44, v44, v45
	v_mul_f32_e64 v45, |v74|, s1
	v_mul_f32_e32 v47, 0xbfb8aa3b, v45
	v_fma_f32 v46, v45, s3, 1.0
	v_mul_f32_e32 v45, v45, v47
	v_exp_f32_e32 v52, v45
	v_mul_f32_e64 v45, |v75|, s1
	v_fma_f32 v47, v45, s3, 1.0
	v_rcp_f32_e32 v46, v46
	v_rcp_f32_e32 v47, v47
	v_mul_f32_e32 v53, 0xbfb8aa3b, v45
	v_mul_f32_e32 v45, v45, v53
	v_exp_f32_e32 v53, v45
	v_pk_fma_f32 v[54:55], v[46:47], s[0:1], v[36:37] op_sel_hi:[1,0,0]
	v_cmp_le_f32_e32 vcc, 0, v75
	v_pk_fma_f32 v[54:55], v[46:47], v[54:55], s[2:3] op_sel_hi:[1,1,0]
	s_nop 0
	v_pk_fma_f32 v[54:55], v[46:47], v[54:55], s[4:5] op_sel_hi:[1,1,0]
	s_nop 0
	v_pk_fma_f32 v[54:55], v[46:47], v[54:55], s[6:7] op_sel_hi:[1,1,0]
	s_nop 0
	v_pk_mul_f32 v[46:47], v[46:47], v[54:55]
	s_nop 0
	v_pk_mul_f32 v[46:47], v[46:47], 0.5 op_sel_hi:[1,0]
	s_nop 0
	v_pk_mul_f32 v[46:47], v[52:53], v[46:47]
	s_nop 0
	v_pk_mul_f32 v[52:53], v[74:75], v[46:47]
	v_pk_fma_f32 v[46:47], v[74:75], v[46:47], v[74:75] neg_lo:[1,0,0] neg_hi:[1,0,0]
	s_nop 0
	v_cndmask_b32_e32 v45, v53, v47, vcc
	v_cmp_le_f32_e32 vcc, 0, v74
	v_mul_f32_e64 v47, |v65|, s1
	s_nop 0
	v_cndmask_b32_e32 v46, v52, v46, vcc
	v_cvt_pk_f16_f32 v45, v46, v45
	global_store_dwordx2 v[38:39], v[44:45], off offset:256
	v_mul_f32_e64 v45, |v64|, s1
	v_mul_f32_e32 v46, 0xbfb8aa3b, v45
	v_fma_f32 v44, v45, s3, 1.0
	v_mul_f32_e32 v45, v45, v46
	v_exp_f32_e32 v46, v45
	v_fma_f32 v45, v47, s3, 1.0
	v_rcp_f32_e32 v44, v44
	v_rcp_f32_e32 v45, v45
	v_mul_f32_e32 v52, 0xbfb8aa3b, v47
	v_mul_f32_e32 v47, v47, v52
	v_exp_f32_e32 v47, v47
	v_pk_fma_f32 v[52:53], v[44:45], s[0:1], v[36:37] op_sel_hi:[1,0,0]
	v_cmp_le_f32_e32 vcc, 0, v65
	v_pk_fma_f32 v[52:53], v[44:45], v[52:53], s[2:3] op_sel_hi:[1,1,0]
	s_nop 0
	v_pk_fma_f32 v[52:53], v[44:45], v[52:53], s[4:5] op_sel_hi:[1,1,0]
	s_nop 0
	v_pk_fma_f32 v[52:53], v[44:45], v[52:53], s[6:7] op_sel_hi:[1,1,0]
	s_nop 0
	v_pk_mul_f32 v[44:45], v[44:45], v[52:53]
	s_nop 0
	v_pk_mul_f32 v[44:45], v[44:45], 0.5 op_sel_hi:[1,0]
	s_nop 0
	v_pk_mul_f32 v[44:45], v[46:47], v[44:45]
	s_nop 0
	v_pk_mul_f32 v[46:47], v[64:65], v[44:45]
	v_pk_fma_f32 v[44:45], v[64:65], v[44:45], v[64:65] neg_lo:[1,0,0] neg_hi:[1,0,0]
	s_nop 0
	v_cndmask_b32_e32 v45, v47, v45, vcc
	v_cmp_le_f32_e32 vcc, 0, v64
	s_nop 1
	v_cndmask_b32_e32 v44, v46, v44, vcc
	v_cvt_pk_f16_f32 v44, v44, v45
	v_mul_f32_e64 v45, |v66|, s1
	v_mul_f32_e32 v47, 0xbfb8aa3b, v45
	v_fma_f32 v46, v45, s3, 1.0
	v_mul_f32_e32 v45, v45, v47
	v_exp_f32_e32 v52, v45
	v_mul_f32_e64 v45, |v67|, s1
	v_fma_f32 v47, v45, s3, 1.0
	v_rcp_f32_e32 v46, v46
	v_rcp_f32_e32 v47, v47
	v_mul_f32_e32 v53, 0xbfb8aa3b, v45
	v_mul_f32_e32 v45, v45, v53
	v_exp_f32_e32 v53, v45
	v_pk_fma_f32 v[54:55], v[46:47], s[0:1], v[36:37] op_sel_hi:[1,0,0]
	v_cmp_le_f32_e32 vcc, 0, v67
	v_pk_fma_f32 v[54:55], v[46:47], v[54:55], s[2:3] op_sel_hi:[1,1,0]
	s_nop 0
	v_pk_fma_f32 v[54:55], v[46:47], v[54:55], s[4:5] op_sel_hi:[1,1,0]
	s_nop 0
	v_pk_fma_f32 v[54:55], v[46:47], v[54:55], s[6:7] op_sel_hi:[1,1,0]
	s_nop 0
	v_pk_mul_f32 v[46:47], v[46:47], v[54:55]
	s_nop 0
	v_pk_mul_f32 v[46:47], v[46:47], 0.5 op_sel_hi:[1,0]
	s_nop 0
	v_pk_mul_f32 v[46:47], v[52:53], v[46:47]
	s_nop 0
	v_pk_mul_f32 v[52:53], v[66:67], v[46:47]
	v_pk_fma_f32 v[46:47], v[66:67], v[46:47], v[66:67] neg_lo:[1,0,0] neg_hi:[1,0,0]
	s_nop 0
	v_cndmask_b32_e32 v45, v53, v47, vcc
	v_cmp_le_f32_e32 vcc, 0, v66
	v_mul_f32_e64 v47, |v57|, s1
	s_nop 0
	v_cndmask_b32_e32 v46, v52, v46, vcc
	v_cvt_pk_f16_f32 v45, v46, v45
	global_store_dwordx2 v[38:39], v[44:45], off offset:384
	v_mul_f32_e64 v45, |v56|, s1
	v_mul_f32_e32 v46, 0xbfb8aa3b, v45
	v_fma_f32 v44, v45, s3, 1.0
	v_mul_f32_e32 v45, v45, v46
	v_exp_f32_e32 v46, v45
	v_fma_f32 v45, v47, s3, 1.0
	v_rcp_f32_e32 v44, v44
	v_rcp_f32_e32 v45, v45
	v_mul_f32_e32 v52, 0xbfb8aa3b, v47
	v_mul_f32_e32 v47, v47, v52
	v_exp_f32_e32 v47, v47
	v_pk_fma_f32 v[52:53], v[44:45], s[0:1], v[36:37] op_sel_hi:[1,0,0]
	v_cmp_le_f32_e32 vcc, 0, v57
	v_pk_fma_f32 v[52:53], v[44:45], v[52:53], s[2:3] op_sel_hi:[1,1,0]
	s_nop 0
	v_pk_fma_f32 v[52:53], v[44:45], v[52:53], s[4:5] op_sel_hi:[1,1,0]
	s_nop 0
	v_pk_fma_f32 v[52:53], v[44:45], v[52:53], s[6:7] op_sel_hi:[1,1,0]
	s_nop 0
	v_pk_mul_f32 v[44:45], v[44:45], v[52:53]
	s_nop 0
	v_pk_mul_f32 v[44:45], v[44:45], 0.5 op_sel_hi:[1,0]
	s_nop 0
	v_pk_mul_f32 v[44:45], v[46:47], v[44:45]
	s_nop 0
	v_pk_mul_f32 v[46:47], v[56:57], v[44:45]
	v_pk_fma_f32 v[44:45], v[56:57], v[44:45], v[56:57] neg_lo:[1,0,0] neg_hi:[1,0,0]
	s_nop 0
	v_cndmask_b32_e32 v45, v47, v45, vcc
	v_cmp_le_f32_e32 vcc, 0, v56
	s_nop 1
	v_cndmask_b32_e32 v44, v46, v44, vcc
	v_cvt_pk_f16_f32 v44, v44, v45
	v_mul_f32_e64 v45, |v58|, s1
	v_mul_f32_e32 v47, 0xbfb8aa3b, v45
	v_fma_f32 v46, v45, s3, 1.0
	v_mul_f32_e32 v45, v45, v47
	v_exp_f32_e32 v52, v45
	v_mul_f32_e64 v45, |v59|, s1
	v_fma_f32 v47, v45, s3, 1.0
	v_rcp_f32_e32 v46, v46
	v_rcp_f32_e32 v47, v47
	v_mul_f32_e32 v53, 0xbfb8aa3b, v45
	v_mul_f32_e32 v45, v45, v53
	v_exp_f32_e32 v53, v45
	v_pk_fma_f32 v[54:55], v[46:47], s[0:1], v[36:37] op_sel_hi:[1,0,0]
	v_cmp_le_f32_e32 vcc, 0, v59
	v_pk_fma_f32 v[54:55], v[46:47], v[54:55], s[2:3] op_sel_hi:[1,1,0]
	s_nop 0
	v_pk_fma_f32 v[54:55], v[46:47], v[54:55], s[4:5] op_sel_hi:[1,1,0]
	s_nop 0
	v_pk_fma_f32 v[54:55], v[46:47], v[54:55], s[6:7] op_sel_hi:[1,1,0]
	s_nop 0
	v_pk_mul_f32 v[46:47], v[46:47], v[54:55]
	s_nop 0
	v_pk_mul_f32 v[46:47], v[46:47], 0.5 op_sel_hi:[1,0]
	s_nop 0
	v_pk_mul_f32 v[46:47], v[52:53], v[46:47]
	s_nop 0
	v_pk_mul_f32 v[52:53], v[58:59], v[46:47]
	v_pk_fma_f32 v[46:47], v[58:59], v[46:47], v[58:59] neg_lo:[1,0,0] neg_hi:[1,0,0]
	s_nop 0
	v_cndmask_b32_e32 v45, v53, v47, vcc
	v_cmp_le_f32_e32 vcc, 0, v58
	v_mul_f32_e64 v47, |v49|, s1
	s_nop 0
	v_cndmask_b32_e32 v46, v52, v46, vcc
	v_cvt_pk_f16_f32 v45, v46, v45
	global_store_dwordx2 v[38:39], v[44:45], off offset:32
	v_mul_f32_e64 v45, |v48|, s1
	v_mul_f32_e32 v46, 0xbfb8aa3b, v45
	v_fma_f32 v44, v45, s3, 1.0
	v_mul_f32_e32 v45, v45, v46
	v_exp_f32_e32 v46, v45
	v_fma_f32 v45, v47, s3, 1.0
	v_rcp_f32_e32 v44, v44
	v_rcp_f32_e32 v45, v45
	v_mul_f32_e32 v52, 0xbfb8aa3b, v47
	v_mul_f32_e32 v47, v47, v52
	v_exp_f32_e32 v47, v47
	v_pk_fma_f32 v[52:53], v[44:45], s[0:1], v[36:37] op_sel_hi:[1,0,0]
	v_cmp_le_f32_e32 vcc, 0, v49
	v_pk_fma_f32 v[52:53], v[44:45], v[52:53], s[2:3] op_sel_hi:[1,1,0]
	s_nop 0
	v_pk_fma_f32 v[52:53], v[44:45], v[52:53], s[4:5] op_sel_hi:[1,1,0]
	s_nop 0
	v_pk_fma_f32 v[52:53], v[44:45], v[52:53], s[6:7] op_sel_hi:[1,1,0]
	s_nop 0
	v_pk_mul_f32 v[44:45], v[44:45], v[52:53]
	s_nop 0
	v_pk_mul_f32 v[44:45], v[44:45], 0.5 op_sel_hi:[1,0]
	s_nop 0
	v_pk_mul_f32 v[44:45], v[46:47], v[44:45]
	s_nop 0
	v_pk_mul_f32 v[46:47], v[48:49], v[44:45]
	v_pk_fma_f32 v[44:45], v[48:49], v[44:45], v[48:49] neg_lo:[1,0,0] neg_hi:[1,0,0]
	s_nop 0
	v_cndmask_b32_e32 v45, v47, v45, vcc
	v_cmp_le_f32_e32 vcc, 0, v48
	s_nop 1
	v_cndmask_b32_e32 v44, v46, v44, vcc
	v_cvt_pk_f16_f32 v44, v44, v45
	v_mul_f32_e64 v45, |v50|, s1
	v_mul_f32_e32 v47, 0xbfb8aa3b, v45
	v_fma_f32 v46, v45, s3, 1.0
	v_mul_f32_e32 v45, v45, v47
	v_exp_f32_e32 v48, v45
	v_mul_f32_e64 v45, |v51|, s1
	v_fma_f32 v47, v45, s3, 1.0
	v_rcp_f32_e32 v46, v46
	v_rcp_f32_e32 v47, v47
	v_mul_f32_e32 v49, 0xbfb8aa3b, v45
	v_mul_f32_e32 v45, v45, v49
	v_exp_f32_e32 v49, v45
	v_pk_fma_f32 v[52:53], v[46:47], s[0:1], v[36:37] op_sel_hi:[1,0,0]
	v_cmp_le_f32_e32 vcc, 0, v51
	v_pk_fma_f32 v[52:53], v[46:47], v[52:53], s[2:3] op_sel_hi:[1,1,0]
	s_nop 0
	v_pk_fma_f32 v[52:53], v[46:47], v[52:53], s[4:5] op_sel_hi:[1,1,0]
	s_nop 0
	v_pk_fma_f32 v[52:53], v[46:47], v[52:53], s[6:7] op_sel_hi:[1,1,0]
	s_nop 0
	v_pk_mul_f32 v[46:47], v[46:47], v[52:53]
	s_nop 0
	v_pk_mul_f32 v[46:47], v[46:47], 0.5 op_sel_hi:[1,0]
	s_nop 0
	v_pk_mul_f32 v[46:47], v[48:49], v[46:47]
	s_nop 0
	v_pk_mul_f32 v[48:49], v[50:51], v[46:47]
	v_pk_fma_f32 v[46:47], v[50:51], v[46:47], v[50:51] neg_lo:[1,0,0] neg_hi:[1,0,0]
	s_nop 0
	v_cndmask_b32_e32 v45, v49, v47, vcc
	v_cmp_le_f32_e32 vcc, 0, v50
	v_mul_f32_e64 v47, |v41|, s1
	s_nop 0
	v_cndmask_b32_e32 v46, v48, v46, vcc
	v_cvt_pk_f16_f32 v45, v46, v45
	global_store_dwordx2 v[38:39], v[44:45], off offset:160
	v_mul_f32_e64 v45, |v40|, s1
	v_mul_f32_e32 v46, 0xbfb8aa3b, v45
	v_fma_f32 v44, v45, s3, 1.0
	v_mul_f32_e32 v45, v45, v46
	v_exp_f32_e32 v46, v45
	v_fma_f32 v45, v47, s3, 1.0
	v_rcp_f32_e32 v44, v44
	v_rcp_f32_e32 v45, v45
	v_mul_f32_e32 v48, 0xbfb8aa3b, v47
	v_mul_f32_e32 v47, v47, v48
	v_exp_f32_e32 v47, v47
	v_pk_fma_f32 v[48:49], v[44:45], s[0:1], v[36:37] op_sel_hi:[1,0,0]
	v_cmp_le_f32_e32 vcc, 0, v41
	v_pk_fma_f32 v[48:49], v[44:45], v[48:49], s[2:3] op_sel_hi:[1,1,0]
	s_nop 0
	v_pk_fma_f32 v[48:49], v[44:45], v[48:49], s[4:5] op_sel_hi:[1,1,0]
	s_nop 0
	v_pk_fma_f32 v[48:49], v[44:45], v[48:49], s[6:7] op_sel_hi:[1,1,0]
	s_nop 0
	v_pk_mul_f32 v[44:45], v[44:45], v[48:49]
	s_nop 0
	v_pk_mul_f32 v[44:45], v[44:45], 0.5 op_sel_hi:[1,0]
	s_nop 0
	v_pk_mul_f32 v[44:45], v[46:47], v[44:45]
	s_nop 0
	v_pk_mul_f32 v[46:47], v[40:41], v[44:45]
	v_pk_fma_f32 v[44:45], v[40:41], v[44:45], v[40:41] neg_lo:[1,0,0] neg_hi:[1,0,0]
	s_nop 0
	v_cndmask_b32_e32 v41, v47, v45, vcc
	v_cmp_le_f32_e32 vcc, 0, v40
	s_nop 1
	v_cndmask_b32_e32 v40, v46, v44, vcc
	v_cvt_pk_f16_f32 v40, v40, v41
	v_mul_f32_e64 v41, |v42|, s1
	v_mul_f32_e32 v45, 0xbfb8aa3b, v41
	v_fma_f32 v44, v41, s3, 1.0
	v_mul_f32_e32 v41, v41, v45
	v_exp_f32_e32 v46, v41
	v_mul_f32_e64 v41, |v43|, s1
	v_fma_f32 v45, v41, s3, 1.0
	v_rcp_f32_e32 v44, v44
	v_rcp_f32_e32 v45, v45
	v_mul_f32_e32 v47, 0xbfb8aa3b, v41
	v_mul_f32_e32 v41, v41, v47
	v_exp_f32_e32 v47, v41
	v_pk_fma_f32 v[48:49], v[44:45], s[0:1], v[36:37] op_sel_hi:[1,0,0]
	v_cmp_le_f32_e32 vcc, 0, v43
	v_pk_fma_f32 v[48:49], v[44:45], v[48:49], s[2:3] op_sel_hi:[1,1,0]
	s_nop 0
	v_pk_fma_f32 v[48:49], v[44:45], v[48:49], s[4:5] op_sel_hi:[1,1,0]
	s_nop 0
	v_pk_fma_f32 v[48:49], v[44:45], v[48:49], s[6:7] op_sel_hi:[1,1,0]
	s_nop 0
	v_pk_mul_f32 v[44:45], v[44:45], v[48:49]
	s_nop 0
	v_pk_mul_f32 v[44:45], v[44:45], 0.5 op_sel_hi:[1,0]
	s_nop 0
	v_pk_mul_f32 v[44:45], v[46:47], v[44:45]
	s_nop 0
	v_pk_mul_f32 v[46:47], v[42:43], v[44:45]
	v_pk_fma_f32 v[44:45], v[42:43], v[44:45], v[42:43] neg_lo:[1,0,0] neg_hi:[1,0,0]
	v_mul_f32_e64 v43, |v33|, s1
	v_cndmask_b32_e32 v41, v47, v45, vcc
	v_cmp_le_f32_e32 vcc, 0, v42
	s_nop 1
	v_cndmask_b32_e32 v42, v46, v44, vcc
	v_cvt_pk_f16_f32 v41, v42, v41
	global_store_dwordx2 v[38:39], v[40:41], off offset:288
	v_mul_f32_e64 v41, |v32|, s1
	v_mul_f32_e32 v42, 0xbfb8aa3b, v41
	v_fma_f32 v40, v41, s3, 1.0
	v_mul_f32_e32 v41, v41, v42
	v_exp_f32_e32 v42, v41
	v_fma_f32 v41, v43, s3, 1.0
	v_rcp_f32_e32 v40, v40
	v_rcp_f32_e32 v41, v41
	v_mul_f32_e32 v44, 0xbfb8aa3b, v43
	v_mul_f32_e32 v43, v43, v44
	v_exp_f32_e32 v43, v43
	v_pk_fma_f32 v[44:45], v[40:41], s[0:1], v[36:37] op_sel_hi:[1,0,0]
	v_cmp_le_f32_e32 vcc, 0, v33
	v_pk_fma_f32 v[44:45], v[40:41], v[44:45], s[2:3] op_sel_hi:[1,1,0]
	s_nop 0
	v_pk_fma_f32 v[44:45], v[40:41], v[44:45], s[4:5] op_sel_hi:[1,1,0]
	s_nop 0
	v_pk_fma_f32 v[44:45], v[40:41], v[44:45], s[6:7] op_sel_hi:[1,1,0]
	s_nop 0
	v_pk_mul_f32 v[40:41], v[40:41], v[44:45]
	s_nop 0
	v_pk_mul_f32 v[40:41], v[40:41], 0.5 op_sel_hi:[1,0]
	s_nop 0
	v_pk_mul_f32 v[40:41], v[42:43], v[40:41]
	s_nop 0
	v_pk_mul_f32 v[42:43], v[32:33], v[40:41]
	v_pk_fma_f32 v[40:41], v[32:33], v[40:41], v[32:33] neg_lo:[1,0,0] neg_hi:[1,0,0]
	s_nop 0
	v_cndmask_b32_e32 v33, v43, v41, vcc
	v_cmp_le_f32_e32 vcc, 0, v32
	s_nop 1
	v_cndmask_b32_e32 v32, v42, v40, vcc
	v_cvt_pk_f16_f32 v32, v32, v33
	v_mul_f32_e64 v33, |v34|, s1
	v_mul_f32_e32 v41, 0xbfb8aa3b, v33
	v_fma_f32 v40, v33, s3, 1.0
	v_mul_f32_e32 v33, v33, v41
	v_exp_f32_e32 v42, v33
	v_mul_f32_e64 v33, |v35|, s1
	v_fma_f32 v41, v33, s3, 1.0
	v_rcp_f32_e32 v40, v40
	v_rcp_f32_e32 v41, v41
	v_mul_f32_e32 v43, 0xbfb8aa3b, v33
	v_mul_f32_e32 v33, v33, v43
	v_exp_f32_e32 v43, v33
	v_pk_fma_f32 v[44:45], v[40:41], s[0:1], v[36:37] op_sel_hi:[1,0,0]
	v_cmp_le_f32_e32 vcc, 0, v35
	v_pk_fma_f32 v[44:45], v[40:41], v[44:45], s[2:3] op_sel_hi:[1,1,0]
	s_nop 0
	v_pk_fma_f32 v[44:45], v[40:41], v[44:45], s[4:5] op_sel_hi:[1,1,0]
	s_nop 0
	v_pk_fma_f32 v[44:45], v[40:41], v[44:45], s[6:7] op_sel_hi:[1,1,0]
	s_nop 0
	v_pk_mul_f32 v[40:41], v[40:41], v[44:45]
	s_nop 0
	v_pk_mul_f32 v[40:41], v[40:41], 0.5 op_sel_hi:[1,0]
	s_nop 0
	v_pk_mul_f32 v[40:41], v[42:43], v[40:41]
	s_nop 0
	v_pk_mul_f32 v[42:43], v[34:35], v[40:41]
	v_pk_fma_f32 v[40:41], v[34:35], v[40:41], v[34:35] neg_lo:[1,0,0] neg_hi:[1,0,0]
	v_mul_f32_e64 v35, |v29|, s1
	v_cndmask_b32_e32 v33, v43, v41, vcc
	v_cmp_le_f32_e32 vcc, 0, v34
	s_nop 1
	v_cndmask_b32_e32 v34, v42, v40, vcc
	v_cvt_pk_f16_f32 v33, v34, v33
	global_store_dwordx2 v[38:39], v[32:33], off offset:416
	v_mul_f32_e64 v33, |v28|, s1
	v_mul_f32_e32 v34, 0xbfb8aa3b, v33
	v_fma_f32 v32, v33, s3, 1.0
	v_mul_f32_e32 v33, v33, v34
	v_exp_f32_e32 v34, v33
	v_fma_f32 v33, v35, s3, 1.0
	v_rcp_f32_e32 v32, v32
	v_rcp_f32_e32 v33, v33
	v_mul_f32_e32 v40, 0xbfb8aa3b, v35
	v_mul_f32_e32 v35, v35, v40
	v_exp_f32_e32 v35, v35
	v_pk_fma_f32 v[40:41], v[32:33], s[0:1], v[36:37] op_sel_hi:[1,0,0]
	v_cmp_le_f32_e32 vcc, 0, v29
	v_pk_fma_f32 v[40:41], v[32:33], v[40:41], s[2:3] op_sel_hi:[1,1,0]
	s_nop 0
	v_pk_fma_f32 v[40:41], v[32:33], v[40:41], s[4:5] op_sel_hi:[1,1,0]
	s_nop 0
	v_pk_fma_f32 v[40:41], v[32:33], v[40:41], s[6:7] op_sel_hi:[1,1,0]
	s_nop 0
	v_pk_mul_f32 v[32:33], v[32:33], v[40:41]
	s_nop 0
	v_pk_mul_f32 v[32:33], v[32:33], 0.5 op_sel_hi:[1,0]
	s_nop 0
	v_pk_mul_f32 v[32:33], v[34:35], v[32:33]
	s_nop 0
	v_pk_mul_f32 v[34:35], v[28:29], v[32:33]
	v_pk_fma_f32 v[32:33], v[28:29], v[32:33], v[28:29] neg_lo:[1,0,0] neg_hi:[1,0,0]
	s_nop 0
	v_cndmask_b32_e32 v29, v35, v33, vcc
	v_cmp_le_f32_e32 vcc, 0, v28
	s_nop 1
	v_cndmask_b32_e32 v28, v34, v32, vcc
	v_cvt_pk_f16_f32 v28, v28, v29
	v_mul_f32_e64 v29, |v30|, s1
	v_mul_f32_e32 v33, 0xbfb8aa3b, v29
	v_fma_f32 v32, v29, s3, 1.0
	v_mul_f32_e32 v29, v29, v33
	v_exp_f32_e32 v34, v29
	v_mul_f32_e64 v29, |v31|, s1
	v_fma_f32 v33, v29, s3, 1.0
	v_rcp_f32_e32 v32, v32
	v_rcp_f32_e32 v33, v33
	v_mul_f32_e32 v35, 0xbfb8aa3b, v29
	v_mul_f32_e32 v29, v29, v35
	v_exp_f32_e32 v35, v29
	v_pk_fma_f32 v[40:41], v[32:33], s[0:1], v[36:37] op_sel_hi:[1,0,0]
	v_cmp_le_f32_e32 vcc, 0, v31
	v_pk_fma_f32 v[40:41], v[32:33], v[40:41], s[2:3] op_sel_hi:[1,1,0]
	s_nop 0
	v_pk_fma_f32 v[40:41], v[32:33], v[40:41], s[4:5] op_sel_hi:[1,1,0]
	s_nop 0
	v_pk_fma_f32 v[40:41], v[32:33], v[40:41], s[6:7] op_sel_hi:[1,1,0]
	s_nop 0
	v_pk_mul_f32 v[32:33], v[32:33], v[40:41]
	s_nop 0
	v_pk_mul_f32 v[32:33], v[32:33], 0.5 op_sel_hi:[1,0]
	s_nop 0
	v_pk_mul_f32 v[32:33], v[34:35], v[32:33]
	s_nop 0
	v_pk_mul_f32 v[34:35], v[30:31], v[32:33]
	v_pk_fma_f32 v[32:33], v[30:31], v[32:33], v[30:31] neg_lo:[1,0,0] neg_hi:[1,0,0]
	v_mul_f32_e64 v31, |v25|, s1
	v_cndmask_b32_e32 v29, v35, v33, vcc
	v_cmp_le_f32_e32 vcc, 0, v30
	s_nop 1
	v_cndmask_b32_e32 v30, v34, v32, vcc
	v_cvt_pk_f16_f32 v29, v30, v29
	global_store_dwordx2 v[38:39], v[28:29], off offset:64
	v_mul_f32_e64 v29, |v24|, s1
	v_mul_f32_e32 v30, 0xbfb8aa3b, v29
	v_fma_f32 v28, v29, s3, 1.0
	v_mul_f32_e32 v29, v29, v30
	v_exp_f32_e32 v30, v29
	v_fma_f32 v29, v31, s3, 1.0
	v_rcp_f32_e32 v28, v28
	v_rcp_f32_e32 v29, v29
	v_mul_f32_e32 v32, 0xbfb8aa3b, v31
	v_mul_f32_e32 v31, v31, v32
	v_exp_f32_e32 v31, v31
	v_pk_fma_f32 v[32:33], v[28:29], s[0:1], v[36:37] op_sel_hi:[1,0,0]
	v_cmp_le_f32_e32 vcc, 0, v25
	v_pk_fma_f32 v[32:33], v[28:29], v[32:33], s[2:3] op_sel_hi:[1,1,0]
	s_nop 0
	v_pk_fma_f32 v[32:33], v[28:29], v[32:33], s[4:5] op_sel_hi:[1,1,0]
	s_nop 0
	v_pk_fma_f32 v[32:33], v[28:29], v[32:33], s[6:7] op_sel_hi:[1,1,0]
	s_nop 0
	v_pk_mul_f32 v[28:29], v[28:29], v[32:33]
	s_nop 0
	v_pk_mul_f32 v[28:29], v[28:29], 0.5 op_sel_hi:[1,0]
	s_nop 0
	v_pk_mul_f32 v[28:29], v[30:31], v[28:29]
	s_nop 0
	v_pk_mul_f32 v[30:31], v[24:25], v[28:29]
	v_pk_fma_f32 v[28:29], v[24:25], v[28:29], v[24:25] neg_lo:[1,0,0] neg_hi:[1,0,0]
	s_nop 0
	v_cndmask_b32_e32 v25, v31, v29, vcc
	v_cmp_le_f32_e32 vcc, 0, v24
	s_nop 1
	v_cndmask_b32_e32 v24, v30, v28, vcc
	v_cvt_pk_f16_f32 v24, v24, v25
	v_mul_f32_e64 v25, |v26|, s1
	v_mul_f32_e32 v29, 0xbfb8aa3b, v25
	v_fma_f32 v28, v25, s3, 1.0
	v_mul_f32_e32 v25, v25, v29
	v_exp_f32_e32 v30, v25
	v_mul_f32_e64 v25, |v27|, s1
	v_fma_f32 v29, v25, s3, 1.0
	v_rcp_f32_e32 v28, v28
	v_rcp_f32_e32 v29, v29
	v_mul_f32_e32 v31, 0xbfb8aa3b, v25
	v_mul_f32_e32 v25, v25, v31
	v_exp_f32_e32 v31, v25
	v_pk_fma_f32 v[32:33], v[28:29], s[0:1], v[36:37] op_sel_hi:[1,0,0]
	v_cmp_le_f32_e32 vcc, 0, v27
	v_pk_fma_f32 v[32:33], v[28:29], v[32:33], s[2:3] op_sel_hi:[1,1,0]
	s_nop 0
	v_pk_fma_f32 v[32:33], v[28:29], v[32:33], s[4:5] op_sel_hi:[1,1,0]
	s_nop 0
	v_pk_fma_f32 v[32:33], v[28:29], v[32:33], s[6:7] op_sel_hi:[1,1,0]
	s_nop 0
	v_pk_mul_f32 v[28:29], v[28:29], v[32:33]
	s_nop 0
	v_pk_mul_f32 v[28:29], v[28:29], 0.5 op_sel_hi:[1,0]
	s_nop 0
	v_pk_mul_f32 v[28:29], v[30:31], v[28:29]
	s_nop 0
	v_pk_mul_f32 v[30:31], v[26:27], v[28:29]
	v_pk_fma_f32 v[28:29], v[26:27], v[28:29], v[26:27] neg_lo:[1,0,0] neg_hi:[1,0,0]
	v_mul_f32_e64 v27, |v21|, s1
	v_cndmask_b32_e32 v25, v31, v29, vcc
	v_cmp_le_f32_e32 vcc, 0, v26
	s_nop 1
	v_cndmask_b32_e32 v26, v30, v28, vcc
	v_cvt_pk_f16_f32 v25, v26, v25
	global_store_dwordx2 v[38:39], v[24:25], off offset:192
	v_mul_f32_e64 v25, |v20|, s1
	v_mul_f32_e32 v26, 0xbfb8aa3b, v25
	v_fma_f32 v24, v25, s3, 1.0
	v_mul_f32_e32 v25, v25, v26
	v_exp_f32_e32 v26, v25
	v_fma_f32 v25, v27, s3, 1.0
	v_rcp_f32_e32 v24, v24
	v_rcp_f32_e32 v25, v25
	v_mul_f32_e32 v28, 0xbfb8aa3b, v27
	v_mul_f32_e32 v27, v27, v28
	v_exp_f32_e32 v27, v27
	v_pk_fma_f32 v[28:29], v[24:25], s[0:1], v[36:37] op_sel_hi:[1,0,0]
	v_cmp_le_f32_e32 vcc, 0, v21
	v_pk_fma_f32 v[28:29], v[24:25], v[28:29], s[2:3] op_sel_hi:[1,1,0]
	s_nop 0
	v_pk_fma_f32 v[28:29], v[24:25], v[28:29], s[4:5] op_sel_hi:[1,1,0]
	s_nop 0
	v_pk_fma_f32 v[28:29], v[24:25], v[28:29], s[6:7] op_sel_hi:[1,1,0]
	s_nop 0
	v_pk_mul_f32 v[24:25], v[24:25], v[28:29]
	s_nop 0
	v_pk_mul_f32 v[24:25], v[24:25], 0.5 op_sel_hi:[1,0]
	s_nop 0
	v_pk_mul_f32 v[24:25], v[26:27], v[24:25]
	s_nop 0
	v_pk_mul_f32 v[26:27], v[20:21], v[24:25]
	v_pk_fma_f32 v[24:25], v[20:21], v[24:25], v[20:21] neg_lo:[1,0,0] neg_hi:[1,0,0]
	s_nop 0
	v_cndmask_b32_e32 v21, v27, v25, vcc
	v_cmp_le_f32_e32 vcc, 0, v20
	s_nop 1
	v_cndmask_b32_e32 v20, v26, v24, vcc
	v_cvt_pk_f16_f32 v20, v20, v21
	v_mul_f32_e64 v21, |v22|, s1
	v_mul_f32_e32 v25, 0xbfb8aa3b, v21
	v_fma_f32 v24, v21, s3, 1.0
	v_mul_f32_e32 v21, v21, v25
	v_exp_f32_e32 v26, v21
	v_mul_f32_e64 v21, |v23|, s1
	v_fma_f32 v25, v21, s3, 1.0
	v_rcp_f32_e32 v24, v24
	v_rcp_f32_e32 v25, v25
	v_mul_f32_e32 v27, 0xbfb8aa3b, v21
	v_mul_f32_e32 v21, v21, v27
	v_exp_f32_e32 v27, v21
	v_pk_fma_f32 v[28:29], v[24:25], s[0:1], v[36:37] op_sel_hi:[1,0,0]
	v_cmp_le_f32_e32 vcc, 0, v23
	v_pk_fma_f32 v[28:29], v[24:25], v[28:29], s[2:3] op_sel_hi:[1,1,0]
	s_nop 0
	v_pk_fma_f32 v[28:29], v[24:25], v[28:29], s[4:5] op_sel_hi:[1,1,0]
	s_nop 0
	v_pk_fma_f32 v[28:29], v[24:25], v[28:29], s[6:7] op_sel_hi:[1,1,0]
	s_nop 0
	v_pk_mul_f32 v[24:25], v[24:25], v[28:29]
	s_nop 0
	v_pk_mul_f32 v[24:25], v[24:25], 0.5 op_sel_hi:[1,0]
	s_nop 0
	v_pk_mul_f32 v[24:25], v[26:27], v[24:25]
	s_nop 0
	v_pk_mul_f32 v[26:27], v[22:23], v[24:25]
	v_pk_fma_f32 v[24:25], v[22:23], v[24:25], v[22:23] neg_lo:[1,0,0] neg_hi:[1,0,0]
	v_mul_f32_e64 v23, |v17|, s1
	v_cndmask_b32_e32 v21, v27, v25, vcc
	v_cmp_le_f32_e32 vcc, 0, v22
	s_nop 1
	v_cndmask_b32_e32 v22, v26, v24, vcc
	v_cvt_pk_f16_f32 v21, v22, v21
	global_store_dwordx2 v[38:39], v[20:21], off offset:320
	v_mul_f32_e64 v21, |v16|, s1
	v_mul_f32_e32 v22, 0xbfb8aa3b, v21
	v_fma_f32 v20, v21, s3, 1.0
	v_mul_f32_e32 v21, v21, v22
	v_exp_f32_e32 v22, v21
	v_fma_f32 v21, v23, s3, 1.0
	v_rcp_f32_e32 v20, v20
	v_rcp_f32_e32 v21, v21
	v_mul_f32_e32 v24, 0xbfb8aa3b, v23
	v_mul_f32_e32 v23, v23, v24
	v_exp_f32_e32 v23, v23
	v_pk_fma_f32 v[24:25], v[20:21], s[0:1], v[36:37] op_sel_hi:[1,0,0]
	v_cmp_le_f32_e32 vcc, 0, v17
	v_pk_fma_f32 v[24:25], v[20:21], v[24:25], s[2:3] op_sel_hi:[1,1,0]
	s_nop 0
	v_pk_fma_f32 v[24:25], v[20:21], v[24:25], s[4:5] op_sel_hi:[1,1,0]
	s_nop 0
	v_pk_fma_f32 v[24:25], v[20:21], v[24:25], s[6:7] op_sel_hi:[1,1,0]
	s_nop 0
	v_pk_mul_f32 v[20:21], v[20:21], v[24:25]
	s_nop 0
	v_pk_mul_f32 v[20:21], v[20:21], 0.5 op_sel_hi:[1,0]
	s_nop 0
	v_pk_mul_f32 v[20:21], v[22:23], v[20:21]
	s_nop 0
	v_pk_mul_f32 v[22:23], v[16:17], v[20:21]
	v_pk_fma_f32 v[20:21], v[16:17], v[20:21], v[16:17] neg_lo:[1,0,0] neg_hi:[1,0,0]
	s_nop 0
	v_cndmask_b32_e32 v17, v23, v21, vcc
	v_cmp_le_f32_e32 vcc, 0, v16
	s_nop 1
	v_cndmask_b32_e32 v16, v22, v20, vcc
	v_cvt_pk_f16_f32 v16, v16, v17
	v_mul_f32_e64 v17, |v18|, s1
	v_mul_f32_e32 v21, 0xbfb8aa3b, v17
	v_fma_f32 v20, v17, s3, 1.0
	v_mul_f32_e32 v17, v17, v21
	v_exp_f32_e32 v22, v17
	v_mul_f32_e64 v17, |v19|, s1
	v_fma_f32 v21, v17, s3, 1.0
	v_rcp_f32_e32 v20, v20
	v_rcp_f32_e32 v21, v21
	v_mul_f32_e32 v23, 0xbfb8aa3b, v17
	v_mul_f32_e32 v17, v17, v23
	v_exp_f32_e32 v23, v17
	v_pk_fma_f32 v[24:25], v[20:21], s[0:1], v[36:37] op_sel_hi:[1,0,0]
	v_cmp_le_f32_e32 vcc, 0, v19
	v_pk_fma_f32 v[24:25], v[20:21], v[24:25], s[2:3] op_sel_hi:[1,1,0]
	s_nop 0
	v_pk_fma_f32 v[24:25], v[20:21], v[24:25], s[4:5] op_sel_hi:[1,1,0]
	s_nop 0
	v_pk_fma_f32 v[24:25], v[20:21], v[24:25], s[6:7] op_sel_hi:[1,1,0]
	s_nop 0
	v_pk_mul_f32 v[20:21], v[20:21], v[24:25]
	s_nop 0
	v_pk_mul_f32 v[20:21], v[20:21], 0.5 op_sel_hi:[1,0]
	s_nop 0
	v_pk_mul_f32 v[20:21], v[22:23], v[20:21]
	s_nop 0
	v_pk_mul_f32 v[22:23], v[18:19], v[20:21]
	v_pk_fma_f32 v[20:21], v[18:19], v[20:21], v[18:19] neg_lo:[1,0,0] neg_hi:[1,0,0]
	v_mul_f32_e64 v19, |v13|, s1
	v_cndmask_b32_e32 v17, v23, v21, vcc
	v_cmp_le_f32_e32 vcc, 0, v18
	s_nop 1
	v_cndmask_b32_e32 v18, v22, v20, vcc
	v_cvt_pk_f16_f32 v17, v18, v17
	global_store_dwordx2 v[38:39], v[16:17], off offset:448
	v_mul_f32_e64 v17, |v12|, s1
	v_mul_f32_e32 v18, 0xbfb8aa3b, v17
	v_fma_f32 v16, v17, s3, 1.0
	v_mul_f32_e32 v17, v17, v18
	v_exp_f32_e32 v18, v17
	v_fma_f32 v17, v19, s3, 1.0
	v_rcp_f32_e32 v16, v16
	v_rcp_f32_e32 v17, v17
	v_mul_f32_e32 v20, 0xbfb8aa3b, v19
	v_mul_f32_e32 v19, v19, v20
	v_exp_f32_e32 v19, v19
	v_pk_fma_f32 v[20:21], v[16:17], s[0:1], v[36:37] op_sel_hi:[1,0,0]
	v_cmp_le_f32_e32 vcc, 0, v13
	v_pk_fma_f32 v[20:21], v[16:17], v[20:21], s[2:3] op_sel_hi:[1,1,0]
	s_nop 0
	v_pk_fma_f32 v[20:21], v[16:17], v[20:21], s[4:5] op_sel_hi:[1,1,0]
	s_nop 0
	v_pk_fma_f32 v[20:21], v[16:17], v[20:21], s[6:7] op_sel_hi:[1,1,0]
	s_nop 0
	v_pk_mul_f32 v[16:17], v[16:17], v[20:21]
	s_nop 0
	v_pk_mul_f32 v[16:17], v[16:17], 0.5 op_sel_hi:[1,0]
	s_nop 0
	v_pk_mul_f32 v[16:17], v[18:19], v[16:17]
	s_nop 0
	v_pk_mul_f32 v[18:19], v[12:13], v[16:17]
	v_pk_fma_f32 v[16:17], v[12:13], v[16:17], v[12:13] neg_lo:[1,0,0] neg_hi:[1,0,0]
	s_nop 0
	v_cndmask_b32_e32 v13, v19, v17, vcc
	v_cmp_le_f32_e32 vcc, 0, v12
	s_nop 1
	v_cndmask_b32_e32 v12, v18, v16, vcc
	v_cvt_pk_f16_f32 v12, v12, v13
	v_mul_f32_e64 v13, |v14|, s1
	v_mul_f32_e32 v17, 0xbfb8aa3b, v13
	v_fma_f32 v16, v13, s3, 1.0
	v_mul_f32_e32 v13, v13, v17
	v_exp_f32_e32 v18, v13
	v_mul_f32_e64 v13, |v15|, s1
	v_fma_f32 v17, v13, s3, 1.0
	v_rcp_f32_e32 v16, v16
	v_rcp_f32_e32 v17, v17
	v_mul_f32_e32 v19, 0xbfb8aa3b, v13
	v_mul_f32_e32 v13, v13, v19
	v_exp_f32_e32 v19, v13
	v_pk_fma_f32 v[20:21], v[16:17], s[0:1], v[36:37] op_sel_hi:[1,0,0]
	v_cmp_le_f32_e32 vcc, 0, v15
	v_pk_fma_f32 v[20:21], v[16:17], v[20:21], s[2:3] op_sel_hi:[1,1,0]
	s_nop 0
	v_pk_fma_f32 v[20:21], v[16:17], v[20:21], s[4:5] op_sel_hi:[1,1,0]
	s_nop 0
	v_pk_fma_f32 v[20:21], v[16:17], v[20:21], s[6:7] op_sel_hi:[1,1,0]
	s_nop 0
	v_pk_mul_f32 v[16:17], v[16:17], v[20:21]
	s_nop 0
	v_pk_mul_f32 v[16:17], v[16:17], 0.5 op_sel_hi:[1,0]
	s_nop 0
	v_pk_mul_f32 v[16:17], v[18:19], v[16:17]
	s_nop 0
	v_pk_mul_f32 v[18:19], v[14:15], v[16:17]
	v_pk_fma_f32 v[16:17], v[14:15], v[16:17], v[14:15] neg_lo:[1,0,0] neg_hi:[1,0,0]
	v_mul_f32_e64 v15, |v9|, s1
	v_cndmask_b32_e32 v13, v19, v17, vcc
	v_cmp_le_f32_e32 vcc, 0, v14
	s_nop 1
	v_cndmask_b32_e32 v14, v18, v16, vcc
	v_cvt_pk_f16_f32 v13, v14, v13
	global_store_dwordx2 v[38:39], v[12:13], off offset:96
	v_mul_f32_e64 v13, |v8|, s1
	v_mul_f32_e32 v14, 0xbfb8aa3b, v13
	v_fma_f32 v12, v13, s3, 1.0
	v_mul_f32_e32 v13, v13, v14
	v_exp_f32_e32 v14, v13
	v_fma_f32 v13, v15, s3, 1.0
	v_rcp_f32_e32 v12, v12
	v_rcp_f32_e32 v13, v13
	v_mul_f32_e32 v16, 0xbfb8aa3b, v15
	v_mul_f32_e32 v15, v15, v16
	v_exp_f32_e32 v15, v15
	v_pk_fma_f32 v[16:17], v[12:13], s[0:1], v[36:37] op_sel_hi:[1,0,0]
	v_cmp_le_f32_e32 vcc, 0, v9
	v_pk_fma_f32 v[16:17], v[12:13], v[16:17], s[2:3] op_sel_hi:[1,1,0]
	s_nop 0
	v_pk_fma_f32 v[16:17], v[12:13], v[16:17], s[4:5] op_sel_hi:[1,1,0]
	s_nop 0
	v_pk_fma_f32 v[16:17], v[12:13], v[16:17], s[6:7] op_sel_hi:[1,1,0]
	s_nop 0
	v_pk_mul_f32 v[12:13], v[12:13], v[16:17]
	s_nop 0
	v_pk_mul_f32 v[12:13], v[12:13], 0.5 op_sel_hi:[1,0]
	s_nop 0
	v_pk_mul_f32 v[12:13], v[14:15], v[12:13]
	s_nop 0
	v_pk_mul_f32 v[14:15], v[8:9], v[12:13]
	v_pk_fma_f32 v[12:13], v[8:9], v[12:13], v[8:9] neg_lo:[1,0,0] neg_hi:[1,0,0]
	s_nop 0
	v_cndmask_b32_e32 v9, v15, v13, vcc
	v_cmp_le_f32_e32 vcc, 0, v8
	s_nop 1
	v_cndmask_b32_e32 v8, v14, v12, vcc
	v_cvt_pk_f16_f32 v8, v8, v9
	v_mul_f32_e64 v9, |v10|, s1
	v_mul_f32_e32 v13, 0xbfb8aa3b, v9
	v_fma_f32 v12, v9, s3, 1.0
	v_mul_f32_e32 v9, v9, v13
	v_exp_f32_e32 v14, v9
	v_mul_f32_e64 v9, |v11|, s1
	v_fma_f32 v13, v9, s3, 1.0
	v_rcp_f32_e32 v12, v12
	v_rcp_f32_e32 v13, v13
	v_mul_f32_e32 v15, 0xbfb8aa3b, v9
	v_mul_f32_e32 v9, v9, v15
	v_exp_f32_e32 v15, v9
	v_pk_fma_f32 v[16:17], v[12:13], s[0:1], v[36:37] op_sel_hi:[1,0,0]
	v_cmp_le_f32_e32 vcc, 0, v11
	v_pk_fma_f32 v[16:17], v[12:13], v[16:17], s[2:3] op_sel_hi:[1,1,0]
	s_nop 0
	v_pk_fma_f32 v[16:17], v[12:13], v[16:17], s[4:5] op_sel_hi:[1,1,0]
	s_nop 0
	v_pk_fma_f32 v[16:17], v[12:13], v[16:17], s[6:7] op_sel_hi:[1,1,0]
	s_nop 0
	v_pk_mul_f32 v[12:13], v[12:13], v[16:17]
	s_nop 0
	v_pk_mul_f32 v[12:13], v[12:13], 0.5 op_sel_hi:[1,0]
	s_nop 0
	v_pk_mul_f32 v[12:13], v[14:15], v[12:13]
	s_nop 0
	v_pk_mul_f32 v[14:15], v[10:11], v[12:13]
	v_pk_fma_f32 v[12:13], v[10:11], v[12:13], v[10:11] neg_lo:[1,0,0] neg_hi:[1,0,0]
	v_mul_f32_e64 v11, |v5|, s1
	v_cndmask_b32_e32 v9, v15, v13, vcc
	v_cmp_le_f32_e32 vcc, 0, v10
	s_nop 1
	v_cndmask_b32_e32 v10, v14, v12, vcc
	v_cvt_pk_f16_f32 v9, v10, v9
	global_store_dwordx2 v[38:39], v[8:9], off offset:224
	v_mul_f32_e64 v9, |v4|, s1
	v_mul_f32_e32 v10, 0xbfb8aa3b, v9
	v_fma_f32 v8, v9, s3, 1.0
	v_mul_f32_e32 v9, v9, v10
	v_exp_f32_e32 v10, v9
	v_fma_f32 v9, v11, s3, 1.0
	v_rcp_f32_e32 v8, v8
	v_rcp_f32_e32 v9, v9
	v_mul_f32_e32 v12, 0xbfb8aa3b, v11
	v_mul_f32_e32 v11, v11, v12
	v_exp_f32_e32 v11, v11
	v_pk_fma_f32 v[12:13], v[8:9], s[0:1], v[36:37] op_sel_hi:[1,0,0]
	v_cmp_le_f32_e32 vcc, 0, v5
	v_pk_fma_f32 v[12:13], v[8:9], v[12:13], s[2:3] op_sel_hi:[1,1,0]
	s_nop 0
	v_pk_fma_f32 v[12:13], v[8:9], v[12:13], s[4:5] op_sel_hi:[1,1,0]
	s_nop 0
	v_pk_fma_f32 v[12:13], v[8:9], v[12:13], s[6:7] op_sel_hi:[1,1,0]
	s_nop 0
	v_pk_mul_f32 v[8:9], v[8:9], v[12:13]
	s_nop 0
	v_pk_mul_f32 v[8:9], v[8:9], 0.5 op_sel_hi:[1,0]
	s_nop 0
	v_pk_mul_f32 v[8:9], v[10:11], v[8:9]
	s_nop 0
	v_pk_mul_f32 v[10:11], v[4:5], v[8:9]
	v_pk_fma_f32 v[8:9], v[4:5], v[8:9], v[4:5] neg_lo:[1,0,0] neg_hi:[1,0,0]
	s_nop 0
	v_cndmask_b32_e32 v5, v11, v9, vcc
	v_cmp_le_f32_e32 vcc, 0, v4
	s_nop 1
	v_cndmask_b32_e32 v4, v10, v8, vcc
	v_cvt_pk_f16_f32 v4, v4, v5
	v_mul_f32_e64 v5, |v6|, s1
	v_mul_f32_e32 v9, 0xbfb8aa3b, v5
	v_fma_f32 v8, v5, s3, 1.0
	v_mul_f32_e32 v5, v5, v9
	v_exp_f32_e32 v10, v5
	v_mul_f32_e64 v5, |v7|, s1
	v_fma_f32 v9, v5, s3, 1.0
	v_rcp_f32_e32 v8, v8
	v_rcp_f32_e32 v9, v9
	v_mul_f32_e32 v11, 0xbfb8aa3b, v5
	v_mul_f32_e32 v5, v5, v11
	v_exp_f32_e32 v11, v5
	v_pk_fma_f32 v[12:13], v[8:9], s[0:1], v[36:37] op_sel_hi:[1,0,0]
	v_cmp_le_f32_e32 vcc, 0, v7
	v_pk_fma_f32 v[12:13], v[8:9], v[12:13], s[2:3] op_sel_hi:[1,1,0]
	s_nop 0
	v_pk_fma_f32 v[12:13], v[8:9], v[12:13], s[4:5] op_sel_hi:[1,1,0]
	s_nop 0
	v_pk_fma_f32 v[12:13], v[8:9], v[12:13], s[6:7] op_sel_hi:[1,1,0]
	s_nop 0
	v_pk_mul_f32 v[8:9], v[8:9], v[12:13]
	s_nop 0
	v_pk_mul_f32 v[8:9], v[8:9], 0.5 op_sel_hi:[1,0]
	s_nop 0
	v_pk_mul_f32 v[8:9], v[10:11], v[8:9]
	s_nop 0
	v_pk_mul_f32 v[10:11], v[6:7], v[8:9]
	v_pk_fma_f32 v[8:9], v[6:7], v[8:9], v[6:7] neg_lo:[1,0,0] neg_hi:[1,0,0]
	v_mul_f32_e64 v7, |v1|, s1
	v_cndmask_b32_e32 v5, v11, v9, vcc
	v_cmp_le_f32_e32 vcc, 0, v6
	s_nop 1
	v_cndmask_b32_e32 v6, v10, v8, vcc
	v_cvt_pk_f16_f32 v5, v6, v5
	global_store_dwordx2 v[38:39], v[4:5], off offset:352
	v_mul_f32_e64 v5, |v0|, s1
	v_mul_f32_e32 v6, 0xbfb8aa3b, v5
	v_fma_f32 v4, v5, s3, 1.0
	v_mul_f32_e32 v5, v5, v6
	v_exp_f32_e32 v6, v5
	v_fma_f32 v5, v7, s3, 1.0
	v_rcp_f32_e32 v4, v4
	v_rcp_f32_e32 v5, v5
	v_mul_f32_e32 v8, 0xbfb8aa3b, v7
	v_mul_f32_e32 v7, v7, v8
	v_exp_f32_e32 v7, v7
	v_pk_fma_f32 v[8:9], v[4:5], s[0:1], v[36:37] op_sel_hi:[1,0,0]
	v_cmp_le_f32_e32 vcc, 0, v1
	v_pk_fma_f32 v[8:9], v[4:5], v[8:9], s[2:3] op_sel_hi:[1,1,0]
	s_nop 0
	v_pk_fma_f32 v[8:9], v[4:5], v[8:9], s[4:5] op_sel_hi:[1,1,0]
	s_nop 0
	v_pk_fma_f32 v[8:9], v[4:5], v[8:9], s[6:7] op_sel_hi:[1,1,0]
	s_nop 0
	v_pk_mul_f32 v[4:5], v[4:5], v[8:9]
	s_nop 0
	v_pk_mul_f32 v[4:5], v[4:5], 0.5 op_sel_hi:[1,0]
	s_nop 0
	v_pk_mul_f32 v[4:5], v[6:7], v[4:5]
	s_nop 0
	v_pk_mul_f32 v[6:7], v[0:1], v[4:5]
	v_pk_fma_f32 v[4:5], v[0:1], v[4:5], v[0:1] neg_lo:[1,0,0] neg_hi:[1,0,0]
	s_nop 0
	v_cndmask_b32_e32 v1, v7, v5, vcc
	v_cmp_le_f32_e32 vcc, 0, v0
	s_nop 1
	v_cndmask_b32_e32 v0, v6, v4, vcc
	v_cvt_pk_f16_f32 v0, v0, v1
	v_mul_f32_e64 v1, |v2|, s1
	v_mul_f32_e32 v5, 0xbfb8aa3b, v1
	v_fma_f32 v4, v1, s3, 1.0
	v_mul_f32_e32 v1, v1, v5
	v_exp_f32_e32 v6, v1
	v_mul_f32_e64 v1, |v3|, s1
	v_fma_f32 v5, v1, s3, 1.0
	v_rcp_f32_e32 v4, v4
	v_rcp_f32_e32 v5, v5
	v_mul_f32_e32 v7, 0xbfb8aa3b, v1
	v_mul_f32_e32 v1, v1, v7
	v_exp_f32_e32 v7, v1
	v_pk_fma_f32 v[8:9], v[4:5], s[0:1], v[36:37] op_sel_hi:[1,0,0]
	v_cmp_le_f32_e32 vcc, 0, v3
	v_pk_fma_f32 v[8:9], v[4:5], v[8:9], s[2:3] op_sel_hi:[1,1,0]
	s_nop 0
	v_pk_fma_f32 v[8:9], v[4:5], v[8:9], s[4:5] op_sel_hi:[1,1,0]
	s_nop 0
	v_pk_fma_f32 v[8:9], v[4:5], v[8:9], s[6:7] op_sel_hi:[1,1,0]
	s_nop 0
	v_pk_mul_f32 v[4:5], v[4:5], v[8:9]
	s_nop 0
	v_pk_mul_f32 v[4:5], v[4:5], 0.5 op_sel_hi:[1,0]
	s_nop 0
	v_pk_mul_f32 v[4:5], v[6:7], v[4:5]
	s_nop 0
	v_pk_mul_f32 v[6:7], v[2:3], v[4:5]
	v_pk_fma_f32 v[4:5], v[2:3], v[4:5], v[2:3] neg_lo:[1,0,0] neg_hi:[1,0,0]
	s_nop 0
	v_cndmask_b32_e32 v1, v7, v5, vcc
	v_cmp_le_f32_e32 vcc, 0, v2
	s_nop 1
	v_cndmask_b32_e32 v2, v6, v4, vcc
	v_cvt_pk_f16_f32 v1, v2, v1
	global_store_dwordx2 v[38:39], v[0:1], off offset:480
	s_endpgm

.LBB7_4:
	v_add_u32_e32 v0, s40, v143
	v_lshl_or_b32 v0, v145, 2, v0
	v_lshlrev_b32_e32 v148, 2, v0
	global_load_dwordx4 v[138:141], v148, s[8:9]
	global_load_dwordx4 v[142:145], v148, s[8:9] offset:2048
	v_lshlrev_b32_e32 v130, 6, v146
	v_or3_b32 v130, v130, s33, v134
	v_lshlrev_b32_e32 v146, 2, v130
	global_load_dwordx4 v[130:133], v148, s[8:9] offset:64
	global_load_dwordx4 v[134:137], v148, s[8:9] offset:2112
	s_lshl_b64 s[0:1], s[0:1], 23
	s_add_u32 s0, s10, s0
	v_mov_b32_e32 v1, 0
	s_addc_u32 s1, s11, s1
	v_lshlrev_b32_e32 v0, 14, v0
	v_mov_b32_e32 v147, v1
	v_mov_b32_e32 v151, v1
	v_lshl_add_u64 v[154:155], s[0:1], 0, v[0:1]
	v_or_b32_e32 v150, 0x4000, v0
	v_lshl_add_u64 v[154:155], v[154:155], 0, v[146:147]
	v_lshl_add_u64 v[150:151], s[0:1], 0, v[150:151]
	v_lshl_add_u64 v[150:151], v[150:151], 0, v[146:147]
	v_mov_b32_e32 v153, v1
	v_or_b32_e32 v152, 0x8000, v0
	s_waitcnt vmcnt(3)
	v_add_f32_e32 v126, v138, v126
	s_waitcnt vmcnt(2)
	v_add_f32_e32 v110, v142, v110
	v_add_f32_e32 v103, v143, v103
	v_add_f32_e32 v106, v142, v106
	v_add_f32_e32 v102, v142, v102
	v_add_f32_e32 v98, v142, v98
	v_add_f32_e32 v111, v143, v111
	v_add_f32_e32 v107, v143, v107
	v_add_f32_e32 v99, v143, v99
	v_mul_f32_e32 v110, 0xbfb8aa3b, v110
	v_mul_f32_e32 v103, 0xbfb8aa3b, v103
	v_mul_f32_e32 v106, 0xbfb8aa3b, v106
	v_mul_f32_e32 v102, 0xbfb8aa3b, v102
	v_mul_f32_e32 v98, 0xbfb8aa3b, v98
	v_mul_f32_e32 v111, 0xbfb8aa3b, v111
	v_mul_f32_e32 v107, 0xbfb8aa3b, v107
	v_mul_f32_e32 v99, 0xbfb8aa3b, v99
	v_exp_f32_e32 v110, v110
	v_exp_f32_e32 v103, v103
	v_exp_f32_e32 v106, v106
	v_exp_f32_e32 v102, v102
	v_exp_f32_e32 v98, v98
	v_exp_f32_e32 v111, v111
	v_exp_f32_e32 v107, v107
	v_exp_f32_e32 v99, v99
	v_add_f32_e32 v112, v144, v112
	v_mul_f32_e32 v112, 0xbfb8aa3b, v112
	v_add_f32_e32 v108, v144, v108
	v_exp_f32_e32 v112, v112
	v_add_f32_e32 v110, 1.0, v110
	v_add_f32_e32 v103, 1.0, v103
	v_mul_f32_e32 v108, 0xbfb8aa3b, v108
	v_add_f32_e32 v106, 1.0, v106
	v_add_f32_e32 v102, 1.0, v102
	v_add_f32_e32 v98, 1.0, v98
	v_add_f32_e32 v111, 1.0, v111
	v_add_f32_e32 v107, 1.0, v107
	v_add_f32_e32 v99, 1.0, v99
	v_rcp_f32_e32 v110, v110
	v_rcp_f32_e32 v103, v103
	v_exp_f32_e32 v108, v108
	v_rcp_f32_e32 v106, v106
	v_rcp_f32_e32 v102, v102
	v_rcp_f32_e32 v98, v98
	v_rcp_f32_e32 v111, v111
	v_rcp_f32_e32 v107, v107
	v_rcp_f32_e32 v99, v99
	v_add_f32_e32 v119, v139, v119
	v_add_f32_e32 v112, 1.0, v112
	v_add_f32_e32 v122, v138, v122
	v_add_f32_e32 v118, v138, v118
	v_add_f32_e32 v114, v138, v114
	v_add_f32_e32 v127, v139, v127
	v_add_f32_e32 v123, v139, v123
	v_add_f32_e32 v115, v139, v115
	v_rcp_f32_e32 v112, v112
	v_mul_f32_e32 v110, v126, v110
	v_mul_f32_e32 v103, v119, v103
	v_mul_f32_e32 v106, v122, v106
	v_mul_f32_e32 v102, v118, v102
	v_mul_f32_e32 v98, v114, v98
	v_mul_f32_e32 v111, v127, v111
	v_mul_f32_e32 v107, v123, v107
	v_mul_f32_e32 v99, v115, v99
	global_store_dword v[154:155], v110, off
	global_store_dword v[154:155], v106, off offset:64
	global_store_dword v[154:155], v102, off offset:128
	global_store_dword v[154:155], v98, off offset:192
	global_store_dword v[150:151], v111, off
	global_store_dword v[150:151], v107, off offset:64
	global_store_dword v[150:151], v103, off offset:128
	global_store_dword v[150:151], v99, off offset:192
	v_add_f32_e32 v103, 1.0, v108
	v_rcp_f32_e32 v103, v103
	v_lshl_add_u64 v[98:99], s[0:1], 0, v[152:153]
	v_add_f32_e32 v102, v140, v128
	v_mul_f32_e32 v102, v102, v112
	v_lshl_add_u64 v[98:99], v[98:99], 0, v[146:147]
	global_store_dword v[98:99], v102, off
	v_add_f32_e32 v102, v140, v124
	v_mul_f32_e32 v102, v102, v103
	global_store_dword v[98:99], v102, off offset:64
	v_add_f32_e32 v102, v144, v104
	v_mul_f32_e32 v102, 0xbfb8aa3b, v102
	v_exp_f32_e32 v102, v102
	v_add_f32_e32 v100, v144, v100
	v_mul_f32_e32 v100, 0xbfb8aa3b, v100
	v_exp_f32_e32 v100, v100
	v_add_f32_e32 v102, 1.0, v102
	v_rcp_f32_e32 v102, v102
	v_add_f32_e32 v103, v140, v120
	v_add_f32_e32 v100, 1.0, v100
	v_rcp_f32_e32 v100, v100
	v_mul_f32_e32 v102, v103, v102
	global_store_dword v[98:99], v102, off offset:128
	v_add_f32_e32 v102, v140, v116
	v_mul_f32_e32 v100, v102, v100
	v_add_f32_e32 v102, v145, v113
	v_mul_f32_e32 v102, 0xbfb8aa3b, v102
	v_exp_f32_e32 v102, v102
	global_store_dword v[98:99], v100, off offset:192
	v_or_b32_e32 v98, 0xc000, v0
	v_mov_b32_e32 v99, v1
	v_add_f32_e32 v100, 1.0, v102
	v_add_f32_e32 v102, v145, v109
	v_mul_f32_e32 v102, 0xbfb8aa3b, v102
	v_exp_f32_e32 v102, v102
	v_rcp_f32_e32 v100, v100
	v_lshl_add_u64 v[98:99], s[0:1], 0, v[98:99]
	v_add_f32_e32 v103, v141, v129
	v_add_f32_e32 v102, 1.0, v102
	v_rcp_f32_e32 v102, v102
	v_mul_f32_e32 v100, v103, v100
	v_lshl_add_u64 v[98:99], v[98:99], 0, v[146:147]
	global_store_dword v[98:99], v100, off
	v_add_f32_e32 v100, v141, v125
	v_mul_f32_e32 v100, v100, v102
	global_store_dword v[98:99], v100, off offset:64
	v_add_f32_e32 v100, v145, v105
	v_mul_f32_e32 v100, 0xbfb8aa3b, v100
	v_exp_f32_e32 v100, v100
	v_add_f32_e32 v101, v145, v101
	v_mul_f32_e32 v101, 0xbfb8aa3b, v101
	v_exp_f32_e32 v101, v101
	s_waitcnt vmcnt(14)
	v_add_f32_e32 v78, v134, v78
	v_add_f32_e32 v100, 1.0, v100
	v_mul_f32_e32 v78, 0xbfb8aa3b, v78
	v_rcp_f32_e32 v100, v100
	v_exp_f32_e32 v78, v78
	v_add_f32_e32 v74, v134, v74
	v_add_f32_e32 v101, 1.0, v101
	v_mul_f32_e32 v74, 0xbfb8aa3b, v74
	v_rcp_f32_e32 v101, v101
	v_exp_f32_e32 v74, v74
	v_add_f32_e32 v70, v134, v70
	v_add_f32_e32 v102, v141, v121
	v_mul_f32_e32 v70, 0xbfb8aa3b, v70
	v_mul_f32_e32 v100, v102, v100
	v_add_f32_e32 v78, 1.0, v78
	v_exp_f32_e32 v70, v70
	v_add_f32_e32 v66, v134, v66
	global_store_dword v[98:99], v100, off offset:128
	v_add_f32_e32 v100, v141, v117
	v_rcp_f32_e32 v78, v78
	v_mul_f32_e32 v66, 0xbfb8aa3b, v66
	v_mul_f32_e32 v100, v100, v101
	v_add_f32_e32 v74, 1.0, v74
	v_exp_f32_e32 v66, v66
	global_store_dword v[98:99], v100, off offset:192
	v_or_b32_e32 v98, 0x40000, v0
	v_mov_b32_e32 v99, v1
	v_rcp_f32_e32 v74, v74
	v_lshl_add_u64 v[98:99], s[0:1], 0, v[98:99]
	v_add_f32_e32 v94, v130, v94
	v_add_f32_e32 v70, 1.0, v70
	v_mul_f32_e32 v78, v94, v78
	v_lshl_add_u64 v[98:99], v[98:99], 0, v[146:147]
	v_rcp_f32_e32 v70, v70
	global_store_dword v[98:99], v78, off
	v_add_f32_e32 v78, v130, v90
	v_add_f32_e32 v66, 1.0, v66
	v_mul_f32_e32 v74, v78, v74
	v_rcp_f32_e32 v66, v66
	global_store_dword v[98:99], v74, off offset:64
	v_add_f32_e32 v74, v130, v86
	v_mul_f32_e32 v70, v74, v70
	global_store_dword v[98:99], v70, off offset:128
	v_add_f32_e32 v70, v130, v82
	v_mul_f32_e32 v66, v70, v66
	v_add_f32_e32 v70, v135, v79
	v_mul_f32_e32 v70, 0xbfb8aa3b, v70
	v_exp_f32_e32 v70, v70
	global_store_dword v[98:99], v66, off offset:192
	global_load_dwordx4 v[98:101], v148, s[8:9] offset:2176
	v_or_b32_e32 v78, 0x44000, v0
	v_add_f32_e32 v66, 1.0, v70
	v_add_f32_e32 v70, v135, v75
	v_mul_f32_e32 v70, 0xbfb8aa3b, v70
	v_exp_f32_e32 v70, v70
	v_rcp_f32_e32 v66, v66
	v_mov_b32_e32 v79, v1
	v_lshl_add_u64 v[74:75], s[0:1], 0, v[78:79]
	v_add_f32_e32 v70, 1.0, v70
	v_rcp_f32_e32 v70, v70
	v_add_f32_e32 v78, v131, v95
	v_mul_f32_e32 v66, v78, v66
	v_lshl_add_u64 v[74:75], v[74:75], 0, v[146:147]
	global_store_dword v[74:75], v66, off
	v_add_f32_e32 v66, v131, v91
	v_mul_f32_e32 v66, v66, v70
	global_store_dword v[74:75], v66, off offset:64
	v_add_f32_e32 v66, v135, v71
	global_load_dwordx4 v[102:105], v148, s[8:9] offset:128
	v_mul_f32_e32 v66, 0xbfb8aa3b, v66
	v_exp_f32_e32 v66, v66
	v_add_f32_e32 v67, v135, v67
	v_mul_f32_e32 v67, 0xbfb8aa3b, v67
	v_exp_f32_e32 v67, v67
	v_add_f32_e32 v66, 1.0, v66
	v_rcp_f32_e32 v66, v66
	v_add_f32_e32 v70, v131, v87
	v_add_f32_e32 v67, 1.0, v67
	v_rcp_f32_e32 v67, v67
	v_mul_f32_e32 v66, v70, v66
	global_store_dword v[74:75], v66, off offset:128
	v_add_f32_e32 v66, v131, v83
	v_mul_f32_e32 v66, v66, v67
	global_store_dword v[74:75], v66, off offset:192
	v_add_f32_e32 v66, v136, v80
	v_mul_f32_e32 v66, 0xbfb8aa3b, v66
	v_exp_f32_e32 v70, v66
	v_add_f32_e32 v71, v136, v76
	v_mul_f32_e32 v71, 0xbfb8aa3b, v71
	v_exp_f32_e32 v71, v71
	v_add_f32_e32 v70, 1.0, v70
	v_rcp_f32_e32 v70, v70
	v_or_b32_e32 v66, 0x48000, v0
	v_add_f32_e32 v71, 1.0, v71
	v_mov_b32_e32 v67, v1
	v_rcp_f32_e32 v71, v71
	v_lshl_add_u64 v[66:67], s[0:1], 0, v[66:67]
	v_add_f32_e32 v74, v132, v96
	v_mul_f32_e32 v70, v74, v70
	v_lshl_add_u64 v[66:67], v[66:67], 0, v[146:147]
	global_store_dword v[66:67], v70, off
	v_add_f32_e32 v70, v132, v92
	v_mul_f32_e32 v70, v70, v71
	global_store_dword v[66:67], v70, off offset:64
	v_add_f32_e32 v70, v136, v72
	v_mul_f32_e32 v70, 0xbfb8aa3b, v70
	v_exp_f32_e32 v70, v70
	v_add_f32_e32 v68, v136, v68
	v_mul_f32_e32 v68, 0xbfb8aa3b, v68
	v_exp_f32_e32 v68, v68
	v_add_f32_e32 v70, 1.0, v70
	v_rcp_f32_e32 v70, v70
	v_add_f32_e32 v71, v132, v88
	v_add_f32_e32 v68, 1.0, v68
	v_rcp_f32_e32 v68, v68
	v_mul_f32_e32 v70, v71, v70
	global_store_dword v[66:67], v70, off offset:128
	v_add_f32_e32 v70, v132, v84
	v_mul_f32_e32 v68, v70, v68
	v_add_f32_e32 v70, v137, v81
	v_mul_f32_e32 v70, 0xbfb8aa3b, v70
	v_exp_f32_e32 v70, v70
	global_store_dword v[66:67], v68, off offset:192
	v_or_b32_e32 v66, 0x4c000, v0
	v_mov_b32_e32 v67, v1
	v_add_f32_e32 v68, 1.0, v70
	v_add_f32_e32 v70, v137, v77
	v_mul_f32_e32 v70, 0xbfb8aa3b, v70
	v_exp_f32_e32 v70, v70
	v_rcp_f32_e32 v68, v68
	v_lshl_add_u64 v[66:67], s[0:1], 0, v[66:67]
	v_add_f32_e32 v71, v133, v97
	v_add_f32_e32 v70, 1.0, v70
	v_rcp_f32_e32 v70, v70
	v_mul_f32_e32 v68, v71, v68
	v_lshl_add_u64 v[66:67], v[66:67], 0, v[146:147]
	global_store_dword v[66:67], v68, off
	v_add_f32_e32 v68, v133, v93
	v_mul_f32_e32 v68, v68, v70
	global_store_dword v[66:67], v68, off offset:64
	v_add_f32_e32 v68, v137, v73
	v_mul_f32_e32 v68, 0xbfb8aa3b, v68
	v_exp_f32_e32 v68, v68
	v_add_f32_e32 v69, v137, v69
	v_mul_f32_e32 v69, 0xbfb8aa3b, v69
	v_exp_f32_e32 v69, v69
	v_add_f32_e32 v68, 1.0, v68
	v_rcp_f32_e32 v68, v68
	v_add_f32_e32 v70, v133, v89
	v_add_f32_e32 v69, 1.0, v69
	v_rcp_f32_e32 v69, v69
	v_mul_f32_e32 v68, v70, v68
	global_load_dwordx4 v[70:73], v148, s[8:9] offset:2240
	s_waitcnt vmcnt(12)
	v_add_f32_e32 v46, v98, v46
	v_mul_f32_e32 v46, 0xbfb8aa3b, v46
	v_exp_f32_e32 v46, v46
	v_add_f32_e32 v42, v98, v42
	v_mul_f32_e32 v42, 0xbfb8aa3b, v42
	v_exp_f32_e32 v42, v42
	v_add_f32_e32 v38, v98, v38
	v_mul_f32_e32 v38, 0xbfb8aa3b, v38
	v_add_f32_e32 v46, 1.0, v46
	v_exp_f32_e32 v38, v38
	global_store_dword v[66:67], v68, off offset:128
	v_add_f32_e32 v68, v133, v85
	v_rcp_f32_e32 v46, v46
	v_mul_f32_e32 v68, v68, v69
	v_add_f32_e32 v42, 1.0, v42
	global_store_dword v[66:67], v68, off offset:192
	v_or_b32_e32 v66, 0x80000, v0
	v_mov_b32_e32 v67, v1
	v_rcp_f32_e32 v42, v42
	v_add_f32_e32 v2, v98, v2
	v_lshl_add_u64 v[74:75], s[0:1], 0, v[66:67]
	global_load_dwordx4 v[66:69], v148, s[8:9] offset:192
	s_waitcnt vmcnt(12)
	v_add_f32_e32 v62, v102, v62
	v_add_f32_e32 v38, 1.0, v38
	v_mul_f32_e32 v2, 0xbfb8aa3b, v2
	v_mul_f32_e32 v46, v62, v46
	v_lshl_add_u64 v[74:75], v[74:75], 0, v[146:147]
	v_rcp_f32_e32 v38, v38
	v_exp_f32_e32 v2, v2
	global_store_dword v[74:75], v46, off
	v_add_f32_e32 v46, v102, v58
	v_mul_f32_e32 v42, v46, v42
	global_store_dword v[74:75], v42, off offset:64
	v_add_f32_e32 v42, v102, v54
	v_mul_f32_e32 v38, v42, v38
	v_add_f32_e32 v2, 1.0, v2
	v_add_f32_e32 v42, v99, v47
	v_rcp_f32_e32 v2, v2
	v_mul_f32_e32 v42, 0xbfb8aa3b, v42
	v_exp_f32_e32 v42, v42
	global_store_dword v[74:75], v38, off offset:128
	v_add_f32_e32 v38, v102, v50
	v_mul_f32_e32 v2, v38, v2
	global_store_dword v[74:75], v2, off offset:192
	v_add_f32_e32 v2, 1.0, v42
	v_rcp_f32_e32 v2, v2
	v_add_f32_e32 v38, v103, v63
	v_add_f32_e32 v39, v99, v39
	v_mul_f32_e32 v39, 0xbfb8aa3b, v39
	v_mul_f32_e32 v2, v38, v2
	v_add_f32_e32 v38, v99, v43
	v_mul_f32_e32 v38, 0xbfb8aa3b, v38
	v_exp_f32_e32 v38, v38
	v_or_b32_e32 v46, 0x84000, v0
	v_mov_b32_e32 v47, v1
	v_exp_f32_e32 v39, v39
	v_add_f32_e32 v38, 1.0, v38
	v_rcp_f32_e32 v38, v38
	v_lshl_add_u64 v[46:47], s[0:1], 0, v[46:47]
	v_lshl_add_u64 v[42:43], v[46:47], 0, v[146:147]
	global_store_dword v[42:43], v2, off
	v_add_f32_e32 v2, v103, v59
	v_mul_f32_e32 v2, v2, v38
	v_add_f32_e32 v38, 1.0, v39
	v_add_f32_e32 v3, v99, v3
	v_rcp_f32_e32 v38, v38
	v_mul_f32_e32 v3, 0xbfb8aa3b, v3
	v_exp_f32_e32 v3, v3
	global_store_dword v[42:43], v2, off offset:64
	v_add_f32_e32 v2, v103, v55
	v_mul_f32_e32 v2, v2, v38
	v_add_f32_e32 v38, v100, v48
	v_add_f32_e32 v3, 1.0, v3
	v_mul_f32_e32 v38, 0xbfb8aa3b, v38
	v_rcp_f32_e32 v3, v3
	v_exp_f32_e32 v38, v38
	global_store_dword v[42:43], v2, off offset:128
	v_add_f32_e32 v2, v103, v51
	v_mul_f32_e32 v2, v2, v3
	v_add_f32_e32 v3, 1.0, v38
	v_rcp_f32_e32 v38, v3
	v_add_f32_e32 v39, v104, v64
	v_add_f32_e32 v40, v100, v40
	v_mul_f32_e32 v40, 0xbfb8aa3b, v40
	v_mul_f32_e32 v38, v39, v38
	v_add_f32_e32 v39, v100, v44
	v_mul_f32_e32 v39, 0xbfb8aa3b, v39
	v_exp_f32_e32 v39, v39
	global_store_dword v[42:43], v2, off offset:192
	v_or_b32_e32 v2, 0x88000, v0
	v_mov_b32_e32 v3, v1
	v_add_f32_e32 v39, 1.0, v39
	v_rcp_f32_e32 v39, v39
	v_exp_f32_e32 v40, v40
	v_lshl_add_u64 v[2:3], s[0:1], 0, v[2:3]
	v_lshl_add_u64 v[2:3], v[2:3], 0, v[146:147]
	global_store_dword v[2:3], v38, off
	v_add_f32_e32 v38, v104, v60
	v_add_f32_e32 v4, v100, v4
	v_mul_f32_e32 v38, v38, v39
	v_add_f32_e32 v39, 1.0, v40
	v_mul_f32_e32 v4, 0xbfb8aa3b, v4
	v_rcp_f32_e32 v39, v39
	v_exp_f32_e32 v4, v4
	global_store_dword v[2:3], v38, off offset:64
	v_add_f32_e32 v38, v104, v56
	v_mul_f32_e32 v38, v38, v39
	v_add_f32_e32 v4, 1.0, v4
	v_add_f32_e32 v39, v101, v49
	v_rcp_f32_e32 v4, v4
	v_mul_f32_e32 v39, 0xbfb8aa3b, v39
	v_exp_f32_e32 v39, v39
	global_store_dword v[2:3], v38, off offset:128
	v_add_f32_e32 v38, v104, v52
	v_mul_f32_e32 v4, v38, v4
	global_store_dword v[2:3], v4, off offset:192
	v_add_f32_e32 v3, 1.0, v39
	v_rcp_f32_e32 v4, v3
	v_add_f32_e32 v38, v105, v65
	v_add_f32_e32 v39, v101, v41
	v_mul_f32_e32 v39, 0xbfb8aa3b, v39
	v_mul_f32_e32 v4, v38, v4
	v_add_f32_e32 v38, v101, v45
	v_mul_f32_e32 v38, 0xbfb8aa3b, v38
	v_exp_f32_e32 v38, v38
	v_or_b32_e32 v2, 0x8c000, v0
	v_mov_b32_e32 v3, v1
	v_exp_f32_e32 v39, v39
	v_add_f32_e32 v38, 1.0, v38
	v_rcp_f32_e32 v38, v38
	v_add_f32_e32 v5, v101, v5
	v_lshl_add_u64 v[2:3], s[0:1], 0, v[2:3]
	v_mul_f32_e32 v5, 0xbfb8aa3b, v5
	v_lshl_add_u64 v[2:3], v[2:3], 0, v[146:147]
	v_exp_f32_e32 v5, v5
	global_store_dword v[2:3], v4, off
	v_add_f32_e32 v4, v105, v61
	v_mul_f32_e32 v4, v4, v38
	v_add_f32_e32 v38, 1.0, v39
	v_rcp_f32_e32 v38, v38
	v_add_f32_e32 v5, 1.0, v5
	s_waitcnt vmcnt(16)
	v_add_f32_e32 v34, v70, v34
	v_rcp_f32_e32 v5, v5
	v_mul_f32_e32 v34, 0xbfb8aa3b, v34
	global_store_dword v[2:3], v4, off offset:64
	v_add_f32_e32 v4, v105, v57
	v_exp_f32_e32 v34, v34
	v_mul_f32_e32 v4, v4, v38
	global_store_dword v[2:3], v4, off offset:128
	v_add_f32_e32 v4, v105, v53
	v_mul_f32_e32 v4, v4, v5
	global_store_dword v[2:3], v4, off offset:192
	v_add_f32_e32 v3, 1.0, v34
	v_rcp_f32_e32 v4, v3
	s_waitcnt vmcnt(16)
	v_add_f32_e32 v5, v66, v18
	v_or_b32_e32 v2, 0xc0000, v0
	v_mov_b32_e32 v3, v1
	v_mul_f32_e32 v4, v5, v4
	v_add_f32_e32 v5, v70, v30
	v_mul_f32_e32 v5, 0xbfb8aa3b, v5
	v_exp_f32_e32 v5, v5
	v_lshl_add_u64 v[2:3], s[0:1], 0, v[2:3]
	v_lshl_add_u64 v[2:3], v[2:3], 0, v[146:147]
	global_store_dword v[2:3], v4, off
	v_add_f32_e32 v4, v66, v14
	v_add_f32_e32 v5, 1.0, v5
	v_add_f32_e32 v14, v70, v26
	v_rcp_f32_e32 v5, v5
	v_mul_f32_e32 v14, 0xbfb8aa3b, v14
	v_exp_f32_e32 v14, v14
	v_mul_f32_e32 v4, v4, v5
	global_store_dword v[2:3], v4, off offset:64
	v_add_f32_e32 v4, v66, v10
	v_add_f32_e32 v5, 1.0, v14
	v_add_f32_e32 v10, v70, v22
	v_rcp_f32_e32 v5, v5
	v_mul_f32_e32 v10, 0xbfb8aa3b, v10
	v_exp_f32_e32 v10, v10
	v_mul_f32_e32 v4, v4, v5
	global_store_dword v[2:3], v4, off offset:128
	v_add_f32_e32 v4, v66, v6
	v_add_f32_e32 v5, 1.0, v10
	v_add_f32_e32 v6, v71, v35
	v_rcp_f32_e32 v5, v5
	v_mul_f32_e32 v6, 0xbfb8aa3b, v6
	v_exp_f32_e32 v6, v6
	v_mul_f32_e32 v4, v4, v5
	global_store_dword v[2:3], v4, off offset:192
	v_add_f32_e32 v3, 1.0, v6
	v_rcp_f32_e32 v4, v3
	v_add_f32_e32 v5, v67, v19
	v_add_f32_e32 v6, v71, v27
	v_mul_f32_e32 v6, 0xbfb8aa3b, v6
	v_mul_f32_e32 v4, v5, v4
	v_add_f32_e32 v5, v71, v31
	v_mul_f32_e32 v5, 0xbfb8aa3b, v5
	v_exp_f32_e32 v5, v5
	v_or_b32_e32 v2, 0xc4000, v0
	v_mov_b32_e32 v3, v1
	v_exp_f32_e32 v6, v6
	v_add_f32_e32 v5, 1.0, v5
	v_rcp_f32_e32 v5, v5
	v_lshl_add_u64 v[2:3], s[0:1], 0, v[2:3]
	v_lshl_add_u64 v[2:3], v[2:3], 0, v[146:147]
	global_store_dword v[2:3], v4, off
	v_add_f32_e32 v4, v67, v15
	v_mul_f32_e32 v4, v4, v5
	v_add_f32_e32 v5, 1.0, v6
	v_add_f32_e32 v6, v71, v23
	v_mul_f32_e32 v6, 0xbfb8aa3b, v6
	v_rcp_f32_e32 v5, v5
	v_exp_f32_e32 v6, v6
	global_store_dword v[2:3], v4, off offset:64
	v_add_f32_e32 v4, v67, v11
	v_mul_f32_e32 v4, v4, v5
	v_add_f32_e32 v5, 1.0, v6
	v_add_f32_e32 v6, v72, v36
	v_rcp_f32_e32 v5, v5
	v_mul_f32_e32 v6, 0xbfb8aa3b, v6
	v_exp_f32_e32 v6, v6
	global_store_dword v[2:3], v4, off offset:128
	v_add_f32_e32 v4, v67, v7
	v_mul_f32_e32 v4, v4, v5
	global_store_dword v[2:3], v4, off offset:192
	v_add_f32_e32 v3, 1.0, v6
	v_rcp_f32_e32 v4, v3
	v_add_f32_e32 v5, v68, v20
	v_add_f32_e32 v6, v72, v28
	v_mul_f32_e32 v6, 0xbfb8aa3b, v6
	v_mul_f32_e32 v4, v5, v4
	v_add_f32_e32 v5, v72, v32
	v_mul_f32_e32 v5, 0xbfb8aa3b, v5
	v_exp_f32_e32 v5, v5
	v_or_b32_e32 v2, 0xc8000, v0
	v_mov_b32_e32 v3, v1
	v_exp_f32_e32 v6, v6
	v_add_f32_e32 v5, 1.0, v5
	v_rcp_f32_e32 v5, v5
	v_lshl_add_u64 v[2:3], s[0:1], 0, v[2:3]
	v_lshl_add_u64 v[2:3], v[2:3], 0, v[146:147]
	global_store_dword v[2:3], v4, off
	v_add_f32_e32 v4, v68, v16
	v_mul_f32_e32 v4, v4, v5
	v_add_f32_e32 v5, 1.0, v6
	v_add_f32_e32 v6, v72, v24
	v_mul_f32_e32 v6, 0xbfb8aa3b, v6
	v_rcp_f32_e32 v5, v5
	v_exp_f32_e32 v6, v6
	global_store_dword v[2:3], v4, off offset:64
	v_add_f32_e32 v4, v68, v12
	v_mul_f32_e32 v4, v4, v5
	v_add_f32_e32 v5, 1.0, v6
	v_rcp_f32_e32 v5, v5
	global_store_dword v[2:3], v4, off offset:128
	v_add_f32_e32 v4, v68, v8
	v_add_f32_e32 v6, v73, v37
	v_mul_f32_e32 v6, 0xbfb8aa3b, v6
	v_mul_f32_e32 v4, v4, v5
	v_exp_f32_e32 v6, v6
	global_store_dword v[2:3], v4, off offset:192
	v_add_f32_e32 v3, v73, v33
	v_mul_f32_e32 v3, 0xbfb8aa3b, v3
	v_exp_f32_e32 v3, v3
	v_add_f32_e32 v2, 1.0, v6
	v_rcp_f32_e32 v2, v2
	v_or_b32_e32 v0, 0xcc000, v0
	v_add_f32_e32 v3, 1.0, v3
	v_rcp_f32_e32 v3, v3
	v_lshl_add_u64 v[0:1], s[0:1], 0, v[0:1]
	v_add_f32_e32 v4, v69, v21
	v_mul_f32_e32 v2, v4, v2
	v_lshl_add_u64 v[0:1], v[0:1], 0, v[146:147]
	global_store_dword v[0:1], v2, off
	v_add_f32_e32 v2, v69, v17
	v_mul_f32_e32 v2, v2, v3
	global_store_dword v[0:1], v2, off offset:64
	v_add_f32_e32 v2, v73, v29
	v_mul_f32_e32 v2, 0xbfb8aa3b, v2
	v_exp_f32_e32 v2, v2
	v_add_f32_e32 v3, v73, v25
	v_mul_f32_e32 v3, 0xbfb8aa3b, v3
	v_exp_f32_e32 v3, v3
	v_add_f32_e32 v2, 1.0, v2
	v_rcp_f32_e32 v2, v2
	v_add_f32_e32 v4, v69, v13
	v_add_f32_e32 v3, 1.0, v3
	v_rcp_f32_e32 v3, v3
	v_mul_f32_e32 v2, v4, v2
	global_store_dword v[0:1], v2, off offset:128
	v_add_f32_e32 v2, v69, v9
	v_mul_f32_e32 v2, v2, v3
	global_store_dword v[0:1], v2, off offset:192
	s_endpgm

.LBB8_4:
	v_and_or_b32 v130, v1, 12, s34
	v_lshlrev_b32_e32 v148, 2, v130
	global_load_dwordx4 v[138:141], v148, s[8:9]
	global_load_dwordx4 v[142:145], v148, s[8:9] offset:2048
	v_and_b32_e32 v0, 0xc0, v0
	v_add_u32_e32 v131, s33, v0
	v_lshlrev_b32_e32 v0, 14, v130
	v_or_b32_e32 v146, v131, v134
	global_load_dwordx4 v[130:133], v148, s[8:9] offset:64
	global_load_dwordx4 v[134:137], v148, s[8:9] offset:2112
	v_mov_b32_e32 v1, 0
	s_lshl_b64 s[0:1], s[0:1], 23
	v_mov_b32_e32 v151, v1
	v_lshl_add_u64 v[154:155], s[10:11], 0, v[0:1]
	v_or_b32_e32 v150, 0x4000, v0
	v_mov_b32_e32 v147, v1
	v_lshl_add_u64 v[154:155], v[154:155], 0, s[0:1]
	v_lshlrev_b32_e32 v146, 2, v146
	v_lshl_add_u64 v[150:151], s[10:11], 0, v[150:151]
	v_lshl_add_u64 v[154:155], v[154:155], 0, v[146:147]
	v_lshl_add_u64 v[150:151], v[150:151], 0, s[0:1]
	v_lshl_add_u64 v[150:151], v[150:151], 0, v[146:147]
	v_mov_b32_e32 v153, v1
	v_or_b32_e32 v152, 0x8000, v0
	v_lshl_add_u64 v[152:153], s[10:11], 0, v[152:153]
	s_waitcnt vmcnt(3)
	v_add_f32_e32 v110, v138, v110
	s_waitcnt vmcnt(2)
	v_add_f32_e32 v126, v142, v126
	v_add_f32_e32 v118, v142, v118
	v_add_f32_e32 v122, v142, v122
	v_add_f32_e32 v114, v142, v114
	v_add_f32_e32 v127, v143, v127
	v_add_f32_e32 v123, v143, v123
	v_add_f32_e32 v115, v143, v115
	v_add_f32_e32 v119, v143, v119
	v_mul_f32_e32 v126, 0xbfb8aa3b, v126
	v_mul_f32_e32 v118, 0xbfb8aa3b, v118
	v_mul_f32_e32 v122, 0xbfb8aa3b, v122
	v_mul_f32_e32 v114, 0xbfb8aa3b, v114
	v_mul_f32_e32 v127, 0xbfb8aa3b, v127
	v_mul_f32_e32 v123, 0xbfb8aa3b, v123
	v_mul_f32_e32 v115, 0xbfb8aa3b, v115
	v_mul_f32_e32 v119, 0xbfb8aa3b, v119
	v_exp_f32_e32 v126, v126
	v_exp_f32_e32 v118, v118
	v_exp_f32_e32 v122, v122
	v_exp_f32_e32 v114, v114
	v_exp_f32_e32 v127, v127
	v_exp_f32_e32 v123, v123
	v_exp_f32_e32 v115, v115
	v_exp_f32_e32 v119, v119
	v_add_f32_e32 v126, 1.0, v126
	v_add_f32_e32 v118, 1.0, v118
	v_add_f32_e32 v122, 1.0, v122
	v_add_f32_e32 v114, 1.0, v114
	v_add_f32_e32 v127, 1.0, v127
	v_add_f32_e32 v123, 1.0, v123
	v_add_f32_e32 v115, 1.0, v115
	v_add_f32_e32 v119, 1.0, v119
	v_rcp_f32_e32 v126, v126
	v_rcp_f32_e32 v118, v118
	v_rcp_f32_e32 v122, v122
	v_rcp_f32_e32 v114, v114
	v_rcp_f32_e32 v127, v127
	v_rcp_f32_e32 v123, v123
	v_rcp_f32_e32 v115, v115
	v_rcp_f32_e32 v119, v119
	v_add_f32_e32 v128, v144, v128
	v_add_f32_e32 v98, v138, v98
	v_mul_f32_e32 v128, 0xbfb8aa3b, v128
	v_add_f32_e32 v106, v138, v106
	v_add_f32_e32 v102, v138, v102
	v_add_f32_e32 v111, v139, v111
	v_add_f32_e32 v107, v139, v107
	v_add_f32_e32 v103, v139, v103
	v_add_f32_e32 v99, v139, v99
	v_add_f32_e32 v124, v144, v124
	v_exp_f32_e32 v128, v128
	v_mul_f32_e32 v110, v110, v126
	v_mul_f32_e32 v98, v98, v118
	v_mul_f32_e32 v106, v106, v122
	v_mul_f32_e32 v102, v102, v114
	v_mul_f32_e32 v111, v111, v127
	v_mul_f32_e32 v107, v107, v123
	v_mul_f32_e32 v103, v103, v115
	v_mul_f32_e32 v99, v99, v119
	global_store_dword v[154:155], v110, off
	global_store_dword v[154:155], v106, off offset:64
	global_store_dword v[154:155], v102, off offset:128
	global_store_dword v[154:155], v98, off offset:192
	global_store_dword v[150:151], v111, off
	global_store_dword v[150:151], v107, off offset:64
	global_store_dword v[150:151], v103, off offset:128
	global_store_dword v[150:151], v99, off offset:192
	v_mul_f32_e32 v98, 0xbfb8aa3b, v124
	v_exp_f32_e32 v102, v98
	v_add_f32_e32 v128, 1.0, v128
	v_rcp_f32_e32 v128, v128
	v_lshl_add_u64 v[98:99], v[152:153], 0, s[0:1]
	v_add_f32_e32 v102, 1.0, v102
	v_rcp_f32_e32 v102, v102
	v_add_f32_e32 v103, v140, v112
	v_mul_f32_e32 v103, v103, v128
	v_lshl_add_u64 v[98:99], v[98:99], 0, v[146:147]
	global_store_dword v[98:99], v103, off
	v_add_f32_e32 v103, v140, v108
	v_mul_f32_e32 v102, v103, v102
	global_store_dword v[98:99], v102, off offset:64
	v_add_f32_e32 v102, v144, v116
	v_add_f32_e32 v103, v144, v120
	v_mul_f32_e32 v102, 0xbfb8aa3b, v102
	v_mul_f32_e32 v103, 0xbfb8aa3b, v103
	v_exp_f32_e32 v102, v102
	v_exp_f32_e32 v103, v103
	v_add_f32_e32 v104, v140, v104
	v_add_f32_e32 v100, v140, v100
	v_add_f32_e32 v102, 1.0, v102
	v_add_f32_e32 v103, 1.0, v103
	v_rcp_f32_e32 v102, v102
	v_rcp_f32_e32 v103, v103
	s_waitcnt vmcnt(10)
	v_add_f32_e32 v94, v134, v94
	v_mul_f32_e32 v94, 0xbfb8aa3b, v94
	v_mul_f32_e32 v102, v104, v102
	v_mul_f32_e32 v100, v100, v103
	global_store_dword v[98:99], v102, off offset:128
	global_store_dword v[98:99], v100, off offset:192
	v_add_f32_e32 v98, v145, v129
	v_mul_f32_e32 v98, 0xbfb8aa3b, v98
	v_exp_f32_e32 v100, v98
	v_add_f32_e32 v102, v145, v125
	v_mul_f32_e32 v102, 0xbfb8aa3b, v102
	v_exp_f32_e32 v102, v102
	v_add_f32_e32 v100, 1.0, v100
	v_rcp_f32_e32 v100, v100
	v_or_b32_e32 v98, 0xc000, v0
	v_mov_b32_e32 v99, v1
	v_add_f32_e32 v102, 1.0, v102
	v_lshl_add_u64 v[98:99], s[10:11], 0, v[98:99]
	v_rcp_f32_e32 v102, v102
	v_lshl_add_u64 v[98:99], v[98:99], 0, s[0:1]
	v_add_f32_e32 v103, v141, v113
	v_mul_f32_e32 v100, v103, v100
	v_lshl_add_u64 v[98:99], v[98:99], 0, v[146:147]
	global_store_dword v[98:99], v100, off
	v_add_f32_e32 v100, v141, v109
	v_mul_f32_e32 v100, v100, v102
	global_store_dword v[98:99], v100, off offset:64
	v_add_f32_e32 v100, v145, v117
	v_mul_f32_e32 v100, 0xbfb8aa3b, v100
	v_exp_f32_e32 v100, v100
	v_add_f32_e32 v102, v145, v121
	v_mul_f32_e32 v102, 0xbfb8aa3b, v102
	v_exp_f32_e32 v102, v102
	v_add_f32_e32 v100, 1.0, v100
	v_rcp_f32_e32 v100, v100
	v_exp_f32_e32 v94, v94
	v_add_f32_e32 v102, 1.0, v102
	v_rcp_f32_e32 v102, v102
	v_add_f32_e32 v90, v134, v90
	v_add_f32_e32 v103, v141, v105
	v_mul_f32_e32 v90, 0xbfb8aa3b, v90
	v_mul_f32_e32 v100, v103, v100
	v_exp_f32_e32 v90, v90
	global_store_dword v[98:99], v100, off offset:128
	v_add_f32_e32 v100, v141, v101
	v_add_f32_e32 v94, 1.0, v94
	v_mul_f32_e32 v100, v100, v102
	v_rcp_f32_e32 v94, v94
	global_store_dword v[98:99], v100, off offset:192
	v_or_b32_e32 v98, 0x40000, v0
	v_mov_b32_e32 v99, v1
	v_lshl_add_u64 v[98:99], s[10:11], 0, v[98:99]
	v_add_f32_e32 v90, 1.0, v90
	v_lshl_add_u64 v[98:99], v[98:99], 0, s[0:1]
	v_add_f32_e32 v78, v130, v78
	v_rcp_f32_e32 v90, v90
	v_mul_f32_e32 v78, v78, v94
	v_lshl_add_u64 v[98:99], v[98:99], 0, v[146:147]
	global_store_dword v[98:99], v78, off
	v_add_f32_e32 v78, v134, v86
	v_add_f32_e32 v74, v130, v74
	v_mul_f32_e32 v78, 0xbfb8aa3b, v78
	v_mul_f32_e32 v74, v74, v90
	v_exp_f32_e32 v78, v78
	global_store_dword v[98:99], v74, off offset:64
	v_add_f32_e32 v74, v134, v82
	v_mul_f32_e32 v74, 0xbfb8aa3b, v74
	v_exp_f32_e32 v74, v74
	v_add_f32_e32 v78, 1.0, v78
	v_rcp_f32_e32 v78, v78
	v_add_f32_e32 v66, v130, v66
	v_add_f32_e32 v74, 1.0, v74
	v_rcp_f32_e32 v74, v74
	v_mul_f32_e32 v66, v66, v78
	global_store_dword v[98:99], v66, off offset:192
	v_add_f32_e32 v66, v135, v95
	v_add_f32_e32 v70, v130, v70
	v_mul_f32_e32 v66, 0xbfb8aa3b, v66
	v_mul_f32_e32 v70, v70, v74
	v_exp_f32_e32 v66, v66
	global_store_dword v[98:99], v70, off offset:128
	global_load_dwordx4 v[98:101], v148, s[8:9] offset:2176
	v_add_f32_e32 v70, v135, v91
	v_add_f32_e32 v66, 1.0, v66
	v_rcp_f32_e32 v66, v66
	v_mul_f32_e32 v70, 0xbfb8aa3b, v70
	v_exp_f32_e32 v70, v70
	v_add_f32_e32 v74, v131, v79
	v_mul_f32_e32 v66, v74, v66
	v_add_f32_e32 v74, v135, v83
	v_or_b32_e32 v94, 0x44000, v0
	v_mov_b32_e32 v95, v1
	v_add_f32_e32 v70, 1.0, v70
	v_mul_f32_e32 v74, 0xbfb8aa3b, v74
	v_lshl_add_u64 v[94:95], s[10:11], 0, v[94:95]
	v_rcp_f32_e32 v70, v70
	v_exp_f32_e32 v74, v74
	global_load_dwordx4 v[102:105], v148, s[8:9] offset:128
	v_lshl_add_u64 v[94:95], v[94:95], 0, s[0:1]
	v_lshl_add_u64 v[78:79], v[94:95], 0, v[146:147]
	global_store_dword v[78:79], v66, off
	v_add_f32_e32 v66, v131, v75
	v_mul_f32_e32 v66, v66, v70
	v_add_f32_e32 v70, 1.0, v74
	v_add_f32_e32 v74, v135, v87
	v_mul_f32_e32 v74, 0xbfb8aa3b, v74
	v_rcp_f32_e32 v70, v70
	v_exp_f32_e32 v74, v74
	global_store_dword v[78:79], v66, off offset:64
	v_add_f32_e32 v66, v131, v71
	v_mul_f32_e32 v66, v66, v70
	v_add_f32_e32 v70, 1.0, v74
	v_rcp_f32_e32 v70, v70
	global_store_dword v[78:79], v66, off offset:128
	v_add_f32_e32 v66, v131, v67
	v_add_f32_e32 v71, v136, v92
	v_mul_f32_e32 v66, v66, v70
	global_store_dword v[78:79], v66, off offset:192
	v_add_f32_e32 v66, v136, v96
	v_mul_f32_e32 v66, 0xbfb8aa3b, v66
	v_exp_f32_e32 v70, v66
	v_mul_f32_e32 v71, 0xbfb8aa3b, v71
	v_exp_f32_e32 v71, v71
	v_or_b32_e32 v66, 0x48000, v0
	v_add_f32_e32 v70, 1.0, v70
	v_rcp_f32_e32 v70, v70
	v_mov_b32_e32 v67, v1
	v_add_f32_e32 v71, 1.0, v71
	v_lshl_add_u64 v[66:67], s[10:11], 0, v[66:67]
	v_rcp_f32_e32 v71, v71
	v_lshl_add_u64 v[66:67], v[66:67], 0, s[0:1]
	v_add_f32_e32 v74, v132, v80
	v_mul_f32_e32 v70, v74, v70
	v_lshl_add_u64 v[66:67], v[66:67], 0, v[146:147]
	global_store_dword v[66:67], v70, off
	v_add_f32_e32 v70, v132, v76
	v_mul_f32_e32 v70, v70, v71
	global_store_dword v[66:67], v70, off offset:64
	v_add_f32_e32 v70, v136, v84
	v_add_f32_e32 v71, v136, v88
	v_mul_f32_e32 v70, 0xbfb8aa3b, v70
	v_mul_f32_e32 v71, 0xbfb8aa3b, v71
	v_exp_f32_e32 v70, v70
	v_exp_f32_e32 v71, v71
	v_add_f32_e32 v72, v132, v72
	v_add_f32_e32 v68, v132, v68
	v_add_f32_e32 v70, 1.0, v70
	v_add_f32_e32 v71, 1.0, v71
	v_rcp_f32_e32 v70, v70
	v_rcp_f32_e32 v71, v71
	v_mul_f32_e32 v70, v72, v70
	v_mul_f32_e32 v68, v68, v71
	global_store_dword v[66:67], v70, off offset:128
	global_store_dword v[66:67], v68, off offset:192
	v_add_f32_e32 v66, v137, v97
	v_mul_f32_e32 v66, 0xbfb8aa3b, v66
	v_exp_f32_e32 v68, v66
	v_add_f32_e32 v70, v137, v93
	v_mul_f32_e32 v70, 0xbfb8aa3b, v70
	v_exp_f32_e32 v70, v70
	v_add_f32_e32 v68, 1.0, v68
	v_rcp_f32_e32 v68, v68
	v_or_b32_e32 v66, 0x4c000, v0
	v_mov_b32_e32 v67, v1
	v_add_f32_e32 v70, 1.0, v70
	v_lshl_add_u64 v[66:67], s[10:11], 0, v[66:67]
	v_rcp_f32_e32 v70, v70
	v_lshl_add_u64 v[66:67], v[66:67], 0, s[0:1]
	v_add_f32_e32 v71, v133, v81
	v_mul_f32_e32 v68, v71, v68
	v_lshl_add_u64 v[66:67], v[66:67], 0, v[146:147]
	global_store_dword v[66:67], v68, off
	v_add_f32_e32 v68, v133, v77
	v_mul_f32_e32 v68, v68, v70
	global_store_dword v[66:67], v68, off offset:64
	v_add_f32_e32 v68, v137, v85
	v_mul_f32_e32 v68, 0xbfb8aa3b, v68
	v_exp_f32_e32 v68, v68
	v_add_f32_e32 v70, v137, v89
	v_mul_f32_e32 v70, 0xbfb8aa3b, v70
	v_exp_f32_e32 v70, v70
	v_add_f32_e32 v68, 1.0, v68
	v_rcp_f32_e32 v68, v68
	v_add_f32_e32 v71, v133, v73
	v_add_f32_e32 v70, 1.0, v70
	v_rcp_f32_e32 v70, v70
	v_mul_f32_e32 v68, v71, v68
	global_store_dword v[66:67], v68, off offset:128
	v_add_f32_e32 v68, v133, v69
	v_mul_f32_e32 v68, v68, v70
	global_store_dword v[66:67], v68, off offset:192
	global_load_dwordx4 v[66:69], v148, s[8:9] offset:2240
	s_waitcnt vmcnt(14)
	v_add_f32_e32 v62, v98, v62
	v_mul_f32_e32 v62, 0xbfb8aa3b, v62
	v_exp_f32_e32 v62, v62
	v_add_f32_e32 v58, v98, v58
	v_mul_f32_e32 v58, 0xbfb8aa3b, v58
	v_exp_f32_e32 v58, v58
	v_add_f32_e32 v62, 1.0, v62
	v_rcp_f32_e32 v62, v62
	v_or_b32_e32 v70, 0x80000, v0
	v_mov_b32_e32 v71, v1
	v_add_f32_e32 v58, 1.0, v58
	v_lshl_add_u64 v[70:71], s[10:11], 0, v[70:71]
	v_rcp_f32_e32 v58, v58
	v_lshl_add_u64 v[74:75], v[70:71], 0, s[0:1]
	global_load_dwordx4 v[70:73], v148, s[8:9] offset:192
	s_waitcnt vmcnt(14)
	v_add_f32_e32 v46, v102, v46
	v_mul_f32_e32 v46, v46, v62
	v_lshl_add_u64 v[74:75], v[74:75], 0, v[146:147]
	global_store_dword v[74:75], v46, off
	v_add_f32_e32 v42, v102, v42
	v_add_f32_e32 v46, v98, v54
	v_mul_f32_e32 v42, v42, v58
	v_mul_f32_e32 v46, 0xbfb8aa3b, v46
	global_store_dword v[74:75], v42, off offset:64
	v_add_f32_e32 v42, v98, v50
	v_exp_f32_e32 v46, v46
	v_mul_f32_e32 v42, 0xbfb8aa3b, v42
	v_exp_f32_e32 v42, v42
	v_add_f32_e32 v34, v102, v34
	v_add_f32_e32 v46, 1.0, v46
	v_rcp_f32_e32 v46, v46
	v_add_f32_e32 v42, 1.0, v42
	v_rcp_f32_e32 v42, v42
	v_add_f32_e32 v38, v102, v38
	v_mul_f32_e32 v34, v34, v46
	global_store_dword v[74:75], v34, off offset:192
	v_add_f32_e32 v34, v99, v63
	v_mul_f32_e32 v38, v38, v42
	v_mul_f32_e32 v34, 0xbfb8aa3b, v34
	global_store_dword v[74:75], v38, off offset:128
	v_exp_f32_e32 v34, v34
	v_add_f32_e32 v38, v99, v59
	v_mul_f32_e32 v38, 0xbfb8aa3b, v38
	v_exp_f32_e32 v38, v38
	v_add_f32_e32 v34, 1.0, v34
	v_rcp_f32_e32 v34, v34
	v_or_b32_e32 v62, 0x84000, v0
	v_mov_b32_e32 v63, v1
	v_add_f32_e32 v38, 1.0, v38
	v_lshl_add_u64 v[62:63], s[10:11], 0, v[62:63]
	v_rcp_f32_e32 v38, v38
	v_lshl_add_u64 v[58:59], v[62:63], 0, s[0:1]
	v_add_f32_e32 v42, v103, v47
	v_mul_f32_e32 v34, v42, v34
	v_lshl_add_u64 v[46:47], v[58:59], 0, v[146:147]
	global_store_dword v[46:47], v34, off
	v_add_f32_e32 v34, v103, v43
	v_mul_f32_e32 v34, v34, v38
	global_store_dword v[46:47], v34, off offset:64
	v_add_f32_e32 v34, v99, v51
	v_mul_f32_e32 v34, 0xbfb8aa3b, v34
	v_exp_f32_e32 v34, v34
	v_add_f32_e32 v38, v99, v55
	v_mul_f32_e32 v38, 0xbfb8aa3b, v38
	v_exp_f32_e32 v38, v38
	v_add_f32_e32 v34, 1.0, v34
	v_rcp_f32_e32 v34, v34
	v_add_f32_e32 v39, v103, v39
	v_add_f32_e32 v38, 1.0, v38
	v_rcp_f32_e32 v38, v38
	v_mul_f32_e32 v34, v39, v34
	global_store_dword v[46:47], v34, off offset:128
	v_add_f32_e32 v34, v103, v35
	v_mul_f32_e32 v34, v34, v38
	global_store_dword v[46:47], v34, off offset:192
	v_add_f32_e32 v34, v100, v64
	v_mul_f32_e32 v34, 0xbfb8aa3b, v34
	v_exp_f32_e32 v38, v34
	v_add_f32_e32 v39, v100, v60
	v_mul_f32_e32 v39, 0xbfb8aa3b, v39
	v_exp_f32_e32 v39, v39
	v_add_f32_e32 v38, 1.0, v38
	v_rcp_f32_e32 v38, v38
	v_or_b32_e32 v34, 0x88000, v0
	v_mov_b32_e32 v35, v1
	v_add_f32_e32 v39, 1.0, v39
	v_lshl_add_u64 v[34:35], s[10:11], 0, v[34:35]
	v_rcp_f32_e32 v39, v39
	v_lshl_add_u64 v[34:35], v[34:35], 0, s[0:1]
	v_add_f32_e32 v42, v104, v48
	v_mul_f32_e32 v38, v42, v38
	v_lshl_add_u64 v[34:35], v[34:35], 0, v[146:147]
	global_store_dword v[34:35], v38, off
	v_add_f32_e32 v38, v104, v44
	v_mul_f32_e32 v38, v38, v39
	global_store_dword v[34:35], v38, off offset:64
	v_add_f32_e32 v38, v100, v52
	v_add_f32_e32 v39, v100, v56
	v_mul_f32_e32 v38, 0xbfb8aa3b, v38
	v_mul_f32_e32 v39, 0xbfb8aa3b, v39
	v_exp_f32_e32 v38, v38
	v_exp_f32_e32 v39, v39
	v_add_f32_e32 v40, v104, v40
	v_add_f32_e32 v36, v104, v36
	v_add_f32_e32 v38, 1.0, v38
	v_add_f32_e32 v39, 1.0, v39
	v_rcp_f32_e32 v38, v38
	v_rcp_f32_e32 v39, v39
	s_waitcnt vmcnt(11)
	v_add_f32_e32 v30, v66, v30
	v_mul_f32_e32 v30, 0xbfb8aa3b, v30
	v_mul_f32_e32 v38, v40, v38
	v_mul_f32_e32 v36, v36, v39
	global_store_dword v[34:35], v38, off offset:128
	global_store_dword v[34:35], v36, off offset:192
	v_add_f32_e32 v34, v101, v65
	v_mul_f32_e32 v34, 0xbfb8aa3b, v34
	v_exp_f32_e32 v36, v34
	v_add_f32_e32 v38, v101, v61
	v_mul_f32_e32 v38, 0xbfb8aa3b, v38
	v_exp_f32_e32 v38, v38
	v_add_f32_e32 v36, 1.0, v36
	v_rcp_f32_e32 v36, v36
	v_or_b32_e32 v34, 0x8c000, v0
	v_mov_b32_e32 v35, v1
	v_add_f32_e32 v38, 1.0, v38
	v_lshl_add_u64 v[34:35], s[10:11], 0, v[34:35]
	v_rcp_f32_e32 v38, v38
	v_lshl_add_u64 v[34:35], v[34:35], 0, s[0:1]
	v_add_f32_e32 v39, v105, v49
	v_mul_f32_e32 v36, v39, v36
	v_lshl_add_u64 v[34:35], v[34:35], 0, v[146:147]
	global_store_dword v[34:35], v36, off
	v_add_f32_e32 v36, v105, v45
	v_mul_f32_e32 v36, v36, v38
	global_store_dword v[34:35], v36, off offset:64
	v_add_f32_e32 v36, v101, v53
	v_mul_f32_e32 v36, 0xbfb8aa3b, v36
	v_exp_f32_e32 v36, v36
	v_add_f32_e32 v38, v101, v57
	v_mul_f32_e32 v38, 0xbfb8aa3b, v38
	v_exp_f32_e32 v38, v38
	v_add_f32_e32 v36, 1.0, v36
	v_rcp_f32_e32 v36, v36
	v_exp_f32_e32 v30, v30
	v_add_f32_e32 v38, 1.0, v38
	v_add_f32_e32 v26, v66, v26
	v_rcp_f32_e32 v38, v38
	v_mul_f32_e32 v26, 0xbfb8aa3b, v26
	v_add_f32_e32 v39, v105, v41
	v_exp_f32_e32 v26, v26
	v_mul_f32_e32 v36, v39, v36
	global_store_dword v[34:35], v36, off offset:128
	v_add_f32_e32 v36, v105, v37
	v_add_f32_e32 v30, 1.0, v30
	v_mul_f32_e32 v36, v36, v38
	v_rcp_f32_e32 v30, v30
	global_store_dword v[34:35], v36, off offset:192
	v_or_b32_e32 v34, 0xc0000, v0
	v_mov_b32_e32 v35, v1
	v_add_f32_e32 v26, 1.0, v26
	v_lshl_add_u64 v[34:35], s[10:11], 0, v[34:35]
	v_rcp_f32_e32 v26, v26
	v_lshl_add_u64 v[34:35], v[34:35], 0, s[0:1]
	s_waitcnt vmcnt(16)
	v_add_f32_e32 v14, v70, v14
	v_mul_f32_e32 v14, v14, v30
	v_lshl_add_u64 v[34:35], v[34:35], 0, v[146:147]
	global_store_dword v[34:35], v14, off
	v_add_f32_e32 v10, v70, v10
	v_add_f32_e32 v14, v66, v18
	v_mul_f32_e32 v10, v10, v26
	v_mul_f32_e32 v14, 0xbfb8aa3b, v14
	global_store_dword v[34:35], v10, off offset:64
	v_add_f32_e32 v10, v66, v22
	v_exp_f32_e32 v14, v14
	v_mul_f32_e32 v10, 0xbfb8aa3b, v10
	v_exp_f32_e32 v10, v10
	v_add_f32_e32 v2, v70, v2
	v_add_f32_e32 v14, 1.0, v14
	v_rcp_f32_e32 v14, v14
	v_add_f32_e32 v10, 1.0, v10
	v_rcp_f32_e32 v10, v10
	v_add_f32_e32 v6, v70, v6
	v_mul_f32_e32 v2, v2, v14
	global_store_dword v[34:35], v2, off offset:192
	v_add_f32_e32 v2, v67, v31
	v_mul_f32_e32 v6, v6, v10
	v_mul_f32_e32 v2, 0xbfb8aa3b, v2
	global_store_dword v[34:35], v6, off offset:128
	v_exp_f32_e32 v2, v2
	v_add_f32_e32 v6, v67, v27
	v_mul_f32_e32 v6, 0xbfb8aa3b, v6
	v_exp_f32_e32 v6, v6
	v_add_f32_e32 v2, 1.0, v2
	v_rcp_f32_e32 v2, v2
	v_or_b32_e32 v30, 0xc4000, v0
	v_mov_b32_e32 v31, v1
	v_add_f32_e32 v6, 1.0, v6
	v_lshl_add_u64 v[30:31], s[10:11], 0, v[30:31]
	v_rcp_f32_e32 v6, v6
	v_lshl_add_u64 v[26:27], v[30:31], 0, s[0:1]
	v_add_f32_e32 v10, v71, v15
	v_mul_f32_e32 v2, v10, v2
	v_lshl_add_u64 v[14:15], v[26:27], 0, v[146:147]
	global_store_dword v[14:15], v2, off
	v_add_f32_e32 v2, v71, v11
	v_mul_f32_e32 v2, v2, v6
	global_store_dword v[14:15], v2, off offset:64
	v_add_f32_e32 v2, v67, v23
	v_mul_f32_e32 v2, 0xbfb8aa3b, v2
	v_exp_f32_e32 v2, v2
	v_add_f32_e32 v6, v67, v19
	v_mul_f32_e32 v6, 0xbfb8aa3b, v6
	v_exp_f32_e32 v6, v6
	v_add_f32_e32 v2, 1.0, v2
	v_rcp_f32_e32 v2, v2
	v_add_f32_e32 v7, v71, v7
	v_add_f32_e32 v6, 1.0, v6
	v_rcp_f32_e32 v6, v6
	v_mul_f32_e32 v2, v7, v2
	global_store_dword v[14:15], v2, off offset:128
	v_add_f32_e32 v2, v71, v3
	v_mul_f32_e32 v2, v2, v6
	global_store_dword v[14:15], v2, off offset:192
	v_add_f32_e32 v2, v68, v32
	v_mul_f32_e32 v2, 0xbfb8aa3b, v2
	v_exp_f32_e32 v6, v2
	v_add_f32_e32 v7, v68, v28
	v_mul_f32_e32 v7, 0xbfb8aa3b, v7
	v_exp_f32_e32 v7, v7
	v_add_f32_e32 v6, 1.0, v6
	v_rcp_f32_e32 v6, v6
	v_or_b32_e32 v2, 0xc8000, v0
	v_mov_b32_e32 v3, v1
	v_add_f32_e32 v7, 1.0, v7
	v_lshl_add_u64 v[2:3], s[10:11], 0, v[2:3]
	v_rcp_f32_e32 v7, v7
	v_lshl_add_u64 v[2:3], v[2:3], 0, s[0:1]
	v_add_f32_e32 v10, v72, v16
	v_mul_f32_e32 v6, v10, v6
	v_lshl_add_u64 v[2:3], v[2:3], 0, v[146:147]
	global_store_dword v[2:3], v6, off
	v_add_f32_e32 v6, v72, v12
	v_mul_f32_e32 v6, v6, v7
	global_store_dword v[2:3], v6, off offset:64
	v_add_f32_e32 v6, v68, v24
	v_mul_f32_e32 v6, 0xbfb8aa3b, v6
	v_exp_f32_e32 v6, v6
	v_add_f32_e32 v7, v68, v20
	v_mul_f32_e32 v7, 0xbfb8aa3b, v7
	v_exp_f32_e32 v7, v7
	v_add_f32_e32 v6, 1.0, v6
	v_rcp_f32_e32 v6, v6
	v_add_f32_e32 v8, v72, v8
	v_add_f32_e32 v7, 1.0, v7
	v_rcp_f32_e32 v7, v7
	v_mul_f32_e32 v6, v8, v6
	global_store_dword v[2:3], v6, off offset:128
	v_add_f32_e32 v4, v72, v4
	v_add_f32_e32 v6, v69, v33
	v_mul_f32_e32 v4, v4, v7
	v_mul_f32_e32 v6, 0xbfb8aa3b, v6
	v_exp_f32_e32 v6, v6
	global_store_dword v[2:3], v4, off offset:192
	v_add_f32_e32 v3, v69, v29
	v_mul_f32_e32 v3, 0xbfb8aa3b, v3
	v_exp_f32_e32 v3, v3
	v_add_f32_e32 v2, 1.0, v6
	v_rcp_f32_e32 v2, v2
	v_or_b32_e32 v0, 0xcc000, v0
	v_add_f32_e32 v3, 1.0, v3
	v_lshl_add_u64 v[0:1], s[10:11], 0, v[0:1]
	v_rcp_f32_e32 v3, v3
	v_lshl_add_u64 v[0:1], v[0:1], 0, s[0:1]
	v_add_f32_e32 v4, v73, v17
	v_mul_f32_e32 v2, v4, v2
	v_lshl_add_u64 v[0:1], v[0:1], 0, v[146:147]
	global_store_dword v[0:1], v2, off
	v_add_f32_e32 v2, v73, v13
	v_mul_f32_e32 v2, v2, v3
	global_store_dword v[0:1], v2, off offset:64
	v_add_f32_e32 v2, v69, v25
	v_mul_f32_e32 v2, 0xbfb8aa3b, v2
	v_exp_f32_e32 v2, v2
	v_add_f32_e32 v3, v69, v21
	v_mul_f32_e32 v3, 0xbfb8aa3b, v3
	v_exp_f32_e32 v3, v3
	v_add_f32_e32 v2, 1.0, v2
	v_rcp_f32_e32 v2, v2
	v_add_f32_e32 v4, v73, v9
	v_add_f32_e32 v3, 1.0, v3
	v_rcp_f32_e32 v3, v3
	v_mul_f32_e32 v2, v4, v2
	global_store_dword v[0:1], v2, off offset:128
	v_add_f32_e32 v2, v73, v5
	v_mul_f32_e32 v2, v2, v3
	global_store_dword v[0:1], v2, off offset:192
	s_endpgm
